# baseline (speedup 1.0000x reference)
_Z12scan2_kernelPKDF16_S0_S0_S0_S0_PKfS2_S2_S2_PDF16_PfS4_:
	s_and_b32 s3, s2, 7
	s_lshr_b32 s2, s2, 3
	s_lshl_b32 s3, s3, 5
	s_or_b32 s2, s2, s3
	s_load_dwordx8 s[4:11], s[0:1], 0x0
	s_load_dwordx8 s[12:19], s[0:1], 0x20
	s_load_dwordx4 s[20:23], s[0:1], 0x40
	s_load_dwordx2 s[24:25], s[0:1], 0x50
	s_and_b32 s26, s2, 3
	s_bfe_u32 s27, s2, 0x50002
	s_lshr_b32 s28, s2, 7
	s_lshl_b32 s29, s26, 3
	v_lshrrev_b32_e32 v1, 6, v0
	v_and_b32_e32 v2, 15, v0
	v_bfe_u32 v3, v0, 4, 2
	v_and_b32_e32 v42, 63, v0
	v_readfirstlane_b32 s40, v1
	v_mov_b32_e32 v43, v0
	v_lshrrev_b32_e32 v14, 4, v43
	v_and_b32_e32 v15, 15, v43
	v_and_b32_e32 v188, 15, v14
	v_xor_b32_e32 v15, v15, v188
	v_lshlrev_b32_e32 v15, 4, v15
	v_lshl_or_b32 v4, v14, 13, v15
	v_lshl_or_b32 v6, v14, 8, v15
	v_lshrrev_b32_e32 v14, 3, v43
	v_and_b32_e32 v15, 7, v43
	v_and_b32_e32 v188, 7, v14
	v_xor_b32_e32 v15, v15, v188
	v_lshlrev_b32_e32 v15, 4, v15
	v_lshl_or_b32 v8, v14, 12, v15
	v_lshlrev_b32_e32 v40, 4, v43
	v_add_u32_e32 v32, 0xc800, v40
	v_add_u32_e32 v34, 0x19000, v40
	v_add_u32_e32 v43, 0x200, v0
	v_lshrrev_b32_e32 v14, 4, v43
	v_and_b32_e32 v15, 15, v43
	v_and_b32_e32 v188, 15, v14
	v_xor_b32_e32 v15, v15, v188
	v_lshlrev_b32_e32 v15, 4, v15
	v_lshl_or_b32 v5, v14, 13, v15
	v_lshl_or_b32 v7, v14, 8, v15
	v_lshrrev_b32_e32 v14, 3, v43
	v_and_b32_e32 v15, 7, v43
	v_and_b32_e32 v188, 7, v14
	v_xor_b32_e32 v15, v15, v188
	v_lshlrev_b32_e32 v15, 4, v15
	v_lshl_or_b32 v9, v14, 12, v15
	v_lshlrev_b32_e32 v41, 4, v43
	v_add_u32_e32 v33, 0xc800, v41
	v_add_u32_e32 v35, 0x19000, v41
	s_sub_u32 s45, 11, s40
	s_cmp_lt_u32 s40, 4
	s_cselect_b32 s41, s40, s45
	s_lshr_b32 s42, s41, 1
	s_lshl_b32 s43, s40, 10
	s_lshl_b32 s44, s40, 8
	s_and_b32 s45, s40, 1
	s_lshl_b32 s45, s45, 8
	v_lshl_add_u32 v10, v42, 2, s45
	s_lshl_b32 s45, s41, 4
	v_add_u32_e32 v14, s45, v2
	v_add_u32_e32 v15, 0, v3
	v_xor_b32_e32 v15, v15, v2
	v_lshlrev_b32_e32 v15, 4, v15
	v_lshl_or_b32 v16, v2, 8, v15
	v_add_u32_e32 v20, 0xc800, v16
	v_add_u32_e32 v212, 0x19000, v16
	v_add_u32_e32 v15, 4, v3
	v_xor_b32_e32 v15, v15, v2
	v_lshlrev_b32_e32 v15, 4, v15
	v_lshl_or_b32 v17, v2, 8, v15
	v_add_u32_e32 v21, 0xc800, v17
	v_add_u32_e32 v213, 0x19000, v17
	v_add_u32_e32 v15, 8, v3
	v_xor_b32_e32 v15, v15, v2
	v_lshlrev_b32_e32 v15, 4, v15
	v_lshl_or_b32 v18, v2, 8, v15
	v_add_u32_e32 v22, 0xc800, v18
	v_add_u32_e32 v214, 0x19000, v18
	v_add_u32_e32 v15, 12, v3
	v_xor_b32_e32 v15, v15, v2
	v_lshlrev_b32_e32 v15, 4, v15
	v_lshl_or_b32 v19, v2, 8, v15
	v_add_u32_e32 v23, 0xc800, v19
	v_add_u32_e32 v215, 0x19000, v19
	v_lshrrev_b32_e32 v188, 1, v3
	v_and_b32_e32 v189, 7, v14
	v_and_b32_e32 v190, 1, v3
	v_lshlrev_b32_e32 v190, 3, v190
	v_lshl_or_b32 v190, v14, 7, v190
	v_add_u32_e32 v15, 0, v188
	v_xor_b32_e32 v15, v15, v189
	v_lshl_add_u32 v24, v15, 4, v190
	v_add_u32_e32 v28, 0xc800, v24
	v_add_u32_e32 v216, 0x19000, v24
	v_add_u32_e32 v15, 2, v188
	v_xor_b32_e32 v15, v15, v189
	v_lshl_add_u32 v25, v15, 4, v190
	v_add_u32_e32 v29, 0xc800, v25
	v_add_u32_e32 v217, 0x19000, v25
	v_add_u32_e32 v15, 4, v188
	v_xor_b32_e32 v15, v15, v189
	v_lshl_add_u32 v26, v15, 4, v190
	v_add_u32_e32 v30, 0xc800, v26
	v_add_u32_e32 v218, 0x19000, v26
	v_add_u32_e32 v15, 6, v188
	v_xor_b32_e32 v15, v15, v189
	v_lshl_add_u32 v27, v15, 4, v190
	v_add_u32_e32 v31, 0xc800, v27
	v_add_u32_e32 v219, 0x19000, v27
	v_lshlrev_b32_e32 v36, 2, v14
	v_add_u32_e32 v37, 0xc800, v36
	v_add_u32_e32 v220, 0x19000, v36
	v_lshlrev_b32_e32 v38, 5, v3
	v_add_u32_e32 v39, 0xc800, v38
	v_add_u32_e32 v221, 0x19000, v38
	s_and_b32 s45, s41, 1
	s_lshl_b32 s45, s45, 4
	v_add_u32_e32 v43, s45, v2
	v_lshlrev_b32_e32 v189, 3, v3
	v_sub_u32_e32 v43, v43, v189
	v_cmp_le_i32_e64 s[52:53], 0, v43
	v_cmp_le_i32_e64 s[54:55], 1, v43
	v_cmp_le_i32_e64 s[56:57], 2, v43
	v_cmp_le_i32_e64 s[58:59], 3, v43
	v_cmp_le_i32_e64 s[60:61], 4, v43
	v_cmp_le_i32_e64 s[62:63], 5, v43
	v_cmp_le_i32_e64 s[64:65], 6, v43
	v_cmp_le_i32_e64 s[66:67], 7, v43
	v_cmp_eq_u32_e32 vcc, 0, v43
	s_nop 1
	v_cndmask_b32_e64 v188, 0, 1.0, vcc
	v_cmp_eq_u32_e32 vcc, 1, v43
	s_nop 1
	v_cndmask_b32_e64 v189, 0, 1.0, vcc
	v_cmp_eq_u32_e32 vcc, 2, v43
	s_nop 1
	v_cndmask_b32_e64 v190, 0, 1.0, vcc
	v_cmp_eq_u32_e32 vcc, 3, v43
	s_nop 1
	v_cndmask_b32_e64 v191, 0, 1.0, vcc
	v_cmp_eq_u32_e32 vcc, 4, v43
	s_nop 1
	v_cndmask_b32_e64 v192, 0, 1.0, vcc
	v_cmp_eq_u32_e32 vcc, 5, v43
	s_nop 1
	v_cndmask_b32_e64 v193, 0, 1.0, vcc
	v_cmp_eq_u32_e32 vcc, 6, v43
	s_nop 1
	v_cndmask_b32_e64 v194, 0, 1.0, vcc
	v_cmp_eq_u32_e32 vcc, 7, v43
	s_nop 1
	v_cndmask_b32_e64 v195, 0, 1.0, vcc
	v_cvt_pk_f16_f32 v92, v188, v189
	v_cvt_pk_f16_f32 v93, v190, v191
	v_cvt_pk_f16_f32 v94, v192, v193
	v_cvt_pk_f16_f32 v95, v194, v195
	v_mov_b32_e32 v13, 0
	s_waitcnt lgkmcnt(0)
	s_lshl_b32 s45, s28, 12
	s_lshl_b32 s48, s27, 7
	s_add_u32 s45, s45, s48
	s_lshl_b32 s48, s45, 9
	s_add_u32 s48, s4, s48
	s_addc_u32 s49, s5, 0
	v_lshlrev_b32_e32 v188, 9, v14
	v_lshl_add_u32 v188, v3, 4, v188
	global_load_dwordx4 v[44:47], v188, s[48:49] offset:256
	global_load_dwordx4 v[48:51], v188, s[48:49] offset:320
	global_load_dwordx4 v[52:55], v188, s[48:49] offset:384
	global_load_dwordx4 v[56:59], v188, s[48:49] offset:448
	s_lshl_b32 s48, s28, 5
	s_add_u32 s48, s48, s27
	s_lshl_b32 s48, s48, 15
	s_add_u32 s48, s10, s48
	s_addc_u32 s49, s11, 0
	v_lshlrev_b32_e32 v188, 8, v14
	v_lshl_add_u32 v188, v3, 4, v188
	global_load_dwordx4 v[144:147], v188, s[48:49] offset:0
	global_load_dwordx4 v[148:151], v188, s[48:49] offset:64
	global_load_dwordx4 v[152:155], v188, s[48:49] offset:128
	global_load_dwordx4 v[156:159], v188, s[48:49] offset:192
	v_and_b32_e32 v188, 7, v42
	v_add_u32_e32 v188, s29, v188
	v_lshlrev_b32_e32 v188, 2, v188
	global_load_dword v11, v188, s[20:21]
	global_load_dword v12, v188, s[18:19]
	s_mul_i32 s48, s28, 0x900
	s_lshl_b32 s49, s29, 6
	s_add_u32 s48, s48, s49
	s_lshl_b32 s48, s48, 13
	s_lshl_b32 s49, s27, 8
	s_add_u32 s48, s48, s49
	s_add_u32 s30, s6, s48
	s_addc_u32 s31, s7, 0
	s_lshl_b32 s48, s28, 5
	s_add_u32 s48, s48, s27
	s_lshl_b32 s48, s48, 5
	s_add_u32 s48, s48, s29
	s_lshl_b32 s48, s48, 14
	s_add_u32 s32, s12, s48
	s_addc_u32 s33, s13, 0
	s_lshl_b32 s48, s45, 12
	s_lshl_b32 s49, s29, 7
	s_add_u32 s48, s48, s49
	s_add_u32 s34, s8, s48
	s_addc_u32 s35, s9, 0
	s_add_u32 s38, s22, s48
	s_addc_u32 s39, s23, 0
	s_lshl_b32 s48, s28, 5
	s_add_u32 s48, s48, s29
	s_lshl_b32 s48, s48, 14
	s_lshl_b32 s49, s27, 9
	s_add_u32 s48, s48, s49
	s_lshr_b32 s49, s40, 1
	s_cmp_eq_u32 s49, 1
	s_cselect_b32 s50, s14, s16
	s_cselect_b32 s51, s15, s17
	s_add_u32 s36, s50, s48
	s_addc_u32 s37, s51, 0
	s_lshl_b32 s48, s45, 2
	s_add_u32 s24, s24, s48
	s_addc_u32 s25, s25, 0
	v_lshlrev_b32_e32 v15, 2, v14
	s_mov_b32 s51, 0xbfb8aa3b
	s_add_u32 m0, s43, 0x0
	s_nop 0
	global_load_lds_dwordx4 v4, s[30:31]
	s_add_u32 m0, s43, 0x4000
	s_nop 0
	global_load_lds_dwordx4 v6, s[32:33]
	s_add_u32 m0, s43, 0x8000
	s_nop 0
	global_load_lds_dwordx4 v8, s[34:35]
	s_add_u32 m0, s43, 0x2000
	s_nop 0
	global_load_lds_dwordx4 v5, s[30:31]
	s_add_u32 m0, s43, 0x6000
	s_nop 0
	global_load_lds_dwordx4 v7, s[32:33]
	s_add_u32 m0, s43, 0xa000
	s_nop 0
	global_load_lds_dwordx4 v9, s[34:35]
	s_add_u32 m0, s44, 0xc000
	s_nop 0
	global_load_lds_dword v10, s[36:37]
	s_add_u32 s30, s30, 0x80000
	s_addc_u32 s31, s31, 0
	s_add_u32 s32, s32, 0x4000
	s_addc_u32 s33, s33, 0
	s_add_u32 s34, s34, 0x80
	s_addc_u32 s35, s35, 0
	s_add_u32 s36, s36, 0x4000
	s_addc_u32 s37, s37, 0
	s_add_u32 m0, s43, 0xc800
	s_nop 0
	global_load_lds_dwordx4 v4, s[30:31]
	s_add_u32 m0, s43, 0x10800
	s_nop 0
	global_load_lds_dwordx4 v6, s[32:33]
	s_add_u32 m0, s43, 0x14800
	s_nop 0
	global_load_lds_dwordx4 v8, s[34:35]
	s_add_u32 m0, s43, 0xe800
	s_nop 0
	global_load_lds_dwordx4 v5, s[30:31]
	s_add_u32 m0, s43, 0x12800
	s_nop 0
	global_load_lds_dwordx4 v7, s[32:33]
	s_add_u32 m0, s43, 0x16800
	s_nop 0
	global_load_lds_dwordx4 v9, s[34:35]
	s_add_u32 m0, s44, 0x18800
	s_nop 0
	global_load_lds_dword v10, s[36:37]
	s_add_u32 s30, s30, 0x80000
	s_addc_u32 s31, s31, 0
	s_add_u32 s32, s32, 0x4000
	s_addc_u32 s33, s33, 0
	s_add_u32 s34, s34, 0x80
	s_addc_u32 s35, s35, 0
	s_add_u32 s36, s36, 0x4000
	s_addc_u32 s37, s37, 0
	s_waitcnt vmcnt(19)
	v_cvt_f32_f16_e32 v60, v144
	v_cvt_f32_f16_sdwa v61, v144 dst_sel:DWORD dst_unused:UNUSED_PAD src0_sel:WORD_1
	v_cvt_f32_f16_e32 v62, v145
	v_cvt_f32_f16_sdwa v63, v145 dst_sel:DWORD dst_unused:UNUSED_PAD src0_sel:WORD_1
	v_cvt_f32_f16_e32 v64, v146
	v_cvt_f32_f16_sdwa v65, v146 dst_sel:DWORD dst_unused:UNUSED_PAD src0_sel:WORD_1
	v_cvt_f32_f16_e32 v66, v147
	v_cvt_f32_f16_sdwa v67, v147 dst_sel:DWORD dst_unused:UNUSED_PAD src0_sel:WORD_1
	s_waitcnt vmcnt(18)
	v_cvt_f32_f16_e32 v68, v148
	v_cvt_f32_f16_sdwa v69, v148 dst_sel:DWORD dst_unused:UNUSED_PAD src0_sel:WORD_1
	v_cvt_f32_f16_e32 v70, v149
	v_cvt_f32_f16_sdwa v71, v149 dst_sel:DWORD dst_unused:UNUSED_PAD src0_sel:WORD_1
	v_cvt_f32_f16_e32 v72, v150
	v_cvt_f32_f16_sdwa v73, v150 dst_sel:DWORD dst_unused:UNUSED_PAD src0_sel:WORD_1
	v_cvt_f32_f16_e32 v74, v151
	v_cvt_f32_f16_sdwa v75, v151 dst_sel:DWORD dst_unused:UNUSED_PAD src0_sel:WORD_1
	s_waitcnt vmcnt(17)
	v_cvt_f32_f16_e32 v76, v152
	v_cvt_f32_f16_sdwa v77, v152 dst_sel:DWORD dst_unused:UNUSED_PAD src0_sel:WORD_1
	v_cvt_f32_f16_e32 v78, v153
	v_cvt_f32_f16_sdwa v79, v153 dst_sel:DWORD dst_unused:UNUSED_PAD src0_sel:WORD_1
	v_cvt_f32_f16_e32 v80, v154
	v_cvt_f32_f16_sdwa v81, v154 dst_sel:DWORD dst_unused:UNUSED_PAD src0_sel:WORD_1
	v_cvt_f32_f16_e32 v82, v155
	v_cvt_f32_f16_sdwa v83, v155 dst_sel:DWORD dst_unused:UNUSED_PAD src0_sel:WORD_1
	s_waitcnt vmcnt(16)
	v_cvt_f32_f16_e32 v84, v156
	v_cvt_f32_f16_sdwa v85, v156 dst_sel:DWORD dst_unused:UNUSED_PAD src0_sel:WORD_1
	v_cvt_f32_f16_e32 v86, v157
	v_cvt_f32_f16_sdwa v87, v157 dst_sel:DWORD dst_unused:UNUSED_PAD src0_sel:WORD_1
	v_cvt_f32_f16_e32 v88, v158
	v_cvt_f32_f16_sdwa v89, v158 dst_sel:DWORD dst_unused:UNUSED_PAD src0_sel:WORD_1
	v_cvt_f32_f16_e32 v90, v159
	v_cvt_f32_f16_sdwa v91, v159 dst_sel:DWORD dst_unused:UNUSED_PAD src0_sel:WORD_1
	s_waitcnt vmcnt(14)
	v_mul_f32_e32 v12, 0x3d800000, v12
	s_add_u32 m0, s43, 0x19000
	s_nop 0
	global_load_lds_dwordx4 v4, s[30:31]
	s_add_u32 m0, s43, 0x1d000
	s_nop 0
	global_load_lds_dwordx4 v6, s[32:33]
	s_add_u32 m0, s43, 0x21000
	s_nop 0
	global_load_lds_dwordx4 v8, s[34:35]
	s_add_u32 m0, s43, 0x1b000
	s_nop 0
	global_load_lds_dwordx4 v5, s[30:31]
	s_add_u32 m0, s43, 0x1f000
	s_nop 0
	global_load_lds_dwordx4 v7, s[32:33]
	s_add_u32 m0, s43, 0x23000
	s_nop 0
	global_load_lds_dwordx4 v9, s[34:35]
	s_add_u32 m0, s44, 0x25000
	s_nop 0
	global_load_lds_dword v10, s[36:37]
	s_add_u32 s30, s30, 0x80000
	s_addc_u32 s31, s31, 0
	s_add_u32 s32, s32, 0x4000
	s_addc_u32 s33, s33, 0
	s_add_u32 s34, s34, 0x80
	s_addc_u32 s35, s35, 0
	s_add_u32 s36, s36, 0x4000
	s_addc_u32 s37, s37, 0
	s_waitcnt vmcnt(14)
	s_waitcnt lgkmcnt(0)
	s_barrier
	v_mov_b32_e32 v112, 0
	v_mov_b32_e32 v113, 0
	v_mov_b32_e32 v114, 0
	v_mov_b32_e32 v115, 0
	v_mov_b32_e32 v116, 0
	v_mov_b32_e32 v117, 0
	v_mov_b32_e32 v118, 0
	v_mov_b32_e32 v119, 0
	v_mov_b32_e32 v120, 0
	v_mov_b32_e32 v121, 0
	v_mov_b32_e32 v122, 0
	v_mov_b32_e32 v123, 0
	v_mov_b32_e32 v124, 0
	v_mov_b32_e32 v125, 0
	v_mov_b32_e32 v126, 0
	v_mov_b32_e32 v127, 0
	ds_read_b128 v[144:147], v16 offset:16384
	ds_read_b128 v[148:151], v16 offset:20480
	ds_read_b128 v[152:155], v16 offset:24576
	ds_read_b128 v[156:159], v16 offset:28672
	ds_read_b32 v189, v36 offset:49152
	ds_read_b128 v[160:163], v17 offset:16384
	ds_read_b128 v[164:167], v17 offset:20480
	ds_read_b128 v[168:171], v17 offset:24576
	ds_read_b128 v[172:175], v17 offset:28672
	s_waitcnt lgkmcnt(4)
	v_mfma_f32_16x16x32_f16 v[96:99], v[144:147], v[44:47], 0
	v_mfma_f32_16x16x32_f16 v[100:103], v[148:151], v[44:47], 0
	v_mfma_f32_16x16x32_f16 v[104:107], v[152:155], v[44:47], 0
	v_mfma_f32_16x16x32_f16 v[108:111], v[156:159], v[44:47], 0
	ds_read_b128 v[144:147], v18 offset:16384
	ds_read_b128 v[148:151], v18 offset:20480
	ds_read_b128 v[152:155], v18 offset:24576
	ds_read_b128 v[156:159], v18 offset:28672
	s_waitcnt lgkmcnt(4)
	v_mfma_f32_16x16x32_f16 v[96:99], v[160:163], v[48:51], v[96:99]
	v_mfma_f32_16x16x32_f16 v[100:103], v[164:167], v[48:51], v[100:103]
	v_mfma_f32_16x16x32_f16 v[104:107], v[168:171], v[48:51], v[104:107]
	v_mfma_f32_16x16x32_f16 v[108:111], v[172:175], v[48:51], v[108:111]
	ds_read_b128 v[160:163], v19 offset:16384
	ds_read_b128 v[164:167], v19 offset:20480
	ds_read_b128 v[168:171], v19 offset:24576
	ds_read_b128 v[172:175], v19 offset:28672
	s_waitcnt lgkmcnt(4)
	v_mfma_f32_16x16x32_f16 v[96:99], v[144:147], v[52:55], v[96:99]
	v_mfma_f32_16x16x32_f16 v[100:103], v[148:151], v[52:55], v[100:103]
	v_mfma_f32_16x16x32_f16 v[104:107], v[152:155], v[52:55], v[104:107]
	v_mfma_f32_16x16x32_f16 v[108:111], v[156:159], v[52:55], v[108:111]
	s_waitcnt lgkmcnt(0)
	v_mfma_f32_16x16x32_f16 v[96:99], v[160:163], v[56:59], v[96:99]
	v_mfma_f32_16x16x32_f16 v[100:103], v[164:167], v[56:59], v[100:103]
	v_mfma_f32_16x16x32_f16 v[104:107], v[168:171], v[56:59], v[104:107]
	v_mfma_f32_16x16x32_f16 v[108:111], v[172:175], v[56:59], v[108:111]
	v_mul_f32_e32 v189, 0x3fb8aa3b, v189
	s_cmp_lt_u32 s42, 0
	s_cbranch_scc1 .Lmy_s2_kend1
	s_cmp_eq_u32 s42, 0
	s_cbranch_scc1 .Lmy_s2_diag2
	ds_read_b128 v[176:179], v38 offset:49664
	ds_read_b128 v[180:183], v38 offset:49680
	ds_read_b32 v188, v38 offset:49152
	ds_read_b128 v[160:163], v16 offset:0
	ds_read_b128 v[164:167], v16 offset:4096
	ds_read_b128 v[168:171], v16 offset:8192
	ds_read_b128 v[172:175], v16 offset:12288
	s_waitcnt lgkmcnt(4)
	v_fma_f32 v188, v188, s51, v189
	v_exp_f32_e32 v188, v188
	s_nop 0
	v_mul_f32_e32 v176, v188, v176
	v_mul_f32_e32 v177, v188, v177
	v_mul_f32_e32 v178, v188, v178
	v_mul_f32_e32 v179, v188, v179
	v_mul_f32_e32 v180, v188, v180
	v_mul_f32_e32 v181, v188, v181
	v_mul_f32_e32 v182, v188, v182
	v_mul_f32_e32 v183, v188, v183
	v_mul_f32_e32 v176, v60, v176
	v_mul_f32_e32 v177, v61, v177
	v_mul_f32_e32 v178, v62, v178
	v_mul_f32_e32 v179, v63, v179
	v_mul_f32_e32 v180, v64, v180
	v_mul_f32_e32 v181, v65, v181
	v_mul_f32_e32 v182, v66, v182
	v_mul_f32_e32 v183, v67, v183
	v_cvt_pk_f16_f32 v184, v176, v177
	v_cvt_pk_f16_f32 v185, v178, v179
	v_cvt_pk_f16_f32 v186, v180, v181
	v_cvt_pk_f16_f32 v187, v182, v183
	s_waitcnt lgkmcnt(0)
	s_nop 0
	v_mfma_f32_16x16x32_f16 v[112:115], v[160:163], v[184:187], v[112:115]
	v_mfma_f32_16x16x32_f16 v[116:119], v[164:167], v[184:187], v[116:119]
	v_mfma_f32_16x16x32_f16 v[120:123], v[168:171], v[184:187], v[120:123]
	v_mfma_f32_16x16x32_f16 v[124:127], v[172:175], v[184:187], v[124:127]
	s_branch .Lmy_s2_knext3
.Lmy_s2_diag2:
	ds_read_b128 v[176:179], v38 offset:49664
	ds_read_b128 v[180:183], v38 offset:49680
	ds_read_b32 v188, v38 offset:49152
	ds_read_b128 v[160:163], v16 offset:0
	ds_read_b128 v[164:167], v16 offset:4096
	ds_read_b128 v[168:171], v16 offset:8192
	ds_read_b128 v[172:175], v16 offset:12288
	s_waitcnt lgkmcnt(4)
	v_fma_f32 v188, v188, s51, v189
	v_exp_f32_e32 v188, v188
	s_nop 0
	v_mul_f32_e32 v176, v188, v176
	v_mul_f32_e32 v177, v188, v177
	v_mul_f32_e32 v178, v188, v178
	v_mul_f32_e32 v179, v188, v179
	v_mul_f32_e32 v180, v188, v180
	v_mul_f32_e32 v181, v188, v181
	v_mul_f32_e32 v182, v188, v182
	v_mul_f32_e32 v183, v188, v183
	v_mul_f32_e32 v176, v60, v176
	v_mul_f32_e32 v177, v61, v177
	v_mul_f32_e32 v178, v62, v178
	v_mul_f32_e32 v179, v63, v179
	v_mul_f32_e32 v180, v64, v180
	v_mul_f32_e32 v181, v65, v181
	v_mul_f32_e32 v182, v66, v182
	v_mul_f32_e32 v183, v67, v183
	v_cndmask_b32_e64 v176, 0, v176, s[52:53]
	v_cndmask_b32_e64 v177, 0, v177, s[54:55]
	v_cndmask_b32_e64 v178, 0, v178, s[56:57]
	v_cndmask_b32_e64 v179, 0, v179, s[58:59]
	v_cndmask_b32_e64 v180, 0, v180, s[60:61]
	v_cndmask_b32_e64 v181, 0, v181, s[62:63]
	v_cndmask_b32_e64 v182, 0, v182, s[64:65]
	v_cndmask_b32_e64 v183, 0, v183, s[66:67]
	v_cvt_pk_f16_f32 v184, v176, v177
	v_cvt_pk_f16_f32 v185, v178, v179
	v_cvt_pk_f16_f32 v186, v180, v181
	v_cvt_pk_f16_f32 v187, v182, v183
	s_waitcnt lgkmcnt(0)
	s_nop 0
	v_mfma_f32_16x16x32_f16 v[112:115], v[160:163], v[184:187], v[112:115]
	v_mfma_f32_16x16x32_f16 v[116:119], v[164:167], v[184:187], v[116:119]
	v_mfma_f32_16x16x32_f16 v[120:123], v[168:171], v[184:187], v[120:123]
	v_mfma_f32_16x16x32_f16 v[124:127], v[172:175], v[184:187], v[124:127]
	v_mfma_f32_16x16x32_f16 v[128:131], v[160:163], v[92:95], 0
	v_mfma_f32_16x16x32_f16 v[132:135], v[164:167], v[92:95], 0
	v_mfma_f32_16x16x32_f16 v[136:139], v[168:171], v[92:95], 0
	v_mfma_f32_16x16x32_f16 v[140:143], v[172:175], v[92:95], 0
	s_branch .Lmy_s2_kend1
.Lmy_s2_knext3:
	s_cmp_lt_u32 s42, 1
	s_cbranch_scc1 .Lmy_s2_kend1
	s_cmp_eq_u32 s42, 1
	s_cbranch_scc1 .Lmy_s2_diag4
	ds_read_b128 v[176:179], v38 offset:49792
	ds_read_b128 v[180:183], v38 offset:49808
	ds_read_b32 v188, v38 offset:49280
	ds_read_b128 v[160:163], v17 offset:0
	ds_read_b128 v[164:167], v17 offset:4096
	ds_read_b128 v[168:171], v17 offset:8192
	ds_read_b128 v[172:175], v17 offset:12288
	s_waitcnt lgkmcnt(4)
	v_fma_f32 v188, v188, s51, v189
	v_exp_f32_e32 v188, v188
	s_nop 0
	v_mul_f32_e32 v176, v188, v176
	v_mul_f32_e32 v177, v188, v177
	v_mul_f32_e32 v178, v188, v178
	v_mul_f32_e32 v179, v188, v179
	v_mul_f32_e32 v180, v188, v180
	v_mul_f32_e32 v181, v188, v181
	v_mul_f32_e32 v182, v188, v182
	v_mul_f32_e32 v183, v188, v183
	v_mul_f32_e32 v176, v68, v176
	v_mul_f32_e32 v177, v69, v177
	v_mul_f32_e32 v178, v70, v178
	v_mul_f32_e32 v179, v71, v179
	v_mul_f32_e32 v180, v72, v180
	v_mul_f32_e32 v181, v73, v181
	v_mul_f32_e32 v182, v74, v182
	v_mul_f32_e32 v183, v75, v183
	v_cvt_pk_f16_f32 v184, v176, v177
	v_cvt_pk_f16_f32 v185, v178, v179
	v_cvt_pk_f16_f32 v186, v180, v181
	v_cvt_pk_f16_f32 v187, v182, v183
	s_waitcnt lgkmcnt(0)
	s_nop 0
	v_mfma_f32_16x16x32_f16 v[112:115], v[160:163], v[184:187], v[112:115]
	v_mfma_f32_16x16x32_f16 v[116:119], v[164:167], v[184:187], v[116:119]
	v_mfma_f32_16x16x32_f16 v[120:123], v[168:171], v[184:187], v[120:123]
	v_mfma_f32_16x16x32_f16 v[124:127], v[172:175], v[184:187], v[124:127]
	s_branch .Lmy_s2_knext5
.Lmy_s2_diag4:
	ds_read_b128 v[176:179], v38 offset:49792
	ds_read_b128 v[180:183], v38 offset:49808
	ds_read_b32 v188, v38 offset:49280
	ds_read_b128 v[160:163], v17 offset:0
	ds_read_b128 v[164:167], v17 offset:4096
	ds_read_b128 v[168:171], v17 offset:8192
	ds_read_b128 v[172:175], v17 offset:12288
	s_waitcnt lgkmcnt(4)
	v_fma_f32 v188, v188, s51, v189
	v_exp_f32_e32 v188, v188
	s_nop 0
	v_mul_f32_e32 v176, v188, v176
	v_mul_f32_e32 v177, v188, v177
	v_mul_f32_e32 v178, v188, v178
	v_mul_f32_e32 v179, v188, v179
	v_mul_f32_e32 v180, v188, v180
	v_mul_f32_e32 v181, v188, v181
	v_mul_f32_e32 v182, v188, v182
	v_mul_f32_e32 v183, v188, v183
	v_mul_f32_e32 v176, v68, v176
	v_mul_f32_e32 v177, v69, v177
	v_mul_f32_e32 v178, v70, v178
	v_mul_f32_e32 v179, v71, v179
	v_mul_f32_e32 v180, v72, v180
	v_mul_f32_e32 v181, v73, v181
	v_mul_f32_e32 v182, v74, v182
	v_mul_f32_e32 v183, v75, v183
	v_cndmask_b32_e64 v176, 0, v176, s[52:53]
	v_cndmask_b32_e64 v177, 0, v177, s[54:55]
	v_cndmask_b32_e64 v178, 0, v178, s[56:57]
	v_cndmask_b32_e64 v179, 0, v179, s[58:59]
	v_cndmask_b32_e64 v180, 0, v180, s[60:61]
	v_cndmask_b32_e64 v181, 0, v181, s[62:63]
	v_cndmask_b32_e64 v182, 0, v182, s[64:65]
	v_cndmask_b32_e64 v183, 0, v183, s[66:67]
	v_cvt_pk_f16_f32 v184, v176, v177
	v_cvt_pk_f16_f32 v185, v178, v179
	v_cvt_pk_f16_f32 v186, v180, v181
	v_cvt_pk_f16_f32 v187, v182, v183
	s_waitcnt lgkmcnt(0)
	s_nop 0
	v_mfma_f32_16x16x32_f16 v[112:115], v[160:163], v[184:187], v[112:115]
	v_mfma_f32_16x16x32_f16 v[116:119], v[164:167], v[184:187], v[116:119]
	v_mfma_f32_16x16x32_f16 v[120:123], v[168:171], v[184:187], v[120:123]
	v_mfma_f32_16x16x32_f16 v[124:127], v[172:175], v[184:187], v[124:127]
	v_mfma_f32_16x16x32_f16 v[128:131], v[160:163], v[92:95], 0
	v_mfma_f32_16x16x32_f16 v[132:135], v[164:167], v[92:95], 0
	v_mfma_f32_16x16x32_f16 v[136:139], v[168:171], v[92:95], 0
	v_mfma_f32_16x16x32_f16 v[140:143], v[172:175], v[92:95], 0
	s_branch .Lmy_s2_kend1
.Lmy_s2_knext5:
	s_cmp_lt_u32 s42, 2
	s_cbranch_scc1 .Lmy_s2_kend1
	s_cmp_eq_u32 s42, 2
	s_cbranch_scc1 .Lmy_s2_diag6
	ds_read_b128 v[176:179], v38 offset:49920
	ds_read_b128 v[180:183], v38 offset:49936
	ds_read_b32 v188, v38 offset:49408
	ds_read_b128 v[160:163], v18 offset:0
	ds_read_b128 v[164:167], v18 offset:4096
	ds_read_b128 v[168:171], v18 offset:8192
	ds_read_b128 v[172:175], v18 offset:12288
	s_waitcnt lgkmcnt(4)
	v_fma_f32 v188, v188, s51, v189
	v_exp_f32_e32 v188, v188
	s_nop 0
	v_mul_f32_e32 v176, v188, v176
	v_mul_f32_e32 v177, v188, v177
	v_mul_f32_e32 v178, v188, v178
	v_mul_f32_e32 v179, v188, v179
	v_mul_f32_e32 v180, v188, v180
	v_mul_f32_e32 v181, v188, v181
	v_mul_f32_e32 v182, v188, v182
	v_mul_f32_e32 v183, v188, v183
	v_mul_f32_e32 v176, v76, v176
	v_mul_f32_e32 v177, v77, v177
	v_mul_f32_e32 v178, v78, v178
	v_mul_f32_e32 v179, v79, v179
	v_mul_f32_e32 v180, v80, v180
	v_mul_f32_e32 v181, v81, v181
	v_mul_f32_e32 v182, v82, v182
	v_mul_f32_e32 v183, v83, v183
	v_cvt_pk_f16_f32 v184, v176, v177
	v_cvt_pk_f16_f32 v185, v178, v179
	v_cvt_pk_f16_f32 v186, v180, v181
	v_cvt_pk_f16_f32 v187, v182, v183
	s_waitcnt lgkmcnt(0)
	s_nop 0
	v_mfma_f32_16x16x32_f16 v[112:115], v[160:163], v[184:187], v[112:115]
	v_mfma_f32_16x16x32_f16 v[116:119], v[164:167], v[184:187], v[116:119]
	v_mfma_f32_16x16x32_f16 v[120:123], v[168:171], v[184:187], v[120:123]
	v_mfma_f32_16x16x32_f16 v[124:127], v[172:175], v[184:187], v[124:127]
	s_branch .Lmy_s2_knext7
.Lmy_s2_diag6:
	ds_read_b128 v[176:179], v38 offset:49920
	ds_read_b128 v[180:183], v38 offset:49936
	ds_read_b32 v188, v38 offset:49408
	ds_read_b128 v[160:163], v18 offset:0
	ds_read_b128 v[164:167], v18 offset:4096
	ds_read_b128 v[168:171], v18 offset:8192
	ds_read_b128 v[172:175], v18 offset:12288
	s_waitcnt lgkmcnt(4)
	v_fma_f32 v188, v188, s51, v189
	v_exp_f32_e32 v188, v188
	s_nop 0
	v_mul_f32_e32 v176, v188, v176
	v_mul_f32_e32 v177, v188, v177
	v_mul_f32_e32 v178, v188, v178
	v_mul_f32_e32 v179, v188, v179
	v_mul_f32_e32 v180, v188, v180
	v_mul_f32_e32 v181, v188, v181
	v_mul_f32_e32 v182, v188, v182
	v_mul_f32_e32 v183, v188, v183
	v_mul_f32_e32 v176, v76, v176
	v_mul_f32_e32 v177, v77, v177
	v_mul_f32_e32 v178, v78, v178
	v_mul_f32_e32 v179, v79, v179
	v_mul_f32_e32 v180, v80, v180
	v_mul_f32_e32 v181, v81, v181
	v_mul_f32_e32 v182, v82, v182
	v_mul_f32_e32 v183, v83, v183
	v_cndmask_b32_e64 v176, 0, v176, s[52:53]
	v_cndmask_b32_e64 v177, 0, v177, s[54:55]
	v_cndmask_b32_e64 v178, 0, v178, s[56:57]
	v_cndmask_b32_e64 v179, 0, v179, s[58:59]
	v_cndmask_b32_e64 v180, 0, v180, s[60:61]
	v_cndmask_b32_e64 v181, 0, v181, s[62:63]
	v_cndmask_b32_e64 v182, 0, v182, s[64:65]
	v_cndmask_b32_e64 v183, 0, v183, s[66:67]
	v_cvt_pk_f16_f32 v184, v176, v177
	v_cvt_pk_f16_f32 v185, v178, v179
	v_cvt_pk_f16_f32 v186, v180, v181
	v_cvt_pk_f16_f32 v187, v182, v183
	s_waitcnt lgkmcnt(0)
	s_nop 0
	v_mfma_f32_16x16x32_f16 v[112:115], v[160:163], v[184:187], v[112:115]
	v_mfma_f32_16x16x32_f16 v[116:119], v[164:167], v[184:187], v[116:119]
	v_mfma_f32_16x16x32_f16 v[120:123], v[168:171], v[184:187], v[120:123]
	v_mfma_f32_16x16x32_f16 v[124:127], v[172:175], v[184:187], v[124:127]
	v_mfma_f32_16x16x32_f16 v[128:131], v[160:163], v[92:95], 0
	v_mfma_f32_16x16x32_f16 v[132:135], v[164:167], v[92:95], 0
	v_mfma_f32_16x16x32_f16 v[136:139], v[168:171], v[92:95], 0
	v_mfma_f32_16x16x32_f16 v[140:143], v[172:175], v[92:95], 0
	s_branch .Lmy_s2_kend1
.Lmy_s2_knext7:
	s_cmp_lt_u32 s42, 3
	s_cbranch_scc1 .Lmy_s2_kend1
	s_cmp_eq_u32 s42, 3
	s_cbranch_scc1 .Lmy_s2_diag8
	ds_read_b128 v[176:179], v38 offset:50048
	ds_read_b128 v[180:183], v38 offset:50064
	ds_read_b32 v188, v38 offset:49536
	ds_read_b128 v[160:163], v19 offset:0
	ds_read_b128 v[164:167], v19 offset:4096
	ds_read_b128 v[168:171], v19 offset:8192
	ds_read_b128 v[172:175], v19 offset:12288
	s_waitcnt lgkmcnt(4)
	v_fma_f32 v188, v188, s51, v189
	v_exp_f32_e32 v188, v188
	s_nop 0
	v_mul_f32_e32 v176, v188, v176
	v_mul_f32_e32 v177, v188, v177
	v_mul_f32_e32 v178, v188, v178
	v_mul_f32_e32 v179, v188, v179
	v_mul_f32_e32 v180, v188, v180
	v_mul_f32_e32 v181, v188, v181
	v_mul_f32_e32 v182, v188, v182
	v_mul_f32_e32 v183, v188, v183
	v_mul_f32_e32 v176, v84, v176
	v_mul_f32_e32 v177, v85, v177
	v_mul_f32_e32 v178, v86, v178
	v_mul_f32_e32 v179, v87, v179
	v_mul_f32_e32 v180, v88, v180
	v_mul_f32_e32 v181, v89, v181
	v_mul_f32_e32 v182, v90, v182
	v_mul_f32_e32 v183, v91, v183
	v_cvt_pk_f16_f32 v184, v176, v177
	v_cvt_pk_f16_f32 v185, v178, v179
	v_cvt_pk_f16_f32 v186, v180, v181
	v_cvt_pk_f16_f32 v187, v182, v183
	s_waitcnt lgkmcnt(0)
	s_nop 0
	v_mfma_f32_16x16x32_f16 v[112:115], v[160:163], v[184:187], v[112:115]
	v_mfma_f32_16x16x32_f16 v[116:119], v[164:167], v[184:187], v[116:119]
	v_mfma_f32_16x16x32_f16 v[120:123], v[168:171], v[184:187], v[120:123]
	v_mfma_f32_16x16x32_f16 v[124:127], v[172:175], v[184:187], v[124:127]
	s_branch .Lmy_s2_knext9
.Lmy_s2_diag8:
	ds_read_b128 v[176:179], v38 offset:50048
	ds_read_b128 v[180:183], v38 offset:50064
	ds_read_b32 v188, v38 offset:49536
	ds_read_b128 v[160:163], v19 offset:0
	ds_read_b128 v[164:167], v19 offset:4096
	ds_read_b128 v[168:171], v19 offset:8192
	ds_read_b128 v[172:175], v19 offset:12288
	s_waitcnt lgkmcnt(4)
	v_fma_f32 v188, v188, s51, v189
	v_exp_f32_e32 v188, v188
	s_nop 0
	v_mul_f32_e32 v176, v188, v176
	v_mul_f32_e32 v177, v188, v177
	v_mul_f32_e32 v178, v188, v178
	v_mul_f32_e32 v179, v188, v179
	v_mul_f32_e32 v180, v188, v180
	v_mul_f32_e32 v181, v188, v181
	v_mul_f32_e32 v182, v188, v182
	v_mul_f32_e32 v183, v188, v183
	v_mul_f32_e32 v176, v84, v176
	v_mul_f32_e32 v177, v85, v177
	v_mul_f32_e32 v178, v86, v178
	v_mul_f32_e32 v179, v87, v179
	v_mul_f32_e32 v180, v88, v180
	v_mul_f32_e32 v181, v89, v181
	v_mul_f32_e32 v182, v90, v182
	v_mul_f32_e32 v183, v91, v183
	v_cndmask_b32_e64 v176, 0, v176, s[52:53]
	v_cndmask_b32_e64 v177, 0, v177, s[54:55]
	v_cndmask_b32_e64 v178, 0, v178, s[56:57]
	v_cndmask_b32_e64 v179, 0, v179, s[58:59]
	v_cndmask_b32_e64 v180, 0, v180, s[60:61]
	v_cndmask_b32_e64 v181, 0, v181, s[62:63]
	v_cndmask_b32_e64 v182, 0, v182, s[64:65]
	v_cndmask_b32_e64 v183, 0, v183, s[66:67]
	v_cvt_pk_f16_f32 v184, v176, v177
	v_cvt_pk_f16_f32 v185, v178, v179
	v_cvt_pk_f16_f32 v186, v180, v181
	v_cvt_pk_f16_f32 v187, v182, v183
	s_waitcnt lgkmcnt(0)
	s_nop 0
	v_mfma_f32_16x16x32_f16 v[112:115], v[160:163], v[184:187], v[112:115]
	v_mfma_f32_16x16x32_f16 v[116:119], v[164:167], v[184:187], v[116:119]
	v_mfma_f32_16x16x32_f16 v[120:123], v[168:171], v[184:187], v[120:123]
	v_mfma_f32_16x16x32_f16 v[124:127], v[172:175], v[184:187], v[124:127]
	v_mfma_f32_16x16x32_f16 v[128:131], v[160:163], v[92:95], 0
	v_mfma_f32_16x16x32_f16 v[132:135], v[164:167], v[92:95], 0
	v_mfma_f32_16x16x32_f16 v[136:139], v[168:171], v[92:95], 0
	v_mfma_f32_16x16x32_f16 v[140:143], v[172:175], v[92:95], 0
	s_branch .Lmy_s2_kend1
.Lmy_s2_knext9:
.Lmy_s2_kend1:
	v_readlane_b32 s46, v11, 0
	v_readlane_b32 s47, v12, 0
	v_exp_f32_e32 v190, v189
	ds_read_b64 v[176:177], v24 offset:32768
	ds_read_b64 v[178:179], v25 offset:32768
	ds_read_b64 v[180:181], v26 offset:32768
	ds_read_b64 v[182:183], v27 offset:32768
	s_waitcnt lgkmcnt(0)
	s_nop 4
	v_cvt_f32_f16_e32 v198, v176
	v_cvt_f32_f16_sdwa v199, v176 dst_sel:DWORD dst_unused:UNUSED_PAD src0_sel:WORD_1
	v_cvt_f32_f16_e32 v200, v177
	v_cvt_f32_f16_sdwa v201, v177 dst_sel:DWORD dst_unused:UNUSED_PAD src0_sel:WORD_1
	v_fma_f32 v192, v190, v96, v112
	v_fma_f32 v193, v190, v97, v113
	v_fma_f32 v194, v190, v98, v114
	v_fma_f32 v195, v190, v99, v115
	v_mul_f32_e32 v192, s47, v192
	v_mul_f32_e32 v193, s47, v193
	v_mul_f32_e32 v194, s47, v194
	v_mul_f32_e32 v195, s47, v195
	v_fma_f32 v192, s46, v128, v192
	v_fma_f32 v193, s46, v129, v193
	v_fma_f32 v194, s46, v130, v194
	v_fma_f32 v195, s46, v131, v195
	v_mul_f32_e32 v192, v192, v198
	v_mul_f32_e32 v193, v193, v199
	v_mul_f32_e32 v194, v194, v200
	v_mul_f32_e32 v195, v195, v201
	v_fma_f32 v13, v192, v192, v13
	v_fma_f32 v13, v193, v193, v13
	v_fma_f32 v13, v194, v194, v13
	v_fma_f32 v13, v195, v195, v13
	v_mul_f32_e32 v192, 0x41800000, v192
	v_mul_f32_e32 v193, 0x41800000, v193
	v_mul_f32_e32 v194, 0x41800000, v194
	v_mul_f32_e32 v195, 0x41800000, v195
	v_cvt_pk_f16_f32 v196, v192, v193
	v_cvt_pk_f16_f32 v197, v194, v195
	ds_write_b64 v24, v[196:197] offset:32768
	v_cvt_f32_f16_e32 v198, v178
	v_cvt_f32_f16_sdwa v199, v178 dst_sel:DWORD dst_unused:UNUSED_PAD src0_sel:WORD_1
	v_cvt_f32_f16_e32 v200, v179
	v_cvt_f32_f16_sdwa v201, v179 dst_sel:DWORD dst_unused:UNUSED_PAD src0_sel:WORD_1
	v_fma_f32 v192, v190, v100, v116
	v_fma_f32 v193, v190, v101, v117
	v_fma_f32 v194, v190, v102, v118
	v_fma_f32 v195, v190, v103, v119
	v_mul_f32_e32 v192, s47, v192
	v_mul_f32_e32 v193, s47, v193
	v_mul_f32_e32 v194, s47, v194
	v_mul_f32_e32 v195, s47, v195
	v_fma_f32 v192, s46, v132, v192
	v_fma_f32 v193, s46, v133, v193
	v_fma_f32 v194, s46, v134, v194
	v_fma_f32 v195, s46, v135, v195
	v_mul_f32_e32 v192, v192, v198
	v_mul_f32_e32 v193, v193, v199
	v_mul_f32_e32 v194, v194, v200
	v_mul_f32_e32 v195, v195, v201
	v_fma_f32 v13, v192, v192, v13
	v_fma_f32 v13, v193, v193, v13
	v_fma_f32 v13, v194, v194, v13
	v_fma_f32 v13, v195, v195, v13
	v_mul_f32_e32 v192, 0x41800000, v192
	v_mul_f32_e32 v193, 0x41800000, v193
	v_mul_f32_e32 v194, 0x41800000, v194
	v_mul_f32_e32 v195, 0x41800000, v195
	v_cvt_pk_f16_f32 v196, v192, v193
	v_cvt_pk_f16_f32 v197, v194, v195
	ds_write_b64 v25, v[196:197] offset:32768
	v_cvt_f32_f16_e32 v198, v180
	v_cvt_f32_f16_sdwa v199, v180 dst_sel:DWORD dst_unused:UNUSED_PAD src0_sel:WORD_1
	v_cvt_f32_f16_e32 v200, v181
	v_cvt_f32_f16_sdwa v201, v181 dst_sel:DWORD dst_unused:UNUSED_PAD src0_sel:WORD_1
	v_fma_f32 v192, v190, v104, v120
	v_fma_f32 v193, v190, v105, v121
	v_fma_f32 v194, v190, v106, v122
	v_fma_f32 v195, v190, v107, v123
	v_mul_f32_e32 v192, s47, v192
	v_mul_f32_e32 v193, s47, v193
	v_mul_f32_e32 v194, s47, v194
	v_mul_f32_e32 v195, s47, v195
	v_fma_f32 v192, s46, v136, v192
	v_fma_f32 v193, s46, v137, v193
	v_fma_f32 v194, s46, v138, v194
	v_fma_f32 v195, s46, v139, v195
	v_mul_f32_e32 v192, v192, v198
	v_mul_f32_e32 v193, v193, v199
	v_mul_f32_e32 v194, v194, v200
	v_mul_f32_e32 v195, v195, v201
	v_fma_f32 v13, v192, v192, v13
	v_fma_f32 v13, v193, v193, v13
	v_fma_f32 v13, v194, v194, v13
	v_fma_f32 v13, v195, v195, v13
	v_mul_f32_e32 v192, 0x41800000, v192
	v_mul_f32_e32 v193, 0x41800000, v193
	v_mul_f32_e32 v194, 0x41800000, v194
	v_mul_f32_e32 v195, 0x41800000, v195
	v_cvt_pk_f16_f32 v196, v192, v193
	v_cvt_pk_f16_f32 v197, v194, v195
	ds_write_b64 v26, v[196:197] offset:32768
	v_cvt_f32_f16_e32 v198, v182
	v_cvt_f32_f16_sdwa v199, v182 dst_sel:DWORD dst_unused:UNUSED_PAD src0_sel:WORD_1
	v_cvt_f32_f16_e32 v200, v183
	v_cvt_f32_f16_sdwa v201, v183 dst_sel:DWORD dst_unused:UNUSED_PAD src0_sel:WORD_1
	v_fma_f32 v192, v190, v108, v124
	v_fma_f32 v193, v190, v109, v125
	v_fma_f32 v194, v190, v110, v126
	v_fma_f32 v195, v190, v111, v127
	v_mul_f32_e32 v192, s47, v192
	v_mul_f32_e32 v193, s47, v193
	v_mul_f32_e32 v194, s47, v194
	v_mul_f32_e32 v195, s47, v195
	v_fma_f32 v192, s46, v140, v192
	v_fma_f32 v193, s46, v141, v193
	v_fma_f32 v194, s46, v142, v194
	v_fma_f32 v195, s46, v143, v195
	v_mul_f32_e32 v192, v192, v198
	v_mul_f32_e32 v193, v193, v199
	v_mul_f32_e32 v194, v194, v200
	v_mul_f32_e32 v195, v195, v201
	v_fma_f32 v13, v192, v192, v13
	v_fma_f32 v13, v193, v193, v13
	v_fma_f32 v13, v194, v194, v13
	v_fma_f32 v13, v195, v195, v13
	v_mul_f32_e32 v192, 0x41800000, v192
	v_mul_f32_e32 v193, 0x41800000, v193
	v_mul_f32_e32 v194, 0x41800000, v194
	v_mul_f32_e32 v195, 0x41800000, v195
	v_cvt_pk_f16_f32 v196, v192, v193
	v_cvt_pk_f16_f32 v197, v194, v195
	ds_write_b64 v27, v[196:197] offset:32768
	s_waitcnt lgkmcnt(0)
	s_barrier
	ds_read_b128 v[204:207], v40 offset:32768
	ds_read_b128 v[208:211], v41 offset:32768
	s_waitcnt lgkmcnt(0)
	global_store_dwordx4 v8, v[204:207], s[38:39]
	global_store_dwordx4 v9, v[208:211], s[38:39]
	s_add_u32 s38, s38, 0x80
	s_addc_u32 s39, s39, 0
	s_add_u32 m0, s43, 0x0
	s_nop 0
	global_load_lds_dwordx4 v4, s[30:31]
	s_add_u32 m0, s43, 0x4000
	s_nop 0
	global_load_lds_dwordx4 v6, s[32:33]
	s_add_u32 m0, s43, 0x8000
	s_nop 0
	global_load_lds_dwordx4 v8, s[34:35]
	s_add_u32 m0, s43, 0x2000
	s_nop 0
	global_load_lds_dwordx4 v5, s[30:31]
	s_add_u32 m0, s43, 0x6000
	s_nop 0
	global_load_lds_dwordx4 v7, s[32:33]
	s_add_u32 m0, s43, 0xa000
	s_nop 0
	global_load_lds_dwordx4 v9, s[34:35]
	s_add_u32 m0, s44, 0xc000
	s_nop 0
	global_load_lds_dword v10, s[36:37]
	s_add_u32 s30, s30, 0x80000
	s_addc_u32 s31, s31, 0
	s_add_u32 s32, s32, 0x4000
	s_addc_u32 s33, s33, 0
	s_add_u32 s34, s34, 0x80
	s_addc_u32 s35, s35, 0
	s_add_u32 s36, s36, 0x4000
	s_addc_u32 s37, s37, 0
	s_waitcnt vmcnt(16)
	s_waitcnt lgkmcnt(0)
	s_barrier
	v_mov_b32_e32 v112, 0
	v_mov_b32_e32 v113, 0
	v_mov_b32_e32 v114, 0
	v_mov_b32_e32 v115, 0
	v_mov_b32_e32 v116, 0
	v_mov_b32_e32 v117, 0
	v_mov_b32_e32 v118, 0
	v_mov_b32_e32 v119, 0
	v_mov_b32_e32 v120, 0
	v_mov_b32_e32 v121, 0
	v_mov_b32_e32 v122, 0
	v_mov_b32_e32 v123, 0
	v_mov_b32_e32 v124, 0
	v_mov_b32_e32 v125, 0
	v_mov_b32_e32 v126, 0
	v_mov_b32_e32 v127, 0
	ds_read_b128 v[144:147], v20 offset:16384
	ds_read_b128 v[148:151], v20 offset:20480
	ds_read_b128 v[152:155], v20 offset:24576
	ds_read_b128 v[156:159], v20 offset:28672
	ds_read_b32 v189, v37 offset:49152
	ds_read_b128 v[160:163], v21 offset:16384
	ds_read_b128 v[164:167], v21 offset:20480
	ds_read_b128 v[168:171], v21 offset:24576
	ds_read_b128 v[172:175], v21 offset:28672
	s_waitcnt lgkmcnt(4)
	v_mfma_f32_16x16x32_f16 v[96:99], v[144:147], v[44:47], 0
	v_mfma_f32_16x16x32_f16 v[100:103], v[148:151], v[44:47], 0
	v_mfma_f32_16x16x32_f16 v[104:107], v[152:155], v[44:47], 0
	v_mfma_f32_16x16x32_f16 v[108:111], v[156:159], v[44:47], 0
	ds_read_b128 v[144:147], v22 offset:16384
	ds_read_b128 v[148:151], v22 offset:20480
	ds_read_b128 v[152:155], v22 offset:24576
	ds_read_b128 v[156:159], v22 offset:28672
	s_waitcnt lgkmcnt(4)
	v_mfma_f32_16x16x32_f16 v[96:99], v[160:163], v[48:51], v[96:99]
	v_mfma_f32_16x16x32_f16 v[100:103], v[164:167], v[48:51], v[100:103]
	v_mfma_f32_16x16x32_f16 v[104:107], v[168:171], v[48:51], v[104:107]
	v_mfma_f32_16x16x32_f16 v[108:111], v[172:175], v[48:51], v[108:111]
	ds_read_b128 v[160:163], v23 offset:16384
	ds_read_b128 v[164:167], v23 offset:20480
	ds_read_b128 v[168:171], v23 offset:24576
	ds_read_b128 v[172:175], v23 offset:28672
	s_waitcnt lgkmcnt(4)
	v_mfma_f32_16x16x32_f16 v[96:99], v[144:147], v[52:55], v[96:99]
	v_mfma_f32_16x16x32_f16 v[100:103], v[148:151], v[52:55], v[100:103]
	v_mfma_f32_16x16x32_f16 v[104:107], v[152:155], v[52:55], v[104:107]
	v_mfma_f32_16x16x32_f16 v[108:111], v[156:159], v[52:55], v[108:111]
	s_waitcnt lgkmcnt(0)
	v_mfma_f32_16x16x32_f16 v[96:99], v[160:163], v[56:59], v[96:99]
	v_mfma_f32_16x16x32_f16 v[100:103], v[164:167], v[56:59], v[100:103]
	v_mfma_f32_16x16x32_f16 v[104:107], v[168:171], v[56:59], v[104:107]
	v_mfma_f32_16x16x32_f16 v[108:111], v[172:175], v[56:59], v[108:111]
	v_mul_f32_e32 v189, 0x3fb8aa3b, v189
	s_cmp_lt_u32 s42, 0
	s_cbranch_scc1 .Lmy_s2_kend10
	s_cmp_eq_u32 s42, 0
	s_cbranch_scc1 .Lmy_s2_diag11
	ds_read_b128 v[176:179], v39 offset:49664
	ds_read_b128 v[180:183], v39 offset:49680
	ds_read_b32 v188, v39 offset:49152
	ds_read_b128 v[160:163], v20 offset:0
	ds_read_b128 v[164:167], v20 offset:4096
	ds_read_b128 v[168:171], v20 offset:8192
	ds_read_b128 v[172:175], v20 offset:12288
	s_waitcnt lgkmcnt(4)
	v_fma_f32 v188, v188, s51, v189
	v_exp_f32_e32 v188, v188
	s_nop 0
	v_mul_f32_e32 v176, v188, v176
	v_mul_f32_e32 v177, v188, v177
	v_mul_f32_e32 v178, v188, v178
	v_mul_f32_e32 v179, v188, v179
	v_mul_f32_e32 v180, v188, v180
	v_mul_f32_e32 v181, v188, v181
	v_mul_f32_e32 v182, v188, v182
	v_mul_f32_e32 v183, v188, v183
	v_mul_f32_e32 v176, v60, v176
	v_mul_f32_e32 v177, v61, v177
	v_mul_f32_e32 v178, v62, v178
	v_mul_f32_e32 v179, v63, v179
	v_mul_f32_e32 v180, v64, v180
	v_mul_f32_e32 v181, v65, v181
	v_mul_f32_e32 v182, v66, v182
	v_mul_f32_e32 v183, v67, v183
	v_cvt_pk_f16_f32 v184, v176, v177
	v_cvt_pk_f16_f32 v185, v178, v179
	v_cvt_pk_f16_f32 v186, v180, v181
	v_cvt_pk_f16_f32 v187, v182, v183
	s_waitcnt lgkmcnt(0)
	s_nop 0
	v_mfma_f32_16x16x32_f16 v[112:115], v[160:163], v[184:187], v[112:115]
	v_mfma_f32_16x16x32_f16 v[116:119], v[164:167], v[184:187], v[116:119]
	v_mfma_f32_16x16x32_f16 v[120:123], v[168:171], v[184:187], v[120:123]
	v_mfma_f32_16x16x32_f16 v[124:127], v[172:175], v[184:187], v[124:127]
	s_branch .Lmy_s2_knext12
.Lmy_s2_diag11:
	ds_read_b128 v[176:179], v39 offset:49664
	ds_read_b128 v[180:183], v39 offset:49680
	ds_read_b32 v188, v39 offset:49152
	ds_read_b128 v[160:163], v20 offset:0
	ds_read_b128 v[164:167], v20 offset:4096
	ds_read_b128 v[168:171], v20 offset:8192
	ds_read_b128 v[172:175], v20 offset:12288
	s_waitcnt lgkmcnt(4)
	v_fma_f32 v188, v188, s51, v189
	v_exp_f32_e32 v188, v188
	s_nop 0
	v_mul_f32_e32 v176, v188, v176
	v_mul_f32_e32 v177, v188, v177
	v_mul_f32_e32 v178, v188, v178
	v_mul_f32_e32 v179, v188, v179
	v_mul_f32_e32 v180, v188, v180
	v_mul_f32_e32 v181, v188, v181
	v_mul_f32_e32 v182, v188, v182
	v_mul_f32_e32 v183, v188, v183
	v_mul_f32_e32 v176, v60, v176
	v_mul_f32_e32 v177, v61, v177
	v_mul_f32_e32 v178, v62, v178
	v_mul_f32_e32 v179, v63, v179
	v_mul_f32_e32 v180, v64, v180
	v_mul_f32_e32 v181, v65, v181
	v_mul_f32_e32 v182, v66, v182
	v_mul_f32_e32 v183, v67, v183
	v_cndmask_b32_e64 v176, 0, v176, s[52:53]
	v_cndmask_b32_e64 v177, 0, v177, s[54:55]
	v_cndmask_b32_e64 v178, 0, v178, s[56:57]
	v_cndmask_b32_e64 v179, 0, v179, s[58:59]
	v_cndmask_b32_e64 v180, 0, v180, s[60:61]
	v_cndmask_b32_e64 v181, 0, v181, s[62:63]
	v_cndmask_b32_e64 v182, 0, v182, s[64:65]
	v_cndmask_b32_e64 v183, 0, v183, s[66:67]
	v_cvt_pk_f16_f32 v184, v176, v177
	v_cvt_pk_f16_f32 v185, v178, v179
	v_cvt_pk_f16_f32 v186, v180, v181
	v_cvt_pk_f16_f32 v187, v182, v183
	s_waitcnt lgkmcnt(0)
	s_nop 0
	v_mfma_f32_16x16x32_f16 v[112:115], v[160:163], v[184:187], v[112:115]
	v_mfma_f32_16x16x32_f16 v[116:119], v[164:167], v[184:187], v[116:119]
	v_mfma_f32_16x16x32_f16 v[120:123], v[168:171], v[184:187], v[120:123]
	v_mfma_f32_16x16x32_f16 v[124:127], v[172:175], v[184:187], v[124:127]
	v_mfma_f32_16x16x32_f16 v[128:131], v[160:163], v[92:95], 0
	v_mfma_f32_16x16x32_f16 v[132:135], v[164:167], v[92:95], 0
	v_mfma_f32_16x16x32_f16 v[136:139], v[168:171], v[92:95], 0
	v_mfma_f32_16x16x32_f16 v[140:143], v[172:175], v[92:95], 0
	s_branch .Lmy_s2_kend10
.Lmy_s2_knext12:
	s_cmp_lt_u32 s42, 1
	s_cbranch_scc1 .Lmy_s2_kend10
	s_cmp_eq_u32 s42, 1
	s_cbranch_scc1 .Lmy_s2_diag13
	ds_read_b128 v[176:179], v39 offset:49792
	ds_read_b128 v[180:183], v39 offset:49808
	ds_read_b32 v188, v39 offset:49280
	ds_read_b128 v[160:163], v21 offset:0
	ds_read_b128 v[164:167], v21 offset:4096
	ds_read_b128 v[168:171], v21 offset:8192
	ds_read_b128 v[172:175], v21 offset:12288
	s_waitcnt lgkmcnt(4)
	v_fma_f32 v188, v188, s51, v189
	v_exp_f32_e32 v188, v188
	s_nop 0
	v_mul_f32_e32 v176, v188, v176
	v_mul_f32_e32 v177, v188, v177
	v_mul_f32_e32 v178, v188, v178
	v_mul_f32_e32 v179, v188, v179
	v_mul_f32_e32 v180, v188, v180
	v_mul_f32_e32 v181, v188, v181
	v_mul_f32_e32 v182, v188, v182
	v_mul_f32_e32 v183, v188, v183
	v_mul_f32_e32 v176, v68, v176
	v_mul_f32_e32 v177, v69, v177
	v_mul_f32_e32 v178, v70, v178
	v_mul_f32_e32 v179, v71, v179
	v_mul_f32_e32 v180, v72, v180
	v_mul_f32_e32 v181, v73, v181
	v_mul_f32_e32 v182, v74, v182
	v_mul_f32_e32 v183, v75, v183
	v_cvt_pk_f16_f32 v184, v176, v177
	v_cvt_pk_f16_f32 v185, v178, v179
	v_cvt_pk_f16_f32 v186, v180, v181
	v_cvt_pk_f16_f32 v187, v182, v183
	s_waitcnt lgkmcnt(0)
	s_nop 0
	v_mfma_f32_16x16x32_f16 v[112:115], v[160:163], v[184:187], v[112:115]
	v_mfma_f32_16x16x32_f16 v[116:119], v[164:167], v[184:187], v[116:119]
	v_mfma_f32_16x16x32_f16 v[120:123], v[168:171], v[184:187], v[120:123]
	v_mfma_f32_16x16x32_f16 v[124:127], v[172:175], v[184:187], v[124:127]
	s_branch .Lmy_s2_knext14
.Lmy_s2_diag13:
	ds_read_b128 v[176:179], v39 offset:49792
	ds_read_b128 v[180:183], v39 offset:49808
	ds_read_b32 v188, v39 offset:49280
	ds_read_b128 v[160:163], v21 offset:0
	ds_read_b128 v[164:167], v21 offset:4096
	ds_read_b128 v[168:171], v21 offset:8192
	ds_read_b128 v[172:175], v21 offset:12288
	s_waitcnt lgkmcnt(4)
	v_fma_f32 v188, v188, s51, v189
	v_exp_f32_e32 v188, v188
	s_nop 0
	v_mul_f32_e32 v176, v188, v176
	v_mul_f32_e32 v177, v188, v177
	v_mul_f32_e32 v178, v188, v178
	v_mul_f32_e32 v179, v188, v179
	v_mul_f32_e32 v180, v188, v180
	v_mul_f32_e32 v181, v188, v181
	v_mul_f32_e32 v182, v188, v182
	v_mul_f32_e32 v183, v188, v183
	v_mul_f32_e32 v176, v68, v176
	v_mul_f32_e32 v177, v69, v177
	v_mul_f32_e32 v178, v70, v178
	v_mul_f32_e32 v179, v71, v179
	v_mul_f32_e32 v180, v72, v180
	v_mul_f32_e32 v181, v73, v181
	v_mul_f32_e32 v182, v74, v182
	v_mul_f32_e32 v183, v75, v183
	v_cndmask_b32_e64 v176, 0, v176, s[52:53]
	v_cndmask_b32_e64 v177, 0, v177, s[54:55]
	v_cndmask_b32_e64 v178, 0, v178, s[56:57]
	v_cndmask_b32_e64 v179, 0, v179, s[58:59]
	v_cndmask_b32_e64 v180, 0, v180, s[60:61]
	v_cndmask_b32_e64 v181, 0, v181, s[62:63]
	v_cndmask_b32_e64 v182, 0, v182, s[64:65]
	v_cndmask_b32_e64 v183, 0, v183, s[66:67]
	v_cvt_pk_f16_f32 v184, v176, v177
	v_cvt_pk_f16_f32 v185, v178, v179
	v_cvt_pk_f16_f32 v186, v180, v181
	v_cvt_pk_f16_f32 v187, v182, v183
	s_waitcnt lgkmcnt(0)
	s_nop 0
	v_mfma_f32_16x16x32_f16 v[112:115], v[160:163], v[184:187], v[112:115]
	v_mfma_f32_16x16x32_f16 v[116:119], v[164:167], v[184:187], v[116:119]
	v_mfma_f32_16x16x32_f16 v[120:123], v[168:171], v[184:187], v[120:123]
	v_mfma_f32_16x16x32_f16 v[124:127], v[172:175], v[184:187], v[124:127]
	v_mfma_f32_16x16x32_f16 v[128:131], v[160:163], v[92:95], 0
	v_mfma_f32_16x16x32_f16 v[132:135], v[164:167], v[92:95], 0
	v_mfma_f32_16x16x32_f16 v[136:139], v[168:171], v[92:95], 0
	v_mfma_f32_16x16x32_f16 v[140:143], v[172:175], v[92:95], 0
	s_branch .Lmy_s2_kend10
.Lmy_s2_knext14:
	s_cmp_lt_u32 s42, 2
	s_cbranch_scc1 .Lmy_s2_kend10
	s_cmp_eq_u32 s42, 2
	s_cbranch_scc1 .Lmy_s2_diag15
	ds_read_b128 v[176:179], v39 offset:49920
	ds_read_b128 v[180:183], v39 offset:49936
	ds_read_b32 v188, v39 offset:49408
	ds_read_b128 v[160:163], v22 offset:0
	ds_read_b128 v[164:167], v22 offset:4096
	ds_read_b128 v[168:171], v22 offset:8192
	ds_read_b128 v[172:175], v22 offset:12288
	s_waitcnt lgkmcnt(4)
	v_fma_f32 v188, v188, s51, v189
	v_exp_f32_e32 v188, v188
	s_nop 0
	v_mul_f32_e32 v176, v188, v176
	v_mul_f32_e32 v177, v188, v177
	v_mul_f32_e32 v178, v188, v178
	v_mul_f32_e32 v179, v188, v179
	v_mul_f32_e32 v180, v188, v180
	v_mul_f32_e32 v181, v188, v181
	v_mul_f32_e32 v182, v188, v182
	v_mul_f32_e32 v183, v188, v183
	v_mul_f32_e32 v176, v76, v176
	v_mul_f32_e32 v177, v77, v177
	v_mul_f32_e32 v178, v78, v178
	v_mul_f32_e32 v179, v79, v179
	v_mul_f32_e32 v180, v80, v180
	v_mul_f32_e32 v181, v81, v181
	v_mul_f32_e32 v182, v82, v182
	v_mul_f32_e32 v183, v83, v183
	v_cvt_pk_f16_f32 v184, v176, v177
	v_cvt_pk_f16_f32 v185, v178, v179
	v_cvt_pk_f16_f32 v186, v180, v181
	v_cvt_pk_f16_f32 v187, v182, v183
	s_waitcnt lgkmcnt(0)
	s_nop 0
	v_mfma_f32_16x16x32_f16 v[112:115], v[160:163], v[184:187], v[112:115]
	v_mfma_f32_16x16x32_f16 v[116:119], v[164:167], v[184:187], v[116:119]
	v_mfma_f32_16x16x32_f16 v[120:123], v[168:171], v[184:187], v[120:123]
	v_mfma_f32_16x16x32_f16 v[124:127], v[172:175], v[184:187], v[124:127]
	s_branch .Lmy_s2_knext16
.Lmy_s2_diag15:
	ds_read_b128 v[176:179], v39 offset:49920
	ds_read_b128 v[180:183], v39 offset:49936
	ds_read_b32 v188, v39 offset:49408
	ds_read_b128 v[160:163], v22 offset:0
	ds_read_b128 v[164:167], v22 offset:4096
	ds_read_b128 v[168:171], v22 offset:8192
	ds_read_b128 v[172:175], v22 offset:12288
	s_waitcnt lgkmcnt(4)
	v_fma_f32 v188, v188, s51, v189
	v_exp_f32_e32 v188, v188
	s_nop 0
	v_mul_f32_e32 v176, v188, v176
	v_mul_f32_e32 v177, v188, v177
	v_mul_f32_e32 v178, v188, v178
	v_mul_f32_e32 v179, v188, v179
	v_mul_f32_e32 v180, v188, v180
	v_mul_f32_e32 v181, v188, v181
	v_mul_f32_e32 v182, v188, v182
	v_mul_f32_e32 v183, v188, v183
	v_mul_f32_e32 v176, v76, v176
	v_mul_f32_e32 v177, v77, v177
	v_mul_f32_e32 v178, v78, v178
	v_mul_f32_e32 v179, v79, v179
	v_mul_f32_e32 v180, v80, v180
	v_mul_f32_e32 v181, v81, v181
	v_mul_f32_e32 v182, v82, v182
	v_mul_f32_e32 v183, v83, v183
	v_cndmask_b32_e64 v176, 0, v176, s[52:53]
	v_cndmask_b32_e64 v177, 0, v177, s[54:55]
	v_cndmask_b32_e64 v178, 0, v178, s[56:57]
	v_cndmask_b32_e64 v179, 0, v179, s[58:59]
	v_cndmask_b32_e64 v180, 0, v180, s[60:61]
	v_cndmask_b32_e64 v181, 0, v181, s[62:63]
	v_cndmask_b32_e64 v182, 0, v182, s[64:65]
	v_cndmask_b32_e64 v183, 0, v183, s[66:67]
	v_cvt_pk_f16_f32 v184, v176, v177
	v_cvt_pk_f16_f32 v185, v178, v179
	v_cvt_pk_f16_f32 v186, v180, v181
	v_cvt_pk_f16_f32 v187, v182, v183
	s_waitcnt lgkmcnt(0)
	s_nop 0
	v_mfma_f32_16x16x32_f16 v[112:115], v[160:163], v[184:187], v[112:115]
	v_mfma_f32_16x16x32_f16 v[116:119], v[164:167], v[184:187], v[116:119]
	v_mfma_f32_16x16x32_f16 v[120:123], v[168:171], v[184:187], v[120:123]
	v_mfma_f32_16x16x32_f16 v[124:127], v[172:175], v[184:187], v[124:127]
	v_mfma_f32_16x16x32_f16 v[128:131], v[160:163], v[92:95], 0
	v_mfma_f32_16x16x32_f16 v[132:135], v[164:167], v[92:95], 0
	v_mfma_f32_16x16x32_f16 v[136:139], v[168:171], v[92:95], 0
	v_mfma_f32_16x16x32_f16 v[140:143], v[172:175], v[92:95], 0
	s_branch .Lmy_s2_kend10
.Lmy_s2_knext16:
	s_cmp_lt_u32 s42, 3
	s_cbranch_scc1 .Lmy_s2_kend10
	s_cmp_eq_u32 s42, 3
	s_cbranch_scc1 .Lmy_s2_diag17
	ds_read_b128 v[176:179], v39 offset:50048
	ds_read_b128 v[180:183], v39 offset:50064
	ds_read_b32 v188, v39 offset:49536
	ds_read_b128 v[160:163], v23 offset:0
	ds_read_b128 v[164:167], v23 offset:4096
	ds_read_b128 v[168:171], v23 offset:8192
	ds_read_b128 v[172:175], v23 offset:12288
	s_waitcnt lgkmcnt(4)
	v_fma_f32 v188, v188, s51, v189
	v_exp_f32_e32 v188, v188
	s_nop 0
	v_mul_f32_e32 v176, v188, v176
	v_mul_f32_e32 v177, v188, v177
	v_mul_f32_e32 v178, v188, v178
	v_mul_f32_e32 v179, v188, v179
	v_mul_f32_e32 v180, v188, v180
	v_mul_f32_e32 v181, v188, v181
	v_mul_f32_e32 v182, v188, v182
	v_mul_f32_e32 v183, v188, v183
	v_mul_f32_e32 v176, v84, v176
	v_mul_f32_e32 v177, v85, v177
	v_mul_f32_e32 v178, v86, v178
	v_mul_f32_e32 v179, v87, v179
	v_mul_f32_e32 v180, v88, v180
	v_mul_f32_e32 v181, v89, v181
	v_mul_f32_e32 v182, v90, v182
	v_mul_f32_e32 v183, v91, v183
	v_cvt_pk_f16_f32 v184, v176, v177
	v_cvt_pk_f16_f32 v185, v178, v179
	v_cvt_pk_f16_f32 v186, v180, v181
	v_cvt_pk_f16_f32 v187, v182, v183
	s_waitcnt lgkmcnt(0)
	s_nop 0
	v_mfma_f32_16x16x32_f16 v[112:115], v[160:163], v[184:187], v[112:115]
	v_mfma_f32_16x16x32_f16 v[116:119], v[164:167], v[184:187], v[116:119]
	v_mfma_f32_16x16x32_f16 v[120:123], v[168:171], v[184:187], v[120:123]
	v_mfma_f32_16x16x32_f16 v[124:127], v[172:175], v[184:187], v[124:127]
	s_branch .Lmy_s2_knext18
.Lmy_s2_diag17:
	ds_read_b128 v[176:179], v39 offset:50048
	ds_read_b128 v[180:183], v39 offset:50064
	ds_read_b32 v188, v39 offset:49536
	ds_read_b128 v[160:163], v23 offset:0
	ds_read_b128 v[164:167], v23 offset:4096
	ds_read_b128 v[168:171], v23 offset:8192
	ds_read_b128 v[172:175], v23 offset:12288
	s_waitcnt lgkmcnt(4)
	v_fma_f32 v188, v188, s51, v189
	v_exp_f32_e32 v188, v188
	s_nop 0
	v_mul_f32_e32 v176, v188, v176
	v_mul_f32_e32 v177, v188, v177
	v_mul_f32_e32 v178, v188, v178
	v_mul_f32_e32 v179, v188, v179
	v_mul_f32_e32 v180, v188, v180
	v_mul_f32_e32 v181, v188, v181
	v_mul_f32_e32 v182, v188, v182
	v_mul_f32_e32 v183, v188, v183
	v_mul_f32_e32 v176, v84, v176
	v_mul_f32_e32 v177, v85, v177
	v_mul_f32_e32 v178, v86, v178
	v_mul_f32_e32 v179, v87, v179
	v_mul_f32_e32 v180, v88, v180
	v_mul_f32_e32 v181, v89, v181
	v_mul_f32_e32 v182, v90, v182
	v_mul_f32_e32 v183, v91, v183
	v_cndmask_b32_e64 v176, 0, v176, s[52:53]
	v_cndmask_b32_e64 v177, 0, v177, s[54:55]
	v_cndmask_b32_e64 v178, 0, v178, s[56:57]
	v_cndmask_b32_e64 v179, 0, v179, s[58:59]
	v_cndmask_b32_e64 v180, 0, v180, s[60:61]
	v_cndmask_b32_e64 v181, 0, v181, s[62:63]
	v_cndmask_b32_e64 v182, 0, v182, s[64:65]
	v_cndmask_b32_e64 v183, 0, v183, s[66:67]
	v_cvt_pk_f16_f32 v184, v176, v177
	v_cvt_pk_f16_f32 v185, v178, v179
	v_cvt_pk_f16_f32 v186, v180, v181
	v_cvt_pk_f16_f32 v187, v182, v183
	s_waitcnt lgkmcnt(0)
	s_nop 0
	v_mfma_f32_16x16x32_f16 v[112:115], v[160:163], v[184:187], v[112:115]
	v_mfma_f32_16x16x32_f16 v[116:119], v[164:167], v[184:187], v[116:119]
	v_mfma_f32_16x16x32_f16 v[120:123], v[168:171], v[184:187], v[120:123]
	v_mfma_f32_16x16x32_f16 v[124:127], v[172:175], v[184:187], v[124:127]
	v_mfma_f32_16x16x32_f16 v[128:131], v[160:163], v[92:95], 0
	v_mfma_f32_16x16x32_f16 v[132:135], v[164:167], v[92:95], 0
	v_mfma_f32_16x16x32_f16 v[136:139], v[168:171], v[92:95], 0
	v_mfma_f32_16x16x32_f16 v[140:143], v[172:175], v[92:95], 0
	s_branch .Lmy_s2_kend10
.Lmy_s2_knext18:
.Lmy_s2_kend10:
	v_readlane_b32 s46, v11, 1
	v_readlane_b32 s47, v12, 1
	v_exp_f32_e32 v190, v189
	ds_read_b64 v[176:177], v28 offset:32768
	ds_read_b64 v[178:179], v29 offset:32768
	ds_read_b64 v[180:181], v30 offset:32768
	ds_read_b64 v[182:183], v31 offset:32768
	s_waitcnt lgkmcnt(0)
	s_nop 4
	v_cvt_f32_f16_e32 v198, v176
	v_cvt_f32_f16_sdwa v199, v176 dst_sel:DWORD dst_unused:UNUSED_PAD src0_sel:WORD_1
	v_cvt_f32_f16_e32 v200, v177
	v_cvt_f32_f16_sdwa v201, v177 dst_sel:DWORD dst_unused:UNUSED_PAD src0_sel:WORD_1
	v_fma_f32 v192, v190, v96, v112
	v_fma_f32 v193, v190, v97, v113
	v_fma_f32 v194, v190, v98, v114
	v_fma_f32 v195, v190, v99, v115
	v_mul_f32_e32 v192, s47, v192
	v_mul_f32_e32 v193, s47, v193
	v_mul_f32_e32 v194, s47, v194
	v_mul_f32_e32 v195, s47, v195
	v_fma_f32 v192, s46, v128, v192
	v_fma_f32 v193, s46, v129, v193
	v_fma_f32 v194, s46, v130, v194
	v_fma_f32 v195, s46, v131, v195
	v_mul_f32_e32 v192, v192, v198
	v_mul_f32_e32 v193, v193, v199
	v_mul_f32_e32 v194, v194, v200
	v_mul_f32_e32 v195, v195, v201
	v_fma_f32 v13, v192, v192, v13
	v_fma_f32 v13, v193, v193, v13
	v_fma_f32 v13, v194, v194, v13
	v_fma_f32 v13, v195, v195, v13
	v_mul_f32_e32 v192, 0x41800000, v192
	v_mul_f32_e32 v193, 0x41800000, v193
	v_mul_f32_e32 v194, 0x41800000, v194
	v_mul_f32_e32 v195, 0x41800000, v195
	v_cvt_pk_f16_f32 v196, v192, v193
	v_cvt_pk_f16_f32 v197, v194, v195
	ds_write_b64 v28, v[196:197] offset:32768
	v_cvt_f32_f16_e32 v198, v178
	v_cvt_f32_f16_sdwa v199, v178 dst_sel:DWORD dst_unused:UNUSED_PAD src0_sel:WORD_1
	v_cvt_f32_f16_e32 v200, v179
	v_cvt_f32_f16_sdwa v201, v179 dst_sel:DWORD dst_unused:UNUSED_PAD src0_sel:WORD_1
	v_fma_f32 v192, v190, v100, v116
	v_fma_f32 v193, v190, v101, v117
	v_fma_f32 v194, v190, v102, v118
	v_fma_f32 v195, v190, v103, v119
	v_mul_f32_e32 v192, s47, v192
	v_mul_f32_e32 v193, s47, v193
	v_mul_f32_e32 v194, s47, v194
	v_mul_f32_e32 v195, s47, v195
	v_fma_f32 v192, s46, v132, v192
	v_fma_f32 v193, s46, v133, v193
	v_fma_f32 v194, s46, v134, v194
	v_fma_f32 v195, s46, v135, v195
	v_mul_f32_e32 v192, v192, v198
	v_mul_f32_e32 v193, v193, v199
	v_mul_f32_e32 v194, v194, v200
	v_mul_f32_e32 v195, v195, v201
	v_fma_f32 v13, v192, v192, v13
	v_fma_f32 v13, v193, v193, v13
	v_fma_f32 v13, v194, v194, v13
	v_fma_f32 v13, v195, v195, v13
	v_mul_f32_e32 v192, 0x41800000, v192
	v_mul_f32_e32 v193, 0x41800000, v193
	v_mul_f32_e32 v194, 0x41800000, v194
	v_mul_f32_e32 v195, 0x41800000, v195
	v_cvt_pk_f16_f32 v196, v192, v193
	v_cvt_pk_f16_f32 v197, v194, v195
	ds_write_b64 v29, v[196:197] offset:32768
	v_cvt_f32_f16_e32 v198, v180
	v_cvt_f32_f16_sdwa v199, v180 dst_sel:DWORD dst_unused:UNUSED_PAD src0_sel:WORD_1
	v_cvt_f32_f16_e32 v200, v181
	v_cvt_f32_f16_sdwa v201, v181 dst_sel:DWORD dst_unused:UNUSED_PAD src0_sel:WORD_1
	v_fma_f32 v192, v190, v104, v120
	v_fma_f32 v193, v190, v105, v121
	v_fma_f32 v194, v190, v106, v122
	v_fma_f32 v195, v190, v107, v123
	v_mul_f32_e32 v192, s47, v192
	v_mul_f32_e32 v193, s47, v193
	v_mul_f32_e32 v194, s47, v194
	v_mul_f32_e32 v195, s47, v195
	v_fma_f32 v192, s46, v136, v192
	v_fma_f32 v193, s46, v137, v193
	v_fma_f32 v194, s46, v138, v194
	v_fma_f32 v195, s46, v139, v195
	v_mul_f32_e32 v192, v192, v198
	v_mul_f32_e32 v193, v193, v199
	v_mul_f32_e32 v194, v194, v200
	v_mul_f32_e32 v195, v195, v201
	v_fma_f32 v13, v192, v192, v13
	v_fma_f32 v13, v193, v193, v13
	v_fma_f32 v13, v194, v194, v13
	v_fma_f32 v13, v195, v195, v13
	v_mul_f32_e32 v192, 0x41800000, v192
	v_mul_f32_e32 v193, 0x41800000, v193
	v_mul_f32_e32 v194, 0x41800000, v194
	v_mul_f32_e32 v195, 0x41800000, v195
	v_cvt_pk_f16_f32 v196, v192, v193
	v_cvt_pk_f16_f32 v197, v194, v195
	ds_write_b64 v30, v[196:197] offset:32768
	v_cvt_f32_f16_e32 v198, v182
	v_cvt_f32_f16_sdwa v199, v182 dst_sel:DWORD dst_unused:UNUSED_PAD src0_sel:WORD_1
	v_cvt_f32_f16_e32 v200, v183
	v_cvt_f32_f16_sdwa v201, v183 dst_sel:DWORD dst_unused:UNUSED_PAD src0_sel:WORD_1
	v_fma_f32 v192, v190, v108, v124
	v_fma_f32 v193, v190, v109, v125
	v_fma_f32 v194, v190, v110, v126
	v_fma_f32 v195, v190, v111, v127
	v_mul_f32_e32 v192, s47, v192
	v_mul_f32_e32 v193, s47, v193
	v_mul_f32_e32 v194, s47, v194
	v_mul_f32_e32 v195, s47, v195
	v_fma_f32 v192, s46, v140, v192
	v_fma_f32 v193, s46, v141, v193
	v_fma_f32 v194, s46, v142, v194
	v_fma_f32 v195, s46, v143, v195
	v_mul_f32_e32 v192, v192, v198
	v_mul_f32_e32 v193, v193, v199
	v_mul_f32_e32 v194, v194, v200
	v_mul_f32_e32 v195, v195, v201
	v_fma_f32 v13, v192, v192, v13
	v_fma_f32 v13, v193, v193, v13
	v_fma_f32 v13, v194, v194, v13
	v_fma_f32 v13, v195, v195, v13
	v_mul_f32_e32 v192, 0x41800000, v192
	v_mul_f32_e32 v193, 0x41800000, v193
	v_mul_f32_e32 v194, 0x41800000, v194
	v_mul_f32_e32 v195, 0x41800000, v195
	v_cvt_pk_f16_f32 v196, v192, v193
	v_cvt_pk_f16_f32 v197, v194, v195
	ds_write_b64 v31, v[196:197] offset:32768
	s_waitcnt lgkmcnt(0)
	s_barrier
	ds_read_b128 v[204:207], v32 offset:32768
	ds_read_b128 v[208:211], v33 offset:32768
	s_waitcnt lgkmcnt(0)
	global_store_dwordx4 v8, v[204:207], s[38:39]
	global_store_dwordx4 v9, v[208:211], s[38:39]
	s_add_u32 s38, s38, 0x80
	s_addc_u32 s39, s39, 0
	s_add_u32 m0, s43, 0xc800
	s_nop 0
	global_load_lds_dwordx4 v4, s[30:31]
	s_add_u32 m0, s43, 0x10800
	s_nop 0
	global_load_lds_dwordx4 v6, s[32:33]
	s_add_u32 m0, s43, 0x14800
	s_nop 0
	global_load_lds_dwordx4 v8, s[34:35]
	s_add_u32 m0, s43, 0xe800
	s_nop 0
	global_load_lds_dwordx4 v5, s[30:31]
	s_add_u32 m0, s43, 0x12800
	s_nop 0
	global_load_lds_dwordx4 v7, s[32:33]
	s_add_u32 m0, s43, 0x16800
	s_nop 0
	global_load_lds_dwordx4 v9, s[34:35]
	s_add_u32 m0, s44, 0x18800
	s_nop 0
	global_load_lds_dword v10, s[36:37]
	s_add_u32 s30, s30, 0x80000
	s_addc_u32 s31, s31, 0
	s_add_u32 s32, s32, 0x4000
	s_addc_u32 s33, s33, 0
	s_add_u32 s34, s34, 0x80
	s_addc_u32 s35, s35, 0
	s_add_u32 s36, s36, 0x4000
	s_addc_u32 s37, s37, 0
	s_waitcnt vmcnt(18)
	s_waitcnt lgkmcnt(0)
	s_barrier
	v_mov_b32_e32 v112, 0
	v_mov_b32_e32 v113, 0
	v_mov_b32_e32 v114, 0
	v_mov_b32_e32 v115, 0
	v_mov_b32_e32 v116, 0
	v_mov_b32_e32 v117, 0
	v_mov_b32_e32 v118, 0
	v_mov_b32_e32 v119, 0
	v_mov_b32_e32 v120, 0
	v_mov_b32_e32 v121, 0
	v_mov_b32_e32 v122, 0
	v_mov_b32_e32 v123, 0
	v_mov_b32_e32 v124, 0
	v_mov_b32_e32 v125, 0
	v_mov_b32_e32 v126, 0
	v_mov_b32_e32 v127, 0
	ds_read_b128 v[144:147], v212 offset:16384
	ds_read_b128 v[148:151], v212 offset:20480
	ds_read_b128 v[152:155], v212 offset:24576
	ds_read_b128 v[156:159], v212 offset:28672
	ds_read_b32 v189, v220 offset:49152
	ds_read_b128 v[160:163], v213 offset:16384
	ds_read_b128 v[164:167], v213 offset:20480
	ds_read_b128 v[168:171], v213 offset:24576
	ds_read_b128 v[172:175], v213 offset:28672
	s_waitcnt lgkmcnt(4)
	v_mfma_f32_16x16x32_f16 v[96:99], v[144:147], v[44:47], 0
	v_mfma_f32_16x16x32_f16 v[100:103], v[148:151], v[44:47], 0
	v_mfma_f32_16x16x32_f16 v[104:107], v[152:155], v[44:47], 0
	v_mfma_f32_16x16x32_f16 v[108:111], v[156:159], v[44:47], 0
	ds_read_b128 v[144:147], v214 offset:16384
	ds_read_b128 v[148:151], v214 offset:20480
	ds_read_b128 v[152:155], v214 offset:24576
	ds_read_b128 v[156:159], v214 offset:28672
	s_waitcnt lgkmcnt(4)
	v_mfma_f32_16x16x32_f16 v[96:99], v[160:163], v[48:51], v[96:99]
	v_mfma_f32_16x16x32_f16 v[100:103], v[164:167], v[48:51], v[100:103]
	v_mfma_f32_16x16x32_f16 v[104:107], v[168:171], v[48:51], v[104:107]
	v_mfma_f32_16x16x32_f16 v[108:111], v[172:175], v[48:51], v[108:111]
	ds_read_b128 v[160:163], v215 offset:16384
	ds_read_b128 v[164:167], v215 offset:20480
	ds_read_b128 v[168:171], v215 offset:24576
	ds_read_b128 v[172:175], v215 offset:28672
	s_waitcnt lgkmcnt(4)
	v_mfma_f32_16x16x32_f16 v[96:99], v[144:147], v[52:55], v[96:99]
	v_mfma_f32_16x16x32_f16 v[100:103], v[148:151], v[52:55], v[100:103]
	v_mfma_f32_16x16x32_f16 v[104:107], v[152:155], v[52:55], v[104:107]
	v_mfma_f32_16x16x32_f16 v[108:111], v[156:159], v[52:55], v[108:111]
	s_waitcnt lgkmcnt(0)
	v_mfma_f32_16x16x32_f16 v[96:99], v[160:163], v[56:59], v[96:99]
	v_mfma_f32_16x16x32_f16 v[100:103], v[164:167], v[56:59], v[100:103]
	v_mfma_f32_16x16x32_f16 v[104:107], v[168:171], v[56:59], v[104:107]
	v_mfma_f32_16x16x32_f16 v[108:111], v[172:175], v[56:59], v[108:111]
	v_mul_f32_e32 v189, 0x3fb8aa3b, v189
	s_cmp_lt_u32 s42, 0
	s_cbranch_scc1 .Lmy_s2_kend19
	s_cmp_eq_u32 s42, 0
	s_cbranch_scc1 .Lmy_s2_diag20
	ds_read_b128 v[176:179], v221 offset:49664
	ds_read_b128 v[180:183], v221 offset:49680
	ds_read_b32 v188, v221 offset:49152
	ds_read_b128 v[160:163], v212 offset:0
	ds_read_b128 v[164:167], v212 offset:4096
	ds_read_b128 v[168:171], v212 offset:8192
	ds_read_b128 v[172:175], v212 offset:12288
	s_waitcnt lgkmcnt(4)
	v_fma_f32 v188, v188, s51, v189
	v_exp_f32_e32 v188, v188
	s_nop 0
	v_mul_f32_e32 v176, v188, v176
	v_mul_f32_e32 v177, v188, v177
	v_mul_f32_e32 v178, v188, v178
	v_mul_f32_e32 v179, v188, v179
	v_mul_f32_e32 v180, v188, v180
	v_mul_f32_e32 v181, v188, v181
	v_mul_f32_e32 v182, v188, v182
	v_mul_f32_e32 v183, v188, v183
	v_mul_f32_e32 v176, v60, v176
	v_mul_f32_e32 v177, v61, v177
	v_mul_f32_e32 v178, v62, v178
	v_mul_f32_e32 v179, v63, v179
	v_mul_f32_e32 v180, v64, v180
	v_mul_f32_e32 v181, v65, v181
	v_mul_f32_e32 v182, v66, v182
	v_mul_f32_e32 v183, v67, v183
	v_cvt_pk_f16_f32 v184, v176, v177
	v_cvt_pk_f16_f32 v185, v178, v179
	v_cvt_pk_f16_f32 v186, v180, v181
	v_cvt_pk_f16_f32 v187, v182, v183
	s_waitcnt lgkmcnt(0)
	s_nop 0
	v_mfma_f32_16x16x32_f16 v[112:115], v[160:163], v[184:187], v[112:115]
	v_mfma_f32_16x16x32_f16 v[116:119], v[164:167], v[184:187], v[116:119]
	v_mfma_f32_16x16x32_f16 v[120:123], v[168:171], v[184:187], v[120:123]
	v_mfma_f32_16x16x32_f16 v[124:127], v[172:175], v[184:187], v[124:127]
	s_branch .Lmy_s2_knext21
.Lmy_s2_diag20:
	ds_read_b128 v[176:179], v221 offset:49664
	ds_read_b128 v[180:183], v221 offset:49680
	ds_read_b32 v188, v221 offset:49152
	ds_read_b128 v[160:163], v212 offset:0
	ds_read_b128 v[164:167], v212 offset:4096
	ds_read_b128 v[168:171], v212 offset:8192
	ds_read_b128 v[172:175], v212 offset:12288
	s_waitcnt lgkmcnt(4)
	v_fma_f32 v188, v188, s51, v189
	v_exp_f32_e32 v188, v188
	s_nop 0
	v_mul_f32_e32 v176, v188, v176
	v_mul_f32_e32 v177, v188, v177
	v_mul_f32_e32 v178, v188, v178
	v_mul_f32_e32 v179, v188, v179
	v_mul_f32_e32 v180, v188, v180
	v_mul_f32_e32 v181, v188, v181
	v_mul_f32_e32 v182, v188, v182
	v_mul_f32_e32 v183, v188, v183
	v_mul_f32_e32 v176, v60, v176
	v_mul_f32_e32 v177, v61, v177
	v_mul_f32_e32 v178, v62, v178
	v_mul_f32_e32 v179, v63, v179
	v_mul_f32_e32 v180, v64, v180
	v_mul_f32_e32 v181, v65, v181
	v_mul_f32_e32 v182, v66, v182
	v_mul_f32_e32 v183, v67, v183
	v_cndmask_b32_e64 v176, 0, v176, s[52:53]
	v_cndmask_b32_e64 v177, 0, v177, s[54:55]
	v_cndmask_b32_e64 v178, 0, v178, s[56:57]
	v_cndmask_b32_e64 v179, 0, v179, s[58:59]
	v_cndmask_b32_e64 v180, 0, v180, s[60:61]
	v_cndmask_b32_e64 v181, 0, v181, s[62:63]
	v_cndmask_b32_e64 v182, 0, v182, s[64:65]
	v_cndmask_b32_e64 v183, 0, v183, s[66:67]
	v_cvt_pk_f16_f32 v184, v176, v177
	v_cvt_pk_f16_f32 v185, v178, v179
	v_cvt_pk_f16_f32 v186, v180, v181
	v_cvt_pk_f16_f32 v187, v182, v183
	s_waitcnt lgkmcnt(0)
	s_nop 0
	v_mfma_f32_16x16x32_f16 v[112:115], v[160:163], v[184:187], v[112:115]
	v_mfma_f32_16x16x32_f16 v[116:119], v[164:167], v[184:187], v[116:119]
	v_mfma_f32_16x16x32_f16 v[120:123], v[168:171], v[184:187], v[120:123]
	v_mfma_f32_16x16x32_f16 v[124:127], v[172:175], v[184:187], v[124:127]
	v_mfma_f32_16x16x32_f16 v[128:131], v[160:163], v[92:95], 0
	v_mfma_f32_16x16x32_f16 v[132:135], v[164:167], v[92:95], 0
	v_mfma_f32_16x16x32_f16 v[136:139], v[168:171], v[92:95], 0
	v_mfma_f32_16x16x32_f16 v[140:143], v[172:175], v[92:95], 0
	s_branch .Lmy_s2_kend19
.Lmy_s2_knext21:
	s_cmp_lt_u32 s42, 1
	s_cbranch_scc1 .Lmy_s2_kend19
	s_cmp_eq_u32 s42, 1
	s_cbranch_scc1 .Lmy_s2_diag22
	ds_read_b128 v[176:179], v221 offset:49792
	ds_read_b128 v[180:183], v221 offset:49808
	ds_read_b32 v188, v221 offset:49280
	ds_read_b128 v[160:163], v213 offset:0
	ds_read_b128 v[164:167], v213 offset:4096
	ds_read_b128 v[168:171], v213 offset:8192
	ds_read_b128 v[172:175], v213 offset:12288
	s_waitcnt lgkmcnt(4)
	v_fma_f32 v188, v188, s51, v189
	v_exp_f32_e32 v188, v188
	s_nop 0
	v_mul_f32_e32 v176, v188, v176
	v_mul_f32_e32 v177, v188, v177
	v_mul_f32_e32 v178, v188, v178
	v_mul_f32_e32 v179, v188, v179
	v_mul_f32_e32 v180, v188, v180
	v_mul_f32_e32 v181, v188, v181
	v_mul_f32_e32 v182, v188, v182
	v_mul_f32_e32 v183, v188, v183
	v_mul_f32_e32 v176, v68, v176
	v_mul_f32_e32 v177, v69, v177
	v_mul_f32_e32 v178, v70, v178
	v_mul_f32_e32 v179, v71, v179
	v_mul_f32_e32 v180, v72, v180
	v_mul_f32_e32 v181, v73, v181
	v_mul_f32_e32 v182, v74, v182
	v_mul_f32_e32 v183, v75, v183
	v_cvt_pk_f16_f32 v184, v176, v177
	v_cvt_pk_f16_f32 v185, v178, v179
	v_cvt_pk_f16_f32 v186, v180, v181
	v_cvt_pk_f16_f32 v187, v182, v183
	s_waitcnt lgkmcnt(0)
	s_nop 0
	v_mfma_f32_16x16x32_f16 v[112:115], v[160:163], v[184:187], v[112:115]
	v_mfma_f32_16x16x32_f16 v[116:119], v[164:167], v[184:187], v[116:119]
	v_mfma_f32_16x16x32_f16 v[120:123], v[168:171], v[184:187], v[120:123]
	v_mfma_f32_16x16x32_f16 v[124:127], v[172:175], v[184:187], v[124:127]
	s_branch .Lmy_s2_knext23
.Lmy_s2_diag22:
	ds_read_b128 v[176:179], v221 offset:49792
	ds_read_b128 v[180:183], v221 offset:49808
	ds_read_b32 v188, v221 offset:49280
	ds_read_b128 v[160:163], v213 offset:0
	ds_read_b128 v[164:167], v213 offset:4096
	ds_read_b128 v[168:171], v213 offset:8192
	ds_read_b128 v[172:175], v213 offset:12288
	s_waitcnt lgkmcnt(4)
	v_fma_f32 v188, v188, s51, v189
	v_exp_f32_e32 v188, v188
	s_nop 0
	v_mul_f32_e32 v176, v188, v176
	v_mul_f32_e32 v177, v188, v177
	v_mul_f32_e32 v178, v188, v178
	v_mul_f32_e32 v179, v188, v179
	v_mul_f32_e32 v180, v188, v180
	v_mul_f32_e32 v181, v188, v181
	v_mul_f32_e32 v182, v188, v182
	v_mul_f32_e32 v183, v188, v183
	v_mul_f32_e32 v176, v68, v176
	v_mul_f32_e32 v177, v69, v177
	v_mul_f32_e32 v178, v70, v178
	v_mul_f32_e32 v179, v71, v179
	v_mul_f32_e32 v180, v72, v180
	v_mul_f32_e32 v181, v73, v181
	v_mul_f32_e32 v182, v74, v182
	v_mul_f32_e32 v183, v75, v183
	v_cndmask_b32_e64 v176, 0, v176, s[52:53]
	v_cndmask_b32_e64 v177, 0, v177, s[54:55]
	v_cndmask_b32_e64 v178, 0, v178, s[56:57]
	v_cndmask_b32_e64 v179, 0, v179, s[58:59]
	v_cndmask_b32_e64 v180, 0, v180, s[60:61]
	v_cndmask_b32_e64 v181, 0, v181, s[62:63]
	v_cndmask_b32_e64 v182, 0, v182, s[64:65]
	v_cndmask_b32_e64 v183, 0, v183, s[66:67]
	v_cvt_pk_f16_f32 v184, v176, v177
	v_cvt_pk_f16_f32 v185, v178, v179
	v_cvt_pk_f16_f32 v186, v180, v181
	v_cvt_pk_f16_f32 v187, v182, v183
	s_waitcnt lgkmcnt(0)
	s_nop 0
	v_mfma_f32_16x16x32_f16 v[112:115], v[160:163], v[184:187], v[112:115]
	v_mfma_f32_16x16x32_f16 v[116:119], v[164:167], v[184:187], v[116:119]
	v_mfma_f32_16x16x32_f16 v[120:123], v[168:171], v[184:187], v[120:123]
	v_mfma_f32_16x16x32_f16 v[124:127], v[172:175], v[184:187], v[124:127]
	v_mfma_f32_16x16x32_f16 v[128:131], v[160:163], v[92:95], 0
	v_mfma_f32_16x16x32_f16 v[132:135], v[164:167], v[92:95], 0
	v_mfma_f32_16x16x32_f16 v[136:139], v[168:171], v[92:95], 0
	v_mfma_f32_16x16x32_f16 v[140:143], v[172:175], v[92:95], 0
	s_branch .Lmy_s2_kend19
.Lmy_s2_knext23:
	s_cmp_lt_u32 s42, 2
	s_cbranch_scc1 .Lmy_s2_kend19
	s_cmp_eq_u32 s42, 2
	s_cbranch_scc1 .Lmy_s2_diag24
	ds_read_b128 v[176:179], v221 offset:49920
	ds_read_b128 v[180:183], v221 offset:49936
	ds_read_b32 v188, v221 offset:49408
	ds_read_b128 v[160:163], v214 offset:0
	ds_read_b128 v[164:167], v214 offset:4096
	ds_read_b128 v[168:171], v214 offset:8192
	ds_read_b128 v[172:175], v214 offset:12288
	s_waitcnt lgkmcnt(4)
	v_fma_f32 v188, v188, s51, v189
	v_exp_f32_e32 v188, v188
	s_nop 0
	v_mul_f32_e32 v176, v188, v176
	v_mul_f32_e32 v177, v188, v177
	v_mul_f32_e32 v178, v188, v178
	v_mul_f32_e32 v179, v188, v179
	v_mul_f32_e32 v180, v188, v180
	v_mul_f32_e32 v181, v188, v181
	v_mul_f32_e32 v182, v188, v182
	v_mul_f32_e32 v183, v188, v183
	v_mul_f32_e32 v176, v76, v176
	v_mul_f32_e32 v177, v77, v177
	v_mul_f32_e32 v178, v78, v178
	v_mul_f32_e32 v179, v79, v179
	v_mul_f32_e32 v180, v80, v180
	v_mul_f32_e32 v181, v81, v181
	v_mul_f32_e32 v182, v82, v182
	v_mul_f32_e32 v183, v83, v183
	v_cvt_pk_f16_f32 v184, v176, v177
	v_cvt_pk_f16_f32 v185, v178, v179
	v_cvt_pk_f16_f32 v186, v180, v181
	v_cvt_pk_f16_f32 v187, v182, v183
	s_waitcnt lgkmcnt(0)
	s_nop 0
	v_mfma_f32_16x16x32_f16 v[112:115], v[160:163], v[184:187], v[112:115]
	v_mfma_f32_16x16x32_f16 v[116:119], v[164:167], v[184:187], v[116:119]
	v_mfma_f32_16x16x32_f16 v[120:123], v[168:171], v[184:187], v[120:123]
	v_mfma_f32_16x16x32_f16 v[124:127], v[172:175], v[184:187], v[124:127]
	s_branch .Lmy_s2_knext25
.Lmy_s2_diag24:
	ds_read_b128 v[176:179], v221 offset:49920
	ds_read_b128 v[180:183], v221 offset:49936
	ds_read_b32 v188, v221 offset:49408
	ds_read_b128 v[160:163], v214 offset:0
	ds_read_b128 v[164:167], v214 offset:4096
	ds_read_b128 v[168:171], v214 offset:8192
	ds_read_b128 v[172:175], v214 offset:12288
	s_waitcnt lgkmcnt(4)
	v_fma_f32 v188, v188, s51, v189
	v_exp_f32_e32 v188, v188
	s_nop 0
	v_mul_f32_e32 v176, v188, v176
	v_mul_f32_e32 v177, v188, v177
	v_mul_f32_e32 v178, v188, v178
	v_mul_f32_e32 v179, v188, v179
	v_mul_f32_e32 v180, v188, v180
	v_mul_f32_e32 v181, v188, v181
	v_mul_f32_e32 v182, v188, v182
	v_mul_f32_e32 v183, v188, v183
	v_mul_f32_e32 v176, v76, v176
	v_mul_f32_e32 v177, v77, v177
	v_mul_f32_e32 v178, v78, v178
	v_mul_f32_e32 v179, v79, v179
	v_mul_f32_e32 v180, v80, v180
	v_mul_f32_e32 v181, v81, v181
	v_mul_f32_e32 v182, v82, v182
	v_mul_f32_e32 v183, v83, v183
	v_cndmask_b32_e64 v176, 0, v176, s[52:53]
	v_cndmask_b32_e64 v177, 0, v177, s[54:55]
	v_cndmask_b32_e64 v178, 0, v178, s[56:57]
	v_cndmask_b32_e64 v179, 0, v179, s[58:59]
	v_cndmask_b32_e64 v180, 0, v180, s[60:61]
	v_cndmask_b32_e64 v181, 0, v181, s[62:63]
	v_cndmask_b32_e64 v182, 0, v182, s[64:65]
	v_cndmask_b32_e64 v183, 0, v183, s[66:67]
	v_cvt_pk_f16_f32 v184, v176, v177
	v_cvt_pk_f16_f32 v185, v178, v179
	v_cvt_pk_f16_f32 v186, v180, v181
	v_cvt_pk_f16_f32 v187, v182, v183
	s_waitcnt lgkmcnt(0)
	s_nop 0
	v_mfma_f32_16x16x32_f16 v[112:115], v[160:163], v[184:187], v[112:115]
	v_mfma_f32_16x16x32_f16 v[116:119], v[164:167], v[184:187], v[116:119]
	v_mfma_f32_16x16x32_f16 v[120:123], v[168:171], v[184:187], v[120:123]
	v_mfma_f32_16x16x32_f16 v[124:127], v[172:175], v[184:187], v[124:127]
	v_mfma_f32_16x16x32_f16 v[128:131], v[160:163], v[92:95], 0
	v_mfma_f32_16x16x32_f16 v[132:135], v[164:167], v[92:95], 0
	v_mfma_f32_16x16x32_f16 v[136:139], v[168:171], v[92:95], 0
	v_mfma_f32_16x16x32_f16 v[140:143], v[172:175], v[92:95], 0
	s_branch .Lmy_s2_kend19
.Lmy_s2_knext25:
	s_cmp_lt_u32 s42, 3
	s_cbranch_scc1 .Lmy_s2_kend19
	s_cmp_eq_u32 s42, 3
	s_cbranch_scc1 .Lmy_s2_diag26
	ds_read_b128 v[176:179], v221 offset:50048
	ds_read_b128 v[180:183], v221 offset:50064
	ds_read_b32 v188, v221 offset:49536
	ds_read_b128 v[160:163], v215 offset:0
	ds_read_b128 v[164:167], v215 offset:4096
	ds_read_b128 v[168:171], v215 offset:8192
	ds_read_b128 v[172:175], v215 offset:12288
	s_waitcnt lgkmcnt(4)
	v_fma_f32 v188, v188, s51, v189
	v_exp_f32_e32 v188, v188
	s_nop 0
	v_mul_f32_e32 v176, v188, v176
	v_mul_f32_e32 v177, v188, v177
	v_mul_f32_e32 v178, v188, v178
	v_mul_f32_e32 v179, v188, v179
	v_mul_f32_e32 v180, v188, v180
	v_mul_f32_e32 v181, v188, v181
	v_mul_f32_e32 v182, v188, v182
	v_mul_f32_e32 v183, v188, v183
	v_mul_f32_e32 v176, v84, v176
	v_mul_f32_e32 v177, v85, v177
	v_mul_f32_e32 v178, v86, v178
	v_mul_f32_e32 v179, v87, v179
	v_mul_f32_e32 v180, v88, v180
	v_mul_f32_e32 v181, v89, v181
	v_mul_f32_e32 v182, v90, v182
	v_mul_f32_e32 v183, v91, v183
	v_cvt_pk_f16_f32 v184, v176, v177
	v_cvt_pk_f16_f32 v185, v178, v179
	v_cvt_pk_f16_f32 v186, v180, v181
	v_cvt_pk_f16_f32 v187, v182, v183
	s_waitcnt lgkmcnt(0)
	s_nop 0
	v_mfma_f32_16x16x32_f16 v[112:115], v[160:163], v[184:187], v[112:115]
	v_mfma_f32_16x16x32_f16 v[116:119], v[164:167], v[184:187], v[116:119]
	v_mfma_f32_16x16x32_f16 v[120:123], v[168:171], v[184:187], v[120:123]
	v_mfma_f32_16x16x32_f16 v[124:127], v[172:175], v[184:187], v[124:127]
	s_branch .Lmy_s2_knext27
.Lmy_s2_diag26:
	ds_read_b128 v[176:179], v221 offset:50048
	ds_read_b128 v[180:183], v221 offset:50064
	ds_read_b32 v188, v221 offset:49536
	ds_read_b128 v[160:163], v215 offset:0
	ds_read_b128 v[164:167], v215 offset:4096
	ds_read_b128 v[168:171], v215 offset:8192
	ds_read_b128 v[172:175], v215 offset:12288
	s_waitcnt lgkmcnt(4)
	v_fma_f32 v188, v188, s51, v189
	v_exp_f32_e32 v188, v188
	s_nop 0
	v_mul_f32_e32 v176, v188, v176
	v_mul_f32_e32 v177, v188, v177
	v_mul_f32_e32 v178, v188, v178
	v_mul_f32_e32 v179, v188, v179
	v_mul_f32_e32 v180, v188, v180
	v_mul_f32_e32 v181, v188, v181
	v_mul_f32_e32 v182, v188, v182
	v_mul_f32_e32 v183, v188, v183
	v_mul_f32_e32 v176, v84, v176
	v_mul_f32_e32 v177, v85, v177
	v_mul_f32_e32 v178, v86, v178
	v_mul_f32_e32 v179, v87, v179
	v_mul_f32_e32 v180, v88, v180
	v_mul_f32_e32 v181, v89, v181
	v_mul_f32_e32 v182, v90, v182
	v_mul_f32_e32 v183, v91, v183
	v_cndmask_b32_e64 v176, 0, v176, s[52:53]
	v_cndmask_b32_e64 v177, 0, v177, s[54:55]
	v_cndmask_b32_e64 v178, 0, v178, s[56:57]
	v_cndmask_b32_e64 v179, 0, v179, s[58:59]
	v_cndmask_b32_e64 v180, 0, v180, s[60:61]
	v_cndmask_b32_e64 v181, 0, v181, s[62:63]
	v_cndmask_b32_e64 v182, 0, v182, s[64:65]
	v_cndmask_b32_e64 v183, 0, v183, s[66:67]
	v_cvt_pk_f16_f32 v184, v176, v177
	v_cvt_pk_f16_f32 v185, v178, v179
	v_cvt_pk_f16_f32 v186, v180, v181
	v_cvt_pk_f16_f32 v187, v182, v183
	s_waitcnt lgkmcnt(0)
	s_nop 0
	v_mfma_f32_16x16x32_f16 v[112:115], v[160:163], v[184:187], v[112:115]
	v_mfma_f32_16x16x32_f16 v[116:119], v[164:167], v[184:187], v[116:119]
	v_mfma_f32_16x16x32_f16 v[120:123], v[168:171], v[184:187], v[120:123]
	v_mfma_f32_16x16x32_f16 v[124:127], v[172:175], v[184:187], v[124:127]
	v_mfma_f32_16x16x32_f16 v[128:131], v[160:163], v[92:95], 0
	v_mfma_f32_16x16x32_f16 v[132:135], v[164:167], v[92:95], 0
	v_mfma_f32_16x16x32_f16 v[136:139], v[168:171], v[92:95], 0
	v_mfma_f32_16x16x32_f16 v[140:143], v[172:175], v[92:95], 0
	s_branch .Lmy_s2_kend19
.Lmy_s2_knext27:
.Lmy_s2_kend19:
	v_readlane_b32 s46, v11, 2
	v_readlane_b32 s47, v12, 2
	v_exp_f32_e32 v190, v189
	ds_read_b64 v[176:177], v216 offset:32768
	ds_read_b64 v[178:179], v217 offset:32768
	ds_read_b64 v[180:181], v218 offset:32768
	ds_read_b64 v[182:183], v219 offset:32768
	s_waitcnt lgkmcnt(0)
	s_nop 4
	v_cvt_f32_f16_e32 v198, v176
	v_cvt_f32_f16_sdwa v199, v176 dst_sel:DWORD dst_unused:UNUSED_PAD src0_sel:WORD_1
	v_cvt_f32_f16_e32 v200, v177
	v_cvt_f32_f16_sdwa v201, v177 dst_sel:DWORD dst_unused:UNUSED_PAD src0_sel:WORD_1
	v_fma_f32 v192, v190, v96, v112
	v_fma_f32 v193, v190, v97, v113
	v_fma_f32 v194, v190, v98, v114
	v_fma_f32 v195, v190, v99, v115
	v_mul_f32_e32 v192, s47, v192
	v_mul_f32_e32 v193, s47, v193
	v_mul_f32_e32 v194, s47, v194
	v_mul_f32_e32 v195, s47, v195
	v_fma_f32 v192, s46, v128, v192
	v_fma_f32 v193, s46, v129, v193
	v_fma_f32 v194, s46, v130, v194
	v_fma_f32 v195, s46, v131, v195
	v_mul_f32_e32 v192, v192, v198
	v_mul_f32_e32 v193, v193, v199
	v_mul_f32_e32 v194, v194, v200
	v_mul_f32_e32 v195, v195, v201
	v_fma_f32 v13, v192, v192, v13
	v_fma_f32 v13, v193, v193, v13
	v_fma_f32 v13, v194, v194, v13
	v_fma_f32 v13, v195, v195, v13
	v_mul_f32_e32 v192, 0x41800000, v192
	v_mul_f32_e32 v193, 0x41800000, v193
	v_mul_f32_e32 v194, 0x41800000, v194
	v_mul_f32_e32 v195, 0x41800000, v195
	v_cvt_pk_f16_f32 v196, v192, v193
	v_cvt_pk_f16_f32 v197, v194, v195
	ds_write_b64 v216, v[196:197] offset:32768
	v_cvt_f32_f16_e32 v198, v178
	v_cvt_f32_f16_sdwa v199, v178 dst_sel:DWORD dst_unused:UNUSED_PAD src0_sel:WORD_1
	v_cvt_f32_f16_e32 v200, v179
	v_cvt_f32_f16_sdwa v201, v179 dst_sel:DWORD dst_unused:UNUSED_PAD src0_sel:WORD_1
	v_fma_f32 v192, v190, v100, v116
	v_fma_f32 v193, v190, v101, v117
	v_fma_f32 v194, v190, v102, v118
	v_fma_f32 v195, v190, v103, v119
	v_mul_f32_e32 v192, s47, v192
	v_mul_f32_e32 v193, s47, v193
	v_mul_f32_e32 v194, s47, v194
	v_mul_f32_e32 v195, s47, v195
	v_fma_f32 v192, s46, v132, v192
	v_fma_f32 v193, s46, v133, v193
	v_fma_f32 v194, s46, v134, v194
	v_fma_f32 v195, s46, v135, v195
	v_mul_f32_e32 v192, v192, v198
	v_mul_f32_e32 v193, v193, v199
	v_mul_f32_e32 v194, v194, v200
	v_mul_f32_e32 v195, v195, v201
	v_fma_f32 v13, v192, v192, v13
	v_fma_f32 v13, v193, v193, v13
	v_fma_f32 v13, v194, v194, v13
	v_fma_f32 v13, v195, v195, v13
	v_mul_f32_e32 v192, 0x41800000, v192
	v_mul_f32_e32 v193, 0x41800000, v193
	v_mul_f32_e32 v194, 0x41800000, v194
	v_mul_f32_e32 v195, 0x41800000, v195
	v_cvt_pk_f16_f32 v196, v192, v193
	v_cvt_pk_f16_f32 v197, v194, v195
	ds_write_b64 v217, v[196:197] offset:32768
	v_cvt_f32_f16_e32 v198, v180
	v_cvt_f32_f16_sdwa v199, v180 dst_sel:DWORD dst_unused:UNUSED_PAD src0_sel:WORD_1
	v_cvt_f32_f16_e32 v200, v181
	v_cvt_f32_f16_sdwa v201, v181 dst_sel:DWORD dst_unused:UNUSED_PAD src0_sel:WORD_1
	v_fma_f32 v192, v190, v104, v120
	v_fma_f32 v193, v190, v105, v121
	v_fma_f32 v194, v190, v106, v122
	v_fma_f32 v195, v190, v107, v123
	v_mul_f32_e32 v192, s47, v192
	v_mul_f32_e32 v193, s47, v193
	v_mul_f32_e32 v194, s47, v194
	v_mul_f32_e32 v195, s47, v195
	v_fma_f32 v192, s46, v136, v192
	v_fma_f32 v193, s46, v137, v193
	v_fma_f32 v194, s46, v138, v194
	v_fma_f32 v195, s46, v139, v195
	v_mul_f32_e32 v192, v192, v198
	v_mul_f32_e32 v193, v193, v199
	v_mul_f32_e32 v194, v194, v200
	v_mul_f32_e32 v195, v195, v201
	v_fma_f32 v13, v192, v192, v13
	v_fma_f32 v13, v193, v193, v13
	v_fma_f32 v13, v194, v194, v13
	v_fma_f32 v13, v195, v195, v13
	v_mul_f32_e32 v192, 0x41800000, v192
	v_mul_f32_e32 v193, 0x41800000, v193
	v_mul_f32_e32 v194, 0x41800000, v194
	v_mul_f32_e32 v195, 0x41800000, v195
	v_cvt_pk_f16_f32 v196, v192, v193
	v_cvt_pk_f16_f32 v197, v194, v195
	ds_write_b64 v218, v[196:197] offset:32768
	v_cvt_f32_f16_e32 v198, v182
	v_cvt_f32_f16_sdwa v199, v182 dst_sel:DWORD dst_unused:UNUSED_PAD src0_sel:WORD_1
	v_cvt_f32_f16_e32 v200, v183
	v_cvt_f32_f16_sdwa v201, v183 dst_sel:DWORD dst_unused:UNUSED_PAD src0_sel:WORD_1
	v_fma_f32 v192, v190, v108, v124
	v_fma_f32 v193, v190, v109, v125
	v_fma_f32 v194, v190, v110, v126
	v_fma_f32 v195, v190, v111, v127
	v_mul_f32_e32 v192, s47, v192
	v_mul_f32_e32 v193, s47, v193
	v_mul_f32_e32 v194, s47, v194
	v_mul_f32_e32 v195, s47, v195
	v_fma_f32 v192, s46, v140, v192
	v_fma_f32 v193, s46, v141, v193
	v_fma_f32 v194, s46, v142, v194
	v_fma_f32 v195, s46, v143, v195
	v_mul_f32_e32 v192, v192, v198
	v_mul_f32_e32 v193, v193, v199
	v_mul_f32_e32 v194, v194, v200
	v_mul_f32_e32 v195, v195, v201
	v_fma_f32 v13, v192, v192, v13
	v_fma_f32 v13, v193, v193, v13
	v_fma_f32 v13, v194, v194, v13
	v_fma_f32 v13, v195, v195, v13
	v_mul_f32_e32 v192, 0x41800000, v192
	v_mul_f32_e32 v193, 0x41800000, v193
	v_mul_f32_e32 v194, 0x41800000, v194
	v_mul_f32_e32 v195, 0x41800000, v195
	v_cvt_pk_f16_f32 v196, v192, v193
	v_cvt_pk_f16_f32 v197, v194, v195
	ds_write_b64 v219, v[196:197] offset:32768
	s_waitcnt lgkmcnt(0)
	s_barrier
	ds_read_b128 v[204:207], v34 offset:32768
	ds_read_b128 v[208:211], v35 offset:32768
	s_waitcnt lgkmcnt(0)
	global_store_dwordx4 v8, v[204:207], s[38:39]
	global_store_dwordx4 v9, v[208:211], s[38:39]
	s_add_u32 s38, s38, 0x80
	s_addc_u32 s39, s39, 0
	s_add_u32 m0, s43, 0x19000
	s_nop 0
	global_load_lds_dwordx4 v4, s[30:31]
	s_add_u32 m0, s43, 0x1d000
	s_nop 0
	global_load_lds_dwordx4 v6, s[32:33]
	s_add_u32 m0, s43, 0x21000
	s_nop 0
	global_load_lds_dwordx4 v8, s[34:35]
	s_add_u32 m0, s43, 0x1b000
	s_nop 0
	global_load_lds_dwordx4 v5, s[30:31]
	s_add_u32 m0, s43, 0x1f000
	s_nop 0
	global_load_lds_dwordx4 v7, s[32:33]
	s_add_u32 m0, s43, 0x23000
	s_nop 0
	global_load_lds_dwordx4 v9, s[34:35]
	s_add_u32 m0, s44, 0x25000
	s_nop 0
	global_load_lds_dword v10, s[36:37]
	s_add_u32 s30, s30, 0x80000
	s_addc_u32 s31, s31, 0
	s_add_u32 s32, s32, 0x4000
	s_addc_u32 s33, s33, 0
	s_add_u32 s34, s34, 0x80
	s_addc_u32 s35, s35, 0
	s_add_u32 s36, s36, 0x4000
	s_addc_u32 s37, s37, 0
	s_waitcnt vmcnt(18)
	s_waitcnt lgkmcnt(0)
	s_barrier
	v_mov_b32_e32 v112, 0
	v_mov_b32_e32 v113, 0
	v_mov_b32_e32 v114, 0
	v_mov_b32_e32 v115, 0
	v_mov_b32_e32 v116, 0
	v_mov_b32_e32 v117, 0
	v_mov_b32_e32 v118, 0
	v_mov_b32_e32 v119, 0
	v_mov_b32_e32 v120, 0
	v_mov_b32_e32 v121, 0
	v_mov_b32_e32 v122, 0
	v_mov_b32_e32 v123, 0
	v_mov_b32_e32 v124, 0
	v_mov_b32_e32 v125, 0
	v_mov_b32_e32 v126, 0
	v_mov_b32_e32 v127, 0
	ds_read_b128 v[144:147], v16 offset:16384
	ds_read_b128 v[148:151], v16 offset:20480
	ds_read_b128 v[152:155], v16 offset:24576
	ds_read_b128 v[156:159], v16 offset:28672
	ds_read_b32 v189, v36 offset:49152
	ds_read_b128 v[160:163], v17 offset:16384
	ds_read_b128 v[164:167], v17 offset:20480
	ds_read_b128 v[168:171], v17 offset:24576
	ds_read_b128 v[172:175], v17 offset:28672
	s_waitcnt lgkmcnt(4)
	v_mfma_f32_16x16x32_f16 v[96:99], v[144:147], v[44:47], 0
	v_mfma_f32_16x16x32_f16 v[100:103], v[148:151], v[44:47], 0
	v_mfma_f32_16x16x32_f16 v[104:107], v[152:155], v[44:47], 0
	v_mfma_f32_16x16x32_f16 v[108:111], v[156:159], v[44:47], 0
	ds_read_b128 v[144:147], v18 offset:16384
	ds_read_b128 v[148:151], v18 offset:20480
	ds_read_b128 v[152:155], v18 offset:24576
	ds_read_b128 v[156:159], v18 offset:28672
	s_waitcnt lgkmcnt(4)
	v_mfma_f32_16x16x32_f16 v[96:99], v[160:163], v[48:51], v[96:99]
	v_mfma_f32_16x16x32_f16 v[100:103], v[164:167], v[48:51], v[100:103]
	v_mfma_f32_16x16x32_f16 v[104:107], v[168:171], v[48:51], v[104:107]
	v_mfma_f32_16x16x32_f16 v[108:111], v[172:175], v[48:51], v[108:111]
	ds_read_b128 v[160:163], v19 offset:16384
	ds_read_b128 v[164:167], v19 offset:20480
	ds_read_b128 v[168:171], v19 offset:24576
	ds_read_b128 v[172:175], v19 offset:28672
	s_waitcnt lgkmcnt(4)
	v_mfma_f32_16x16x32_f16 v[96:99], v[144:147], v[52:55], v[96:99]
	v_mfma_f32_16x16x32_f16 v[100:103], v[148:151], v[52:55], v[100:103]
	v_mfma_f32_16x16x32_f16 v[104:107], v[152:155], v[52:55], v[104:107]
	v_mfma_f32_16x16x32_f16 v[108:111], v[156:159], v[52:55], v[108:111]
	s_waitcnt lgkmcnt(0)
	v_mfma_f32_16x16x32_f16 v[96:99], v[160:163], v[56:59], v[96:99]
	v_mfma_f32_16x16x32_f16 v[100:103], v[164:167], v[56:59], v[100:103]
	v_mfma_f32_16x16x32_f16 v[104:107], v[168:171], v[56:59], v[104:107]
	v_mfma_f32_16x16x32_f16 v[108:111], v[172:175], v[56:59], v[108:111]
	v_mul_f32_e32 v189, 0x3fb8aa3b, v189
	s_cmp_lt_u32 s42, 0
	s_cbranch_scc1 .Lmy_s2_kend28
	s_cmp_eq_u32 s42, 0
	s_cbranch_scc1 .Lmy_s2_diag29
	ds_read_b128 v[176:179], v38 offset:49664
	ds_read_b128 v[180:183], v38 offset:49680
	ds_read_b32 v188, v38 offset:49152
	ds_read_b128 v[160:163], v16 offset:0
	ds_read_b128 v[164:167], v16 offset:4096
	ds_read_b128 v[168:171], v16 offset:8192
	ds_read_b128 v[172:175], v16 offset:12288
	s_waitcnt lgkmcnt(4)
	v_fma_f32 v188, v188, s51, v189
	v_exp_f32_e32 v188, v188
	s_nop 0
	v_mul_f32_e32 v176, v188, v176
	v_mul_f32_e32 v177, v188, v177
	v_mul_f32_e32 v178, v188, v178
	v_mul_f32_e32 v179, v188, v179
	v_mul_f32_e32 v180, v188, v180
	v_mul_f32_e32 v181, v188, v181
	v_mul_f32_e32 v182, v188, v182
	v_mul_f32_e32 v183, v188, v183
	v_mul_f32_e32 v176, v60, v176
	v_mul_f32_e32 v177, v61, v177
	v_mul_f32_e32 v178, v62, v178
	v_mul_f32_e32 v179, v63, v179
	v_mul_f32_e32 v180, v64, v180
	v_mul_f32_e32 v181, v65, v181
	v_mul_f32_e32 v182, v66, v182
	v_mul_f32_e32 v183, v67, v183
	v_cvt_pk_f16_f32 v184, v176, v177
	v_cvt_pk_f16_f32 v185, v178, v179
	v_cvt_pk_f16_f32 v186, v180, v181
	v_cvt_pk_f16_f32 v187, v182, v183
	s_waitcnt lgkmcnt(0)
	s_nop 0
	v_mfma_f32_16x16x32_f16 v[112:115], v[160:163], v[184:187], v[112:115]
	v_mfma_f32_16x16x32_f16 v[116:119], v[164:167], v[184:187], v[116:119]
	v_mfma_f32_16x16x32_f16 v[120:123], v[168:171], v[184:187], v[120:123]
	v_mfma_f32_16x16x32_f16 v[124:127], v[172:175], v[184:187], v[124:127]
	s_branch .Lmy_s2_knext30

.Lmy_s2_knext36:
.Lmy_s2_kend28:
	v_readlane_b32 s46, v11, 3
	v_readlane_b32 s47, v12, 3
	v_exp_f32_e32 v190, v189
	ds_read_b64 v[176:177], v24 offset:32768
	ds_read_b64 v[178:179], v25 offset:32768
	ds_read_b64 v[180:181], v26 offset:32768
	ds_read_b64 v[182:183], v27 offset:32768
	s_waitcnt lgkmcnt(0)
	s_nop 4
	v_cvt_f32_f16_e32 v198, v176
	v_cvt_f32_f16_sdwa v199, v176 dst_sel:DWORD dst_unused:UNUSED_PAD src0_sel:WORD_1
	v_cvt_f32_f16_e32 v200, v177
	v_cvt_f32_f16_sdwa v201, v177 dst_sel:DWORD dst_unused:UNUSED_PAD src0_sel:WORD_1
	v_fma_f32 v192, v190, v96, v112
	v_fma_f32 v193, v190, v97, v113
	v_fma_f32 v194, v190, v98, v114
	v_fma_f32 v195, v190, v99, v115
	v_mul_f32_e32 v192, s47, v192
	v_mul_f32_e32 v193, s47, v193
	v_mul_f32_e32 v194, s47, v194
	v_mul_f32_e32 v195, s47, v195
	v_fma_f32 v192, s46, v128, v192
	v_fma_f32 v193, s46, v129, v193
	v_fma_f32 v194, s46, v130, v194
	v_fma_f32 v195, s46, v131, v195
	v_mul_f32_e32 v192, v192, v198
	v_mul_f32_e32 v193, v193, v199
	v_mul_f32_e32 v194, v194, v200
	v_mul_f32_e32 v195, v195, v201
	v_fma_f32 v13, v192, v192, v13
	v_fma_f32 v13, v193, v193, v13
	v_fma_f32 v13, v194, v194, v13
	v_fma_f32 v13, v195, v195, v13
	v_mul_f32_e32 v192, 0x41800000, v192
	v_mul_f32_e32 v193, 0x41800000, v193
	v_mul_f32_e32 v194, 0x41800000, v194
	v_mul_f32_e32 v195, 0x41800000, v195
	v_cvt_pk_f16_f32 v196, v192, v193
	v_cvt_pk_f16_f32 v197, v194, v195
	ds_write_b64 v24, v[196:197] offset:32768
	v_cvt_f32_f16_e32 v198, v178
	v_cvt_f32_f16_sdwa v199, v178 dst_sel:DWORD dst_unused:UNUSED_PAD src0_sel:WORD_1
	v_cvt_f32_f16_e32 v200, v179
	v_cvt_f32_f16_sdwa v201, v179 dst_sel:DWORD dst_unused:UNUSED_PAD src0_sel:WORD_1
	v_fma_f32 v192, v190, v100, v116
	v_fma_f32 v193, v190, v101, v117
	v_fma_f32 v194, v190, v102, v118
	v_fma_f32 v195, v190, v103, v119
	v_mul_f32_e32 v192, s47, v192
	v_mul_f32_e32 v193, s47, v193
	v_mul_f32_e32 v194, s47, v194
	v_mul_f32_e32 v195, s47, v195
	v_fma_f32 v192, s46, v132, v192
	v_fma_f32 v193, s46, v133, v193
	v_fma_f32 v194, s46, v134, v194
	v_fma_f32 v195, s46, v135, v195
	v_mul_f32_e32 v192, v192, v198
	v_mul_f32_e32 v193, v193, v199
	v_mul_f32_e32 v194, v194, v200
	v_mul_f32_e32 v195, v195, v201
	v_fma_f32 v13, v192, v192, v13
	v_fma_f32 v13, v193, v193, v13
	v_fma_f32 v13, v194, v194, v13
	v_fma_f32 v13, v195, v195, v13
	v_mul_f32_e32 v192, 0x41800000, v192
	v_mul_f32_e32 v193, 0x41800000, v193
	v_mul_f32_e32 v194, 0x41800000, v194
	v_mul_f32_e32 v195, 0x41800000, v195
	v_cvt_pk_f16_f32 v196, v192, v193
	v_cvt_pk_f16_f32 v197, v194, v195
	ds_write_b64 v25, v[196:197] offset:32768
	v_cvt_f32_f16_e32 v198, v180
	v_cvt_f32_f16_sdwa v199, v180 dst_sel:DWORD dst_unused:UNUSED_PAD src0_sel:WORD_1
	v_cvt_f32_f16_e32 v200, v181
	v_cvt_f32_f16_sdwa v201, v181 dst_sel:DWORD dst_unused:UNUSED_PAD src0_sel:WORD_1
	v_fma_f32 v192, v190, v104, v120
	v_fma_f32 v193, v190, v105, v121
	v_fma_f32 v194, v190, v106, v122
	v_fma_f32 v195, v190, v107, v123
	v_mul_f32_e32 v192, s47, v192
	v_mul_f32_e32 v193, s47, v193
	v_mul_f32_e32 v194, s47, v194
	v_mul_f32_e32 v195, s47, v195
	v_fma_f32 v192, s46, v136, v192
	v_fma_f32 v193, s46, v137, v193
	v_fma_f32 v194, s46, v138, v194
	v_fma_f32 v195, s46, v139, v195
	v_mul_f32_e32 v192, v192, v198
	v_mul_f32_e32 v193, v193, v199
	v_mul_f32_e32 v194, v194, v200
	v_mul_f32_e32 v195, v195, v201
	v_fma_f32 v13, v192, v192, v13
	v_fma_f32 v13, v193, v193, v13
	v_fma_f32 v13, v194, v194, v13
	v_fma_f32 v13, v195, v195, v13
	v_mul_f32_e32 v192, 0x41800000, v192
	v_mul_f32_e32 v193, 0x41800000, v193
	v_mul_f32_e32 v194, 0x41800000, v194
	v_mul_f32_e32 v195, 0x41800000, v195
	v_cvt_pk_f16_f32 v196, v192, v193
	v_cvt_pk_f16_f32 v197, v194, v195
	ds_write_b64 v26, v[196:197] offset:32768
	v_cvt_f32_f16_e32 v198, v182
	v_cvt_f32_f16_sdwa v199, v182 dst_sel:DWORD dst_unused:UNUSED_PAD src0_sel:WORD_1
	v_cvt_f32_f16_e32 v200, v183
	v_cvt_f32_f16_sdwa v201, v183 dst_sel:DWORD dst_unused:UNUSED_PAD src0_sel:WORD_1
	v_fma_f32 v192, v190, v108, v124
	v_fma_f32 v193, v190, v109, v125
	v_fma_f32 v194, v190, v110, v126
	v_fma_f32 v195, v190, v111, v127
	v_mul_f32_e32 v192, s47, v192
	v_mul_f32_e32 v193, s47, v193
	v_mul_f32_e32 v194, s47, v194
	v_mul_f32_e32 v195, s47, v195
	v_fma_f32 v192, s46, v140, v192
	v_fma_f32 v193, s46, v141, v193
	v_fma_f32 v194, s46, v142, v194
	v_fma_f32 v195, s46, v143, v195
	v_mul_f32_e32 v192, v192, v198
	v_mul_f32_e32 v193, v193, v199
	v_mul_f32_e32 v194, v194, v200
	v_mul_f32_e32 v195, v195, v201
	v_fma_f32 v13, v192, v192, v13
	v_fma_f32 v13, v193, v193, v13
	v_fma_f32 v13, v194, v194, v13
	v_fma_f32 v13, v195, v195, v13
	v_mul_f32_e32 v192, 0x41800000, v192
	v_mul_f32_e32 v193, 0x41800000, v193
	v_mul_f32_e32 v194, 0x41800000, v194
	v_mul_f32_e32 v195, 0x41800000, v195
	v_cvt_pk_f16_f32 v196, v192, v193
	v_cvt_pk_f16_f32 v197, v194, v195
	ds_write_b64 v27, v[196:197] offset:32768
	s_waitcnt lgkmcnt(0)
	s_barrier
	ds_read_b128 v[204:207], v40 offset:32768
	ds_read_b128 v[208:211], v41 offset:32768
	s_waitcnt lgkmcnt(0)
	global_store_dwordx4 v8, v[204:207], s[38:39]
	global_store_dwordx4 v9, v[208:211], s[38:39]
	s_add_u32 s38, s38, 0x80
	s_addc_u32 s39, s39, 0
	s_add_u32 m0, s43, 0x0
	s_nop 0
	global_load_lds_dwordx4 v4, s[30:31]
	s_add_u32 m0, s43, 0x4000
	s_nop 0
	global_load_lds_dwordx4 v6, s[32:33]
	s_add_u32 m0, s43, 0x8000
	s_nop 0
	global_load_lds_dwordx4 v8, s[34:35]
	s_add_u32 m0, s43, 0x2000
	s_nop 0
	global_load_lds_dwordx4 v5, s[30:31]
	s_add_u32 m0, s43, 0x6000
	s_nop 0
	global_load_lds_dwordx4 v7, s[32:33]
	s_add_u32 m0, s43, 0xa000
	s_nop 0
	global_load_lds_dwordx4 v9, s[34:35]
	s_add_u32 m0, s44, 0xc000
	s_nop 0
	global_load_lds_dword v10, s[36:37]
	s_add_u32 s30, s30, 0x80000
	s_addc_u32 s31, s31, 0
	s_add_u32 s32, s32, 0x4000
	s_addc_u32 s33, s33, 0
	s_add_u32 s34, s34, 0x80
	s_addc_u32 s35, s35, 0
	s_add_u32 s36, s36, 0x4000
	s_addc_u32 s37, s37, 0
	s_waitcnt vmcnt(18)
	s_waitcnt lgkmcnt(0)
	s_barrier
	v_mov_b32_e32 v112, 0
	v_mov_b32_e32 v113, 0
	v_mov_b32_e32 v114, 0
	v_mov_b32_e32 v115, 0
	v_mov_b32_e32 v116, 0
	v_mov_b32_e32 v117, 0
	v_mov_b32_e32 v118, 0
	v_mov_b32_e32 v119, 0
	v_mov_b32_e32 v120, 0
	v_mov_b32_e32 v121, 0
	v_mov_b32_e32 v122, 0
	v_mov_b32_e32 v123, 0
	v_mov_b32_e32 v124, 0
	v_mov_b32_e32 v125, 0
	v_mov_b32_e32 v126, 0
	v_mov_b32_e32 v127, 0
	ds_read_b128 v[144:147], v20 offset:16384
	ds_read_b128 v[148:151], v20 offset:20480
	ds_read_b128 v[152:155], v20 offset:24576
	ds_read_b128 v[156:159], v20 offset:28672
	ds_read_b32 v189, v37 offset:49152
	ds_read_b128 v[160:163], v21 offset:16384
	ds_read_b128 v[164:167], v21 offset:20480
	ds_read_b128 v[168:171], v21 offset:24576
	ds_read_b128 v[172:175], v21 offset:28672
	s_waitcnt lgkmcnt(4)
	v_mfma_f32_16x16x32_f16 v[96:99], v[144:147], v[44:47], 0
	v_mfma_f32_16x16x32_f16 v[100:103], v[148:151], v[44:47], 0
	v_mfma_f32_16x16x32_f16 v[104:107], v[152:155], v[44:47], 0
	v_mfma_f32_16x16x32_f16 v[108:111], v[156:159], v[44:47], 0
	ds_read_b128 v[144:147], v22 offset:16384
	ds_read_b128 v[148:151], v22 offset:20480
	ds_read_b128 v[152:155], v22 offset:24576
	ds_read_b128 v[156:159], v22 offset:28672
	s_waitcnt lgkmcnt(4)
	v_mfma_f32_16x16x32_f16 v[96:99], v[160:163], v[48:51], v[96:99]
	v_mfma_f32_16x16x32_f16 v[100:103], v[164:167], v[48:51], v[100:103]
	v_mfma_f32_16x16x32_f16 v[104:107], v[168:171], v[48:51], v[104:107]
	v_mfma_f32_16x16x32_f16 v[108:111], v[172:175], v[48:51], v[108:111]
	ds_read_b128 v[160:163], v23 offset:16384
	ds_read_b128 v[164:167], v23 offset:20480
	ds_read_b128 v[168:171], v23 offset:24576
	ds_read_b128 v[172:175], v23 offset:28672
	s_waitcnt lgkmcnt(4)
	v_mfma_f32_16x16x32_f16 v[96:99], v[144:147], v[52:55], v[96:99]
	v_mfma_f32_16x16x32_f16 v[100:103], v[148:151], v[52:55], v[100:103]
	v_mfma_f32_16x16x32_f16 v[104:107], v[152:155], v[52:55], v[104:107]
	v_mfma_f32_16x16x32_f16 v[108:111], v[156:159], v[52:55], v[108:111]
	s_waitcnt lgkmcnt(0)
	v_mfma_f32_16x16x32_f16 v[96:99], v[160:163], v[56:59], v[96:99]
	v_mfma_f32_16x16x32_f16 v[100:103], v[164:167], v[56:59], v[100:103]
	v_mfma_f32_16x16x32_f16 v[104:107], v[168:171], v[56:59], v[104:107]
	v_mfma_f32_16x16x32_f16 v[108:111], v[172:175], v[56:59], v[108:111]
	v_mul_f32_e32 v189, 0x3fb8aa3b, v189
	s_cmp_lt_u32 s42, 0
	s_cbranch_scc1 .Lmy_s2_kend37
	s_cmp_eq_u32 s42, 0
	s_cbranch_scc1 .Lmy_s2_diag38
	ds_read_b128 v[176:179], v39 offset:49664
	ds_read_b128 v[180:183], v39 offset:49680
	ds_read_b32 v188, v39 offset:49152
	ds_read_b128 v[160:163], v20 offset:0
	ds_read_b128 v[164:167], v20 offset:4096
	ds_read_b128 v[168:171], v20 offset:8192
	ds_read_b128 v[172:175], v20 offset:12288
	s_waitcnt lgkmcnt(4)
	v_fma_f32 v188, v188, s51, v189
	v_exp_f32_e32 v188, v188
	s_nop 0
	v_mul_f32_e32 v176, v188, v176
	v_mul_f32_e32 v177, v188, v177
	v_mul_f32_e32 v178, v188, v178
	v_mul_f32_e32 v179, v188, v179
	v_mul_f32_e32 v180, v188, v180
	v_mul_f32_e32 v181, v188, v181
	v_mul_f32_e32 v182, v188, v182
	v_mul_f32_e32 v183, v188, v183
	v_mul_f32_e32 v176, v60, v176
	v_mul_f32_e32 v177, v61, v177
	v_mul_f32_e32 v178, v62, v178
	v_mul_f32_e32 v179, v63, v179
	v_mul_f32_e32 v180, v64, v180
	v_mul_f32_e32 v181, v65, v181
	v_mul_f32_e32 v182, v66, v182
	v_mul_f32_e32 v183, v67, v183
	v_cvt_pk_f16_f32 v184, v176, v177
	v_cvt_pk_f16_f32 v185, v178, v179
	v_cvt_pk_f16_f32 v186, v180, v181
	v_cvt_pk_f16_f32 v187, v182, v183
	s_waitcnt lgkmcnt(0)
	s_nop 0
	v_mfma_f32_16x16x32_f16 v[112:115], v[160:163], v[184:187], v[112:115]
	v_mfma_f32_16x16x32_f16 v[116:119], v[164:167], v[184:187], v[116:119]
	v_mfma_f32_16x16x32_f16 v[120:123], v[168:171], v[184:187], v[120:123]
	v_mfma_f32_16x16x32_f16 v[124:127], v[172:175], v[184:187], v[124:127]
	s_branch .Lmy_s2_knext39

.Lmy_s2_knext45:
.Lmy_s2_kend37:
	v_readlane_b32 s46, v11, 4
	v_readlane_b32 s47, v12, 4
	v_exp_f32_e32 v190, v189
	ds_read_b64 v[176:177], v28 offset:32768
	ds_read_b64 v[178:179], v29 offset:32768
	ds_read_b64 v[180:181], v30 offset:32768
	ds_read_b64 v[182:183], v31 offset:32768
	s_waitcnt lgkmcnt(0)
	s_nop 4
	v_cvt_f32_f16_e32 v198, v176
	v_cvt_f32_f16_sdwa v199, v176 dst_sel:DWORD dst_unused:UNUSED_PAD src0_sel:WORD_1
	v_cvt_f32_f16_e32 v200, v177
	v_cvt_f32_f16_sdwa v201, v177 dst_sel:DWORD dst_unused:UNUSED_PAD src0_sel:WORD_1
	v_fma_f32 v192, v190, v96, v112
	v_fma_f32 v193, v190, v97, v113
	v_fma_f32 v194, v190, v98, v114
	v_fma_f32 v195, v190, v99, v115
	v_mul_f32_e32 v192, s47, v192
	v_mul_f32_e32 v193, s47, v193
	v_mul_f32_e32 v194, s47, v194
	v_mul_f32_e32 v195, s47, v195
	v_fma_f32 v192, s46, v128, v192
	v_fma_f32 v193, s46, v129, v193
	v_fma_f32 v194, s46, v130, v194
	v_fma_f32 v195, s46, v131, v195
	v_mul_f32_e32 v192, v192, v198
	v_mul_f32_e32 v193, v193, v199
	v_mul_f32_e32 v194, v194, v200
	v_mul_f32_e32 v195, v195, v201
	v_fma_f32 v13, v192, v192, v13
	v_fma_f32 v13, v193, v193, v13
	v_fma_f32 v13, v194, v194, v13
	v_fma_f32 v13, v195, v195, v13
	v_mul_f32_e32 v192, 0x41800000, v192
	v_mul_f32_e32 v193, 0x41800000, v193
	v_mul_f32_e32 v194, 0x41800000, v194
	v_mul_f32_e32 v195, 0x41800000, v195
	v_cvt_pk_f16_f32 v196, v192, v193
	v_cvt_pk_f16_f32 v197, v194, v195
	ds_write_b64 v28, v[196:197] offset:32768
	v_cvt_f32_f16_e32 v198, v178
	v_cvt_f32_f16_sdwa v199, v178 dst_sel:DWORD dst_unused:UNUSED_PAD src0_sel:WORD_1
	v_cvt_f32_f16_e32 v200, v179
	v_cvt_f32_f16_sdwa v201, v179 dst_sel:DWORD dst_unused:UNUSED_PAD src0_sel:WORD_1
	v_fma_f32 v192, v190, v100, v116
	v_fma_f32 v193, v190, v101, v117
	v_fma_f32 v194, v190, v102, v118
	v_fma_f32 v195, v190, v103, v119
	v_mul_f32_e32 v192, s47, v192
	v_mul_f32_e32 v193, s47, v193
	v_mul_f32_e32 v194, s47, v194
	v_mul_f32_e32 v195, s47, v195
	v_fma_f32 v192, s46, v132, v192
	v_fma_f32 v193, s46, v133, v193
	v_fma_f32 v194, s46, v134, v194
	v_fma_f32 v195, s46, v135, v195
	v_mul_f32_e32 v192, v192, v198
	v_mul_f32_e32 v193, v193, v199
	v_mul_f32_e32 v194, v194, v200
	v_mul_f32_e32 v195, v195, v201
	v_fma_f32 v13, v192, v192, v13
	v_fma_f32 v13, v193, v193, v13
	v_fma_f32 v13, v194, v194, v13
	v_fma_f32 v13, v195, v195, v13
	v_mul_f32_e32 v192, 0x41800000, v192
	v_mul_f32_e32 v193, 0x41800000, v193
	v_mul_f32_e32 v194, 0x41800000, v194
	v_mul_f32_e32 v195, 0x41800000, v195
	v_cvt_pk_f16_f32 v196, v192, v193
	v_cvt_pk_f16_f32 v197, v194, v195
	ds_write_b64 v29, v[196:197] offset:32768
	v_cvt_f32_f16_e32 v198, v180
	v_cvt_f32_f16_sdwa v199, v180 dst_sel:DWORD dst_unused:UNUSED_PAD src0_sel:WORD_1
	v_cvt_f32_f16_e32 v200, v181
	v_cvt_f32_f16_sdwa v201, v181 dst_sel:DWORD dst_unused:UNUSED_PAD src0_sel:WORD_1
	v_fma_f32 v192, v190, v104, v120
	v_fma_f32 v193, v190, v105, v121
	v_fma_f32 v194, v190, v106, v122
	v_fma_f32 v195, v190, v107, v123
	v_mul_f32_e32 v192, s47, v192
	v_mul_f32_e32 v193, s47, v193
	v_mul_f32_e32 v194, s47, v194
	v_mul_f32_e32 v195, s47, v195
	v_fma_f32 v192, s46, v136, v192
	v_fma_f32 v193, s46, v137, v193
	v_fma_f32 v194, s46, v138, v194
	v_fma_f32 v195, s46, v139, v195
	v_mul_f32_e32 v192, v192, v198
	v_mul_f32_e32 v193, v193, v199
	v_mul_f32_e32 v194, v194, v200
	v_mul_f32_e32 v195, v195, v201
	v_fma_f32 v13, v192, v192, v13
	v_fma_f32 v13, v193, v193, v13
	v_fma_f32 v13, v194, v194, v13
	v_fma_f32 v13, v195, v195, v13
	v_mul_f32_e32 v192, 0x41800000, v192
	v_mul_f32_e32 v193, 0x41800000, v193
	v_mul_f32_e32 v194, 0x41800000, v194
	v_mul_f32_e32 v195, 0x41800000, v195
	v_cvt_pk_f16_f32 v196, v192, v193
	v_cvt_pk_f16_f32 v197, v194, v195
	ds_write_b64 v30, v[196:197] offset:32768
	v_cvt_f32_f16_e32 v198, v182
	v_cvt_f32_f16_sdwa v199, v182 dst_sel:DWORD dst_unused:UNUSED_PAD src0_sel:WORD_1
	v_cvt_f32_f16_e32 v200, v183
	v_cvt_f32_f16_sdwa v201, v183 dst_sel:DWORD dst_unused:UNUSED_PAD src0_sel:WORD_1
	v_fma_f32 v192, v190, v108, v124
	v_fma_f32 v193, v190, v109, v125
	v_fma_f32 v194, v190, v110, v126
	v_fma_f32 v195, v190, v111, v127
	v_mul_f32_e32 v192, s47, v192
	v_mul_f32_e32 v193, s47, v193
	v_mul_f32_e32 v194, s47, v194
	v_mul_f32_e32 v195, s47, v195
	v_fma_f32 v192, s46, v140, v192
	v_fma_f32 v193, s46, v141, v193
	v_fma_f32 v194, s46, v142, v194
	v_fma_f32 v195, s46, v143, v195
	v_mul_f32_e32 v192, v192, v198
	v_mul_f32_e32 v193, v193, v199
	v_mul_f32_e32 v194, v194, v200
	v_mul_f32_e32 v195, v195, v201
	v_fma_f32 v13, v192, v192, v13
	v_fma_f32 v13, v193, v193, v13
	v_fma_f32 v13, v194, v194, v13
	v_fma_f32 v13, v195, v195, v13
	v_mul_f32_e32 v192, 0x41800000, v192
	v_mul_f32_e32 v193, 0x41800000, v193
	v_mul_f32_e32 v194, 0x41800000, v194
	v_mul_f32_e32 v195, 0x41800000, v195
	v_cvt_pk_f16_f32 v196, v192, v193
	v_cvt_pk_f16_f32 v197, v194, v195
	ds_write_b64 v31, v[196:197] offset:32768
	s_waitcnt lgkmcnt(0)
	s_barrier
	ds_read_b128 v[204:207], v32 offset:32768
	ds_read_b128 v[208:211], v33 offset:32768
	s_waitcnt lgkmcnt(0)
	global_store_dwordx4 v8, v[204:207], s[38:39]
	global_store_dwordx4 v9, v[208:211], s[38:39]
	s_add_u32 s38, s38, 0x80
	s_addc_u32 s39, s39, 0
	s_add_u32 m0, s43, 0xc800
	s_nop 0
	global_load_lds_dwordx4 v4, s[30:31]
	s_add_u32 m0, s43, 0x10800
	s_nop 0
	global_load_lds_dwordx4 v6, s[32:33]
	s_add_u32 m0, s43, 0x14800
	s_nop 0
	global_load_lds_dwordx4 v8, s[34:35]
	s_add_u32 m0, s43, 0xe800
	s_nop 0
	global_load_lds_dwordx4 v5, s[30:31]
	s_add_u32 m0, s43, 0x12800
	s_nop 0
	global_load_lds_dwordx4 v7, s[32:33]
	s_add_u32 m0, s43, 0x16800
	s_nop 0
	global_load_lds_dwordx4 v9, s[34:35]
	s_add_u32 m0, s44, 0x18800
	s_nop 0
	global_load_lds_dword v10, s[36:37]
	s_add_u32 s30, s30, 0x80000
	s_addc_u32 s31, s31, 0
	s_add_u32 s32, s32, 0x4000
	s_addc_u32 s33, s33, 0
	s_add_u32 s34, s34, 0x80
	s_addc_u32 s35, s35, 0
	s_add_u32 s36, s36, 0x4000
	s_addc_u32 s37, s37, 0
	s_waitcnt vmcnt(18)
	s_waitcnt lgkmcnt(0)
	s_barrier
	v_mov_b32_e32 v112, 0
	v_mov_b32_e32 v113, 0
	v_mov_b32_e32 v114, 0
	v_mov_b32_e32 v115, 0
	v_mov_b32_e32 v116, 0
	v_mov_b32_e32 v117, 0
	v_mov_b32_e32 v118, 0
	v_mov_b32_e32 v119, 0
	v_mov_b32_e32 v120, 0
	v_mov_b32_e32 v121, 0
	v_mov_b32_e32 v122, 0
	v_mov_b32_e32 v123, 0
	v_mov_b32_e32 v124, 0
	v_mov_b32_e32 v125, 0
	v_mov_b32_e32 v126, 0
	v_mov_b32_e32 v127, 0
	ds_read_b128 v[144:147], v212 offset:16384
	ds_read_b128 v[148:151], v212 offset:20480
	ds_read_b128 v[152:155], v212 offset:24576
	ds_read_b128 v[156:159], v212 offset:28672
	ds_read_b32 v189, v220 offset:49152
	ds_read_b128 v[160:163], v213 offset:16384
	ds_read_b128 v[164:167], v213 offset:20480
	ds_read_b128 v[168:171], v213 offset:24576
	ds_read_b128 v[172:175], v213 offset:28672
	s_waitcnt lgkmcnt(4)
	v_mfma_f32_16x16x32_f16 v[96:99], v[144:147], v[44:47], 0
	v_mfma_f32_16x16x32_f16 v[100:103], v[148:151], v[44:47], 0
	v_mfma_f32_16x16x32_f16 v[104:107], v[152:155], v[44:47], 0
	v_mfma_f32_16x16x32_f16 v[108:111], v[156:159], v[44:47], 0
	ds_read_b128 v[144:147], v214 offset:16384
	ds_read_b128 v[148:151], v214 offset:20480
	ds_read_b128 v[152:155], v214 offset:24576
	ds_read_b128 v[156:159], v214 offset:28672
	s_waitcnt lgkmcnt(4)
	v_mfma_f32_16x16x32_f16 v[96:99], v[160:163], v[48:51], v[96:99]
	v_mfma_f32_16x16x32_f16 v[100:103], v[164:167], v[48:51], v[100:103]
	v_mfma_f32_16x16x32_f16 v[104:107], v[168:171], v[48:51], v[104:107]
	v_mfma_f32_16x16x32_f16 v[108:111], v[172:175], v[48:51], v[108:111]
	ds_read_b128 v[160:163], v215 offset:16384
	ds_read_b128 v[164:167], v215 offset:20480
	ds_read_b128 v[168:171], v215 offset:24576
	ds_read_b128 v[172:175], v215 offset:28672
	s_waitcnt lgkmcnt(4)
	v_mfma_f32_16x16x32_f16 v[96:99], v[144:147], v[52:55], v[96:99]
	v_mfma_f32_16x16x32_f16 v[100:103], v[148:151], v[52:55], v[100:103]
	v_mfma_f32_16x16x32_f16 v[104:107], v[152:155], v[52:55], v[104:107]
	v_mfma_f32_16x16x32_f16 v[108:111], v[156:159], v[52:55], v[108:111]
	s_waitcnt lgkmcnt(0)
	v_mfma_f32_16x16x32_f16 v[96:99], v[160:163], v[56:59], v[96:99]
	v_mfma_f32_16x16x32_f16 v[100:103], v[164:167], v[56:59], v[100:103]
	v_mfma_f32_16x16x32_f16 v[104:107], v[168:171], v[56:59], v[104:107]
	v_mfma_f32_16x16x32_f16 v[108:111], v[172:175], v[56:59], v[108:111]
	v_mul_f32_e32 v189, 0x3fb8aa3b, v189
	s_cmp_lt_u32 s42, 0
	s_cbranch_scc1 .Lmy_s2_kend46
	s_cmp_eq_u32 s42, 0
	s_cbranch_scc1 .Lmy_s2_diag47
	ds_read_b128 v[176:179], v221 offset:49664
	ds_read_b128 v[180:183], v221 offset:49680
	ds_read_b32 v188, v221 offset:49152
	ds_read_b128 v[160:163], v212 offset:0
	ds_read_b128 v[164:167], v212 offset:4096
	ds_read_b128 v[168:171], v212 offset:8192
	ds_read_b128 v[172:175], v212 offset:12288
	s_waitcnt lgkmcnt(4)
	v_fma_f32 v188, v188, s51, v189
	v_exp_f32_e32 v188, v188
	s_nop 0
	v_mul_f32_e32 v176, v188, v176
	v_mul_f32_e32 v177, v188, v177
	v_mul_f32_e32 v178, v188, v178
	v_mul_f32_e32 v179, v188, v179
	v_mul_f32_e32 v180, v188, v180
	v_mul_f32_e32 v181, v188, v181
	v_mul_f32_e32 v182, v188, v182
	v_mul_f32_e32 v183, v188, v183
	v_mul_f32_e32 v176, v60, v176
	v_mul_f32_e32 v177, v61, v177
	v_mul_f32_e32 v178, v62, v178
	v_mul_f32_e32 v179, v63, v179
	v_mul_f32_e32 v180, v64, v180
	v_mul_f32_e32 v181, v65, v181
	v_mul_f32_e32 v182, v66, v182
	v_mul_f32_e32 v183, v67, v183
	v_cvt_pk_f16_f32 v184, v176, v177
	v_cvt_pk_f16_f32 v185, v178, v179
	v_cvt_pk_f16_f32 v186, v180, v181
	v_cvt_pk_f16_f32 v187, v182, v183
	s_waitcnt lgkmcnt(0)
	s_nop 0
	v_mfma_f32_16x16x32_f16 v[112:115], v[160:163], v[184:187], v[112:115]
	v_mfma_f32_16x16x32_f16 v[116:119], v[164:167], v[184:187], v[116:119]
	v_mfma_f32_16x16x32_f16 v[120:123], v[168:171], v[184:187], v[120:123]
	v_mfma_f32_16x16x32_f16 v[124:127], v[172:175], v[184:187], v[124:127]
	s_branch .Lmy_s2_knext48

.Lmy_s2_knext54:
.Lmy_s2_kend46:
	v_readlane_b32 s46, v11, 5
	v_readlane_b32 s47, v12, 5
	v_exp_f32_e32 v190, v189
	ds_read_b64 v[176:177], v216 offset:32768
	ds_read_b64 v[178:179], v217 offset:32768
	ds_read_b64 v[180:181], v218 offset:32768
	ds_read_b64 v[182:183], v219 offset:32768
	s_waitcnt lgkmcnt(0)
	s_nop 4
	v_cvt_f32_f16_e32 v198, v176
	v_cvt_f32_f16_sdwa v199, v176 dst_sel:DWORD dst_unused:UNUSED_PAD src0_sel:WORD_1
	v_cvt_f32_f16_e32 v200, v177
	v_cvt_f32_f16_sdwa v201, v177 dst_sel:DWORD dst_unused:UNUSED_PAD src0_sel:WORD_1
	v_fma_f32 v192, v190, v96, v112
	v_fma_f32 v193, v190, v97, v113
	v_fma_f32 v194, v190, v98, v114
	v_fma_f32 v195, v190, v99, v115
	v_mul_f32_e32 v192, s47, v192
	v_mul_f32_e32 v193, s47, v193
	v_mul_f32_e32 v194, s47, v194
	v_mul_f32_e32 v195, s47, v195
	v_fma_f32 v192, s46, v128, v192
	v_fma_f32 v193, s46, v129, v193
	v_fma_f32 v194, s46, v130, v194
	v_fma_f32 v195, s46, v131, v195
	v_mul_f32_e32 v192, v192, v198
	v_mul_f32_e32 v193, v193, v199
	v_mul_f32_e32 v194, v194, v200
	v_mul_f32_e32 v195, v195, v201
	v_fma_f32 v13, v192, v192, v13
	v_fma_f32 v13, v193, v193, v13
	v_fma_f32 v13, v194, v194, v13
	v_fma_f32 v13, v195, v195, v13
	v_mul_f32_e32 v192, 0x41800000, v192
	v_mul_f32_e32 v193, 0x41800000, v193
	v_mul_f32_e32 v194, 0x41800000, v194
	v_mul_f32_e32 v195, 0x41800000, v195
	v_cvt_pk_f16_f32 v196, v192, v193
	v_cvt_pk_f16_f32 v197, v194, v195
	ds_write_b64 v216, v[196:197] offset:32768
	v_cvt_f32_f16_e32 v198, v178
	v_cvt_f32_f16_sdwa v199, v178 dst_sel:DWORD dst_unused:UNUSED_PAD src0_sel:WORD_1
	v_cvt_f32_f16_e32 v200, v179
	v_cvt_f32_f16_sdwa v201, v179 dst_sel:DWORD dst_unused:UNUSED_PAD src0_sel:WORD_1
	v_fma_f32 v192, v190, v100, v116
	v_fma_f32 v193, v190, v101, v117
	v_fma_f32 v194, v190, v102, v118
	v_fma_f32 v195, v190, v103, v119
	v_mul_f32_e32 v192, s47, v192
	v_mul_f32_e32 v193, s47, v193
	v_mul_f32_e32 v194, s47, v194
	v_mul_f32_e32 v195, s47, v195
	v_fma_f32 v192, s46, v132, v192
	v_fma_f32 v193, s46, v133, v193
	v_fma_f32 v194, s46, v134, v194
	v_fma_f32 v195, s46, v135, v195
	v_mul_f32_e32 v192, v192, v198
	v_mul_f32_e32 v193, v193, v199
	v_mul_f32_e32 v194, v194, v200
	v_mul_f32_e32 v195, v195, v201
	v_fma_f32 v13, v192, v192, v13
	v_fma_f32 v13, v193, v193, v13
	v_fma_f32 v13, v194, v194, v13
	v_fma_f32 v13, v195, v195, v13
	v_mul_f32_e32 v192, 0x41800000, v192
	v_mul_f32_e32 v193, 0x41800000, v193
	v_mul_f32_e32 v194, 0x41800000, v194
	v_mul_f32_e32 v195, 0x41800000, v195
	v_cvt_pk_f16_f32 v196, v192, v193
	v_cvt_pk_f16_f32 v197, v194, v195
	ds_write_b64 v217, v[196:197] offset:32768
	v_cvt_f32_f16_e32 v198, v180
	v_cvt_f32_f16_sdwa v199, v180 dst_sel:DWORD dst_unused:UNUSED_PAD src0_sel:WORD_1
	v_cvt_f32_f16_e32 v200, v181
	v_cvt_f32_f16_sdwa v201, v181 dst_sel:DWORD dst_unused:UNUSED_PAD src0_sel:WORD_1
	v_fma_f32 v192, v190, v104, v120
	v_fma_f32 v193, v190, v105, v121
	v_fma_f32 v194, v190, v106, v122
	v_fma_f32 v195, v190, v107, v123
	v_mul_f32_e32 v192, s47, v192
	v_mul_f32_e32 v193, s47, v193
	v_mul_f32_e32 v194, s47, v194
	v_mul_f32_e32 v195, s47, v195
	v_fma_f32 v192, s46, v136, v192
	v_fma_f32 v193, s46, v137, v193
	v_fma_f32 v194, s46, v138, v194
	v_fma_f32 v195, s46, v139, v195
	v_mul_f32_e32 v192, v192, v198
	v_mul_f32_e32 v193, v193, v199
	v_mul_f32_e32 v194, v194, v200
	v_mul_f32_e32 v195, v195, v201
	v_fma_f32 v13, v192, v192, v13
	v_fma_f32 v13, v193, v193, v13
	v_fma_f32 v13, v194, v194, v13
	v_fma_f32 v13, v195, v195, v13
	v_mul_f32_e32 v192, 0x41800000, v192
	v_mul_f32_e32 v193, 0x41800000, v193
	v_mul_f32_e32 v194, 0x41800000, v194
	v_mul_f32_e32 v195, 0x41800000, v195
	v_cvt_pk_f16_f32 v196, v192, v193
	v_cvt_pk_f16_f32 v197, v194, v195
	ds_write_b64 v218, v[196:197] offset:32768
	v_cvt_f32_f16_e32 v198, v182
	v_cvt_f32_f16_sdwa v199, v182 dst_sel:DWORD dst_unused:UNUSED_PAD src0_sel:WORD_1
	v_cvt_f32_f16_e32 v200, v183
	v_cvt_f32_f16_sdwa v201, v183 dst_sel:DWORD dst_unused:UNUSED_PAD src0_sel:WORD_1
	v_fma_f32 v192, v190, v108, v124
	v_fma_f32 v193, v190, v109, v125
	v_fma_f32 v194, v190, v110, v126
	v_fma_f32 v195, v190, v111, v127
	v_mul_f32_e32 v192, s47, v192
	v_mul_f32_e32 v193, s47, v193
	v_mul_f32_e32 v194, s47, v194
	v_mul_f32_e32 v195, s47, v195
	v_fma_f32 v192, s46, v140, v192
	v_fma_f32 v193, s46, v141, v193
	v_fma_f32 v194, s46, v142, v194
	v_fma_f32 v195, s46, v143, v195
	v_mul_f32_e32 v192, v192, v198
	v_mul_f32_e32 v193, v193, v199
	v_mul_f32_e32 v194, v194, v200
	v_mul_f32_e32 v195, v195, v201
	v_fma_f32 v13, v192, v192, v13
	v_fma_f32 v13, v193, v193, v13
	v_fma_f32 v13, v194, v194, v13
	v_fma_f32 v13, v195, v195, v13
	v_mul_f32_e32 v192, 0x41800000, v192
	v_mul_f32_e32 v193, 0x41800000, v193
	v_mul_f32_e32 v194, 0x41800000, v194
	v_mul_f32_e32 v195, 0x41800000, v195
	v_cvt_pk_f16_f32 v196, v192, v193
	v_cvt_pk_f16_f32 v197, v194, v195
	ds_write_b64 v219, v[196:197] offset:32768
	s_waitcnt lgkmcnt(0)
	s_barrier
	ds_read_b128 v[204:207], v34 offset:32768
	ds_read_b128 v[208:211], v35 offset:32768
	s_waitcnt lgkmcnt(0)
	global_store_dwordx4 v8, v[204:207], s[38:39]
	global_store_dwordx4 v9, v[208:211], s[38:39]
	s_add_u32 s38, s38, 0x80
	s_addc_u32 s39, s39, 0
	s_waitcnt vmcnt(11)
	s_waitcnt lgkmcnt(0)
	s_barrier
	v_mov_b32_e32 v112, 0
	v_mov_b32_e32 v113, 0
	v_mov_b32_e32 v114, 0
	v_mov_b32_e32 v115, 0
	v_mov_b32_e32 v116, 0
	v_mov_b32_e32 v117, 0
	v_mov_b32_e32 v118, 0
	v_mov_b32_e32 v119, 0
	v_mov_b32_e32 v120, 0
	v_mov_b32_e32 v121, 0
	v_mov_b32_e32 v122, 0
	v_mov_b32_e32 v123, 0
	v_mov_b32_e32 v124, 0
	v_mov_b32_e32 v125, 0
	v_mov_b32_e32 v126, 0
	v_mov_b32_e32 v127, 0
	ds_read_b128 v[144:147], v16 offset:16384
	ds_read_b128 v[148:151], v16 offset:20480
	ds_read_b128 v[152:155], v16 offset:24576
	ds_read_b128 v[156:159], v16 offset:28672
	ds_read_b32 v189, v36 offset:49152
	ds_read_b128 v[160:163], v17 offset:16384
	ds_read_b128 v[164:167], v17 offset:20480
	ds_read_b128 v[168:171], v17 offset:24576
	ds_read_b128 v[172:175], v17 offset:28672
	s_waitcnt lgkmcnt(4)
	v_mfma_f32_16x16x32_f16 v[96:99], v[144:147], v[44:47], 0
	v_mfma_f32_16x16x32_f16 v[100:103], v[148:151], v[44:47], 0
	v_mfma_f32_16x16x32_f16 v[104:107], v[152:155], v[44:47], 0
	v_mfma_f32_16x16x32_f16 v[108:111], v[156:159], v[44:47], 0
	ds_read_b128 v[144:147], v18 offset:16384
	ds_read_b128 v[148:151], v18 offset:20480
	ds_read_b128 v[152:155], v18 offset:24576
	ds_read_b128 v[156:159], v18 offset:28672
	s_waitcnt lgkmcnt(4)
	v_mfma_f32_16x16x32_f16 v[96:99], v[160:163], v[48:51], v[96:99]
	v_mfma_f32_16x16x32_f16 v[100:103], v[164:167], v[48:51], v[100:103]
	v_mfma_f32_16x16x32_f16 v[104:107], v[168:171], v[48:51], v[104:107]
	v_mfma_f32_16x16x32_f16 v[108:111], v[172:175], v[48:51], v[108:111]
	ds_read_b128 v[160:163], v19 offset:16384
	ds_read_b128 v[164:167], v19 offset:20480
	ds_read_b128 v[168:171], v19 offset:24576
	ds_read_b128 v[172:175], v19 offset:28672
	s_waitcnt lgkmcnt(4)
	v_mfma_f32_16x16x32_f16 v[96:99], v[144:147], v[52:55], v[96:99]
	v_mfma_f32_16x16x32_f16 v[100:103], v[148:151], v[52:55], v[100:103]
	v_mfma_f32_16x16x32_f16 v[104:107], v[152:155], v[52:55], v[104:107]
	v_mfma_f32_16x16x32_f16 v[108:111], v[156:159], v[52:55], v[108:111]
	s_waitcnt lgkmcnt(0)
	v_mfma_f32_16x16x32_f16 v[96:99], v[160:163], v[56:59], v[96:99]
	v_mfma_f32_16x16x32_f16 v[100:103], v[164:167], v[56:59], v[100:103]
	v_mfma_f32_16x16x32_f16 v[104:107], v[168:171], v[56:59], v[104:107]
	v_mfma_f32_16x16x32_f16 v[108:111], v[172:175], v[56:59], v[108:111]
	v_mul_f32_e32 v189, 0x3fb8aa3b, v189
	s_cmp_lt_u32 s42, 0
	s_cbranch_scc1 .Lmy_s2_kend55
	s_cmp_eq_u32 s42, 0
	s_cbranch_scc1 .Lmy_s2_diag56
	ds_read_b128 v[176:179], v38 offset:49664
	ds_read_b128 v[180:183], v38 offset:49680
	ds_read_b32 v188, v38 offset:49152
	ds_read_b128 v[160:163], v16 offset:0
	ds_read_b128 v[164:167], v16 offset:4096
	ds_read_b128 v[168:171], v16 offset:8192
	ds_read_b128 v[172:175], v16 offset:12288
	s_waitcnt lgkmcnt(4)
	v_fma_f32 v188, v188, s51, v189
	v_exp_f32_e32 v188, v188
	s_nop 0
	v_mul_f32_e32 v176, v188, v176
	v_mul_f32_e32 v177, v188, v177
	v_mul_f32_e32 v178, v188, v178
	v_mul_f32_e32 v179, v188, v179
	v_mul_f32_e32 v180, v188, v180
	v_mul_f32_e32 v181, v188, v181
	v_mul_f32_e32 v182, v188, v182
	v_mul_f32_e32 v183, v188, v183
	v_mul_f32_e32 v176, v60, v176
	v_mul_f32_e32 v177, v61, v177
	v_mul_f32_e32 v178, v62, v178
	v_mul_f32_e32 v179, v63, v179
	v_mul_f32_e32 v180, v64, v180
	v_mul_f32_e32 v181, v65, v181
	v_mul_f32_e32 v182, v66, v182
	v_mul_f32_e32 v183, v67, v183
	v_cvt_pk_f16_f32 v184, v176, v177
	v_cvt_pk_f16_f32 v185, v178, v179
	v_cvt_pk_f16_f32 v186, v180, v181
	v_cvt_pk_f16_f32 v187, v182, v183
	s_waitcnt lgkmcnt(0)
	s_nop 0
	v_mfma_f32_16x16x32_f16 v[112:115], v[160:163], v[184:187], v[112:115]
	v_mfma_f32_16x16x32_f16 v[116:119], v[164:167], v[184:187], v[116:119]
	v_mfma_f32_16x16x32_f16 v[120:123], v[168:171], v[184:187], v[120:123]
	v_mfma_f32_16x16x32_f16 v[124:127], v[172:175], v[184:187], v[124:127]
	s_branch .Lmy_s2_knext57

.Lmy_s2_knext63:
.Lmy_s2_kend55:
	v_readlane_b32 s46, v11, 6
	v_readlane_b32 s47, v12, 6
	v_exp_f32_e32 v190, v189
	ds_read_b64 v[176:177], v24 offset:32768
	ds_read_b64 v[178:179], v25 offset:32768
	ds_read_b64 v[180:181], v26 offset:32768
	ds_read_b64 v[182:183], v27 offset:32768
	s_waitcnt lgkmcnt(0)
	s_nop 4
	v_cvt_f32_f16_e32 v198, v176
	v_cvt_f32_f16_sdwa v199, v176 dst_sel:DWORD dst_unused:UNUSED_PAD src0_sel:WORD_1
	v_cvt_f32_f16_e32 v200, v177
	v_cvt_f32_f16_sdwa v201, v177 dst_sel:DWORD dst_unused:UNUSED_PAD src0_sel:WORD_1
	v_fma_f32 v192, v190, v96, v112
	v_fma_f32 v193, v190, v97, v113
	v_fma_f32 v194, v190, v98, v114
	v_fma_f32 v195, v190, v99, v115
	v_mul_f32_e32 v192, s47, v192
	v_mul_f32_e32 v193, s47, v193
	v_mul_f32_e32 v194, s47, v194
	v_mul_f32_e32 v195, s47, v195
	v_fma_f32 v192, s46, v128, v192
	v_fma_f32 v193, s46, v129, v193
	v_fma_f32 v194, s46, v130, v194
	v_fma_f32 v195, s46, v131, v195
	v_mul_f32_e32 v192, v192, v198
	v_mul_f32_e32 v193, v193, v199
	v_mul_f32_e32 v194, v194, v200
	v_mul_f32_e32 v195, v195, v201
	v_fma_f32 v13, v192, v192, v13
	v_fma_f32 v13, v193, v193, v13
	v_fma_f32 v13, v194, v194, v13
	v_fma_f32 v13, v195, v195, v13
	v_mul_f32_e32 v192, 0x41800000, v192
	v_mul_f32_e32 v193, 0x41800000, v193
	v_mul_f32_e32 v194, 0x41800000, v194
	v_mul_f32_e32 v195, 0x41800000, v195
	v_cvt_pk_f16_f32 v196, v192, v193
	v_cvt_pk_f16_f32 v197, v194, v195
	ds_write_b64 v24, v[196:197] offset:32768
	v_cvt_f32_f16_e32 v198, v178
	v_cvt_f32_f16_sdwa v199, v178 dst_sel:DWORD dst_unused:UNUSED_PAD src0_sel:WORD_1
	v_cvt_f32_f16_e32 v200, v179
	v_cvt_f32_f16_sdwa v201, v179 dst_sel:DWORD dst_unused:UNUSED_PAD src0_sel:WORD_1
	v_fma_f32 v192, v190, v100, v116
	v_fma_f32 v193, v190, v101, v117
	v_fma_f32 v194, v190, v102, v118
	v_fma_f32 v195, v190, v103, v119
	v_mul_f32_e32 v192, s47, v192
	v_mul_f32_e32 v193, s47, v193
	v_mul_f32_e32 v194, s47, v194
	v_mul_f32_e32 v195, s47, v195
	v_fma_f32 v192, s46, v132, v192
	v_fma_f32 v193, s46, v133, v193
	v_fma_f32 v194, s46, v134, v194
	v_fma_f32 v195, s46, v135, v195
	v_mul_f32_e32 v192, v192, v198
	v_mul_f32_e32 v193, v193, v199
	v_mul_f32_e32 v194, v194, v200
	v_mul_f32_e32 v195, v195, v201
	v_fma_f32 v13, v192, v192, v13
	v_fma_f32 v13, v193, v193, v13
	v_fma_f32 v13, v194, v194, v13
	v_fma_f32 v13, v195, v195, v13
	v_mul_f32_e32 v192, 0x41800000, v192
	v_mul_f32_e32 v193, 0x41800000, v193
	v_mul_f32_e32 v194, 0x41800000, v194
	v_mul_f32_e32 v195, 0x41800000, v195
	v_cvt_pk_f16_f32 v196, v192, v193
	v_cvt_pk_f16_f32 v197, v194, v195
	ds_write_b64 v25, v[196:197] offset:32768
	v_cvt_f32_f16_e32 v198, v180
	v_cvt_f32_f16_sdwa v199, v180 dst_sel:DWORD dst_unused:UNUSED_PAD src0_sel:WORD_1
	v_cvt_f32_f16_e32 v200, v181
	v_cvt_f32_f16_sdwa v201, v181 dst_sel:DWORD dst_unused:UNUSED_PAD src0_sel:WORD_1
	v_fma_f32 v192, v190, v104, v120
	v_fma_f32 v193, v190, v105, v121
	v_fma_f32 v194, v190, v106, v122
	v_fma_f32 v195, v190, v107, v123
	v_mul_f32_e32 v192, s47, v192
	v_mul_f32_e32 v193, s47, v193
	v_mul_f32_e32 v194, s47, v194
	v_mul_f32_e32 v195, s47, v195
	v_fma_f32 v192, s46, v136, v192
	v_fma_f32 v193, s46, v137, v193
	v_fma_f32 v194, s46, v138, v194
	v_fma_f32 v195, s46, v139, v195
	v_mul_f32_e32 v192, v192, v198
	v_mul_f32_e32 v193, v193, v199
	v_mul_f32_e32 v194, v194, v200
	v_mul_f32_e32 v195, v195, v201
	v_fma_f32 v13, v192, v192, v13
	v_fma_f32 v13, v193, v193, v13
	v_fma_f32 v13, v194, v194, v13
	v_fma_f32 v13, v195, v195, v13
	v_mul_f32_e32 v192, 0x41800000, v192
	v_mul_f32_e32 v193, 0x41800000, v193
	v_mul_f32_e32 v194, 0x41800000, v194
	v_mul_f32_e32 v195, 0x41800000, v195
	v_cvt_pk_f16_f32 v196, v192, v193
	v_cvt_pk_f16_f32 v197, v194, v195
	ds_write_b64 v26, v[196:197] offset:32768
	v_cvt_f32_f16_e32 v198, v182
	v_cvt_f32_f16_sdwa v199, v182 dst_sel:DWORD dst_unused:UNUSED_PAD src0_sel:WORD_1
	v_cvt_f32_f16_e32 v200, v183
	v_cvt_f32_f16_sdwa v201, v183 dst_sel:DWORD dst_unused:UNUSED_PAD src0_sel:WORD_1
	v_fma_f32 v192, v190, v108, v124
	v_fma_f32 v193, v190, v109, v125
	v_fma_f32 v194, v190, v110, v126
	v_fma_f32 v195, v190, v111, v127
	v_mul_f32_e32 v192, s47, v192
	v_mul_f32_e32 v193, s47, v193
	v_mul_f32_e32 v194, s47, v194
	v_mul_f32_e32 v195, s47, v195
	v_fma_f32 v192, s46, v140, v192
	v_fma_f32 v193, s46, v141, v193
	v_fma_f32 v194, s46, v142, v194
	v_fma_f32 v195, s46, v143, v195
	v_mul_f32_e32 v192, v192, v198
	v_mul_f32_e32 v193, v193, v199
	v_mul_f32_e32 v194, v194, v200
	v_mul_f32_e32 v195, v195, v201
	v_fma_f32 v13, v192, v192, v13
	v_fma_f32 v13, v193, v193, v13
	v_fma_f32 v13, v194, v194, v13
	v_fma_f32 v13, v195, v195, v13
	v_mul_f32_e32 v192, 0x41800000, v192
	v_mul_f32_e32 v193, 0x41800000, v193
	v_mul_f32_e32 v194, 0x41800000, v194
	v_mul_f32_e32 v195, 0x41800000, v195
	v_cvt_pk_f16_f32 v196, v192, v193
	v_cvt_pk_f16_f32 v197, v194, v195
	ds_write_b64 v27, v[196:197] offset:32768
	s_waitcnt lgkmcnt(0)
	s_barrier
	ds_read_b128 v[204:207], v40 offset:32768
	ds_read_b128 v[208:211], v41 offset:32768
	s_waitcnt lgkmcnt(0)
	global_store_dwordx4 v8, v[204:207], s[38:39]
	global_store_dwordx4 v9, v[208:211], s[38:39]
	s_add_u32 s38, s38, 0x80
	s_addc_u32 s39, s39, 0
	s_waitcnt vmcnt(4)
	s_waitcnt lgkmcnt(0)
	s_barrier
	v_mov_b32_e32 v112, 0
	v_mov_b32_e32 v113, 0
	v_mov_b32_e32 v114, 0
	v_mov_b32_e32 v115, 0
	v_mov_b32_e32 v116, 0
	v_mov_b32_e32 v117, 0
	v_mov_b32_e32 v118, 0
	v_mov_b32_e32 v119, 0
	v_mov_b32_e32 v120, 0
	v_mov_b32_e32 v121, 0
	v_mov_b32_e32 v122, 0
	v_mov_b32_e32 v123, 0
	v_mov_b32_e32 v124, 0
	v_mov_b32_e32 v125, 0
	v_mov_b32_e32 v126, 0
	v_mov_b32_e32 v127, 0
	ds_read_b128 v[144:147], v20 offset:16384
	ds_read_b128 v[148:151], v20 offset:20480
	ds_read_b128 v[152:155], v20 offset:24576
	ds_read_b128 v[156:159], v20 offset:28672
	ds_read_b32 v189, v37 offset:49152
	ds_read_b128 v[160:163], v21 offset:16384
	ds_read_b128 v[164:167], v21 offset:20480
	ds_read_b128 v[168:171], v21 offset:24576
	ds_read_b128 v[172:175], v21 offset:28672
	s_waitcnt lgkmcnt(4)
	v_mfma_f32_16x16x32_f16 v[96:99], v[144:147], v[44:47], 0
	v_mfma_f32_16x16x32_f16 v[100:103], v[148:151], v[44:47], 0
	v_mfma_f32_16x16x32_f16 v[104:107], v[152:155], v[44:47], 0
	v_mfma_f32_16x16x32_f16 v[108:111], v[156:159], v[44:47], 0
	ds_read_b128 v[144:147], v22 offset:16384
	ds_read_b128 v[148:151], v22 offset:20480
	ds_read_b128 v[152:155], v22 offset:24576
	ds_read_b128 v[156:159], v22 offset:28672
	s_waitcnt lgkmcnt(4)
	v_mfma_f32_16x16x32_f16 v[96:99], v[160:163], v[48:51], v[96:99]
	v_mfma_f32_16x16x32_f16 v[100:103], v[164:167], v[48:51], v[100:103]
	v_mfma_f32_16x16x32_f16 v[104:107], v[168:171], v[48:51], v[104:107]
	v_mfma_f32_16x16x32_f16 v[108:111], v[172:175], v[48:51], v[108:111]
	ds_read_b128 v[160:163], v23 offset:16384
	ds_read_b128 v[164:167], v23 offset:20480
	ds_read_b128 v[168:171], v23 offset:24576
	ds_read_b128 v[172:175], v23 offset:28672
	s_waitcnt lgkmcnt(4)
	v_mfma_f32_16x16x32_f16 v[96:99], v[144:147], v[52:55], v[96:99]
	v_mfma_f32_16x16x32_f16 v[100:103], v[148:151], v[52:55], v[100:103]
	v_mfma_f32_16x16x32_f16 v[104:107], v[152:155], v[52:55], v[104:107]
	v_mfma_f32_16x16x32_f16 v[108:111], v[156:159], v[52:55], v[108:111]
	s_waitcnt lgkmcnt(0)
	v_mfma_f32_16x16x32_f16 v[96:99], v[160:163], v[56:59], v[96:99]
	v_mfma_f32_16x16x32_f16 v[100:103], v[164:167], v[56:59], v[100:103]
	v_mfma_f32_16x16x32_f16 v[104:107], v[168:171], v[56:59], v[104:107]
	v_mfma_f32_16x16x32_f16 v[108:111], v[172:175], v[56:59], v[108:111]
	v_mul_f32_e32 v189, 0x3fb8aa3b, v189
	s_cmp_lt_u32 s42, 0
	s_cbranch_scc1 .Lmy_s2_kend64
	s_cmp_eq_u32 s42, 0
	s_cbranch_scc1 .Lmy_s2_diag65
	ds_read_b128 v[176:179], v39 offset:49664
	ds_read_b128 v[180:183], v39 offset:49680
	ds_read_b32 v188, v39 offset:49152
	ds_read_b128 v[160:163], v20 offset:0
	ds_read_b128 v[164:167], v20 offset:4096
	ds_read_b128 v[168:171], v20 offset:8192
	ds_read_b128 v[172:175], v20 offset:12288
	s_waitcnt lgkmcnt(4)
	v_fma_f32 v188, v188, s51, v189
	v_exp_f32_e32 v188, v188
	s_nop 0
	v_mul_f32_e32 v176, v188, v176
	v_mul_f32_e32 v177, v188, v177
	v_mul_f32_e32 v178, v188, v178
	v_mul_f32_e32 v179, v188, v179
	v_mul_f32_e32 v180, v188, v180
	v_mul_f32_e32 v181, v188, v181
	v_mul_f32_e32 v182, v188, v182
	v_mul_f32_e32 v183, v188, v183
	v_mul_f32_e32 v176, v60, v176
	v_mul_f32_e32 v177, v61, v177
	v_mul_f32_e32 v178, v62, v178
	v_mul_f32_e32 v179, v63, v179
	v_mul_f32_e32 v180, v64, v180
	v_mul_f32_e32 v181, v65, v181
	v_mul_f32_e32 v182, v66, v182
	v_mul_f32_e32 v183, v67, v183
	v_cvt_pk_f16_f32 v184, v176, v177
	v_cvt_pk_f16_f32 v185, v178, v179
	v_cvt_pk_f16_f32 v186, v180, v181
	v_cvt_pk_f16_f32 v187, v182, v183
	s_waitcnt lgkmcnt(0)
	s_nop 0
	v_mfma_f32_16x16x32_f16 v[112:115], v[160:163], v[184:187], v[112:115]
	v_mfma_f32_16x16x32_f16 v[116:119], v[164:167], v[184:187], v[116:119]
	v_mfma_f32_16x16x32_f16 v[120:123], v[168:171], v[184:187], v[120:123]
	v_mfma_f32_16x16x32_f16 v[124:127], v[172:175], v[184:187], v[124:127]
	s_branch .Lmy_s2_knext66

.Lmy_s2_knext72:
.Lmy_s2_kend64:
	v_readlane_b32 s46, v11, 7
	v_readlane_b32 s47, v12, 7
	v_exp_f32_e32 v190, v189
	ds_read_b64 v[176:177], v28 offset:32768
	ds_read_b64 v[178:179], v29 offset:32768
	ds_read_b64 v[180:181], v30 offset:32768
	ds_read_b64 v[182:183], v31 offset:32768
	s_waitcnt lgkmcnt(0)
	s_nop 4
	v_cvt_f32_f16_e32 v198, v176
	v_cvt_f32_f16_sdwa v199, v176 dst_sel:DWORD dst_unused:UNUSED_PAD src0_sel:WORD_1
	v_cvt_f32_f16_e32 v200, v177
	v_cvt_f32_f16_sdwa v201, v177 dst_sel:DWORD dst_unused:UNUSED_PAD src0_sel:WORD_1
	v_fma_f32 v192, v190, v96, v112
	v_fma_f32 v193, v190, v97, v113
	v_fma_f32 v194, v190, v98, v114
	v_fma_f32 v195, v190, v99, v115
	v_mul_f32_e32 v192, s47, v192
	v_mul_f32_e32 v193, s47, v193
	v_mul_f32_e32 v194, s47, v194
	v_mul_f32_e32 v195, s47, v195
	v_fma_f32 v192, s46, v128, v192
	v_fma_f32 v193, s46, v129, v193
	v_fma_f32 v194, s46, v130, v194
	v_fma_f32 v195, s46, v131, v195
	v_mul_f32_e32 v192, v192, v198
	v_mul_f32_e32 v193, v193, v199
	v_mul_f32_e32 v194, v194, v200
	v_mul_f32_e32 v195, v195, v201
	v_fma_f32 v13, v192, v192, v13
	v_fma_f32 v13, v193, v193, v13
	v_fma_f32 v13, v194, v194, v13
	v_fma_f32 v13, v195, v195, v13
	v_mul_f32_e32 v192, 0x41800000, v192
	v_mul_f32_e32 v193, 0x41800000, v193
	v_mul_f32_e32 v194, 0x41800000, v194
	v_mul_f32_e32 v195, 0x41800000, v195
	v_cvt_pk_f16_f32 v196, v192, v193
	v_cvt_pk_f16_f32 v197, v194, v195
	ds_write_b64 v28, v[196:197] offset:32768
	v_cvt_f32_f16_e32 v198, v178
	v_cvt_f32_f16_sdwa v199, v178 dst_sel:DWORD dst_unused:UNUSED_PAD src0_sel:WORD_1
	v_cvt_f32_f16_e32 v200, v179
	v_cvt_f32_f16_sdwa v201, v179 dst_sel:DWORD dst_unused:UNUSED_PAD src0_sel:WORD_1
	v_fma_f32 v192, v190, v100, v116
	v_fma_f32 v193, v190, v101, v117
	v_fma_f32 v194, v190, v102, v118
	v_fma_f32 v195, v190, v103, v119
	v_mul_f32_e32 v192, s47, v192
	v_mul_f32_e32 v193, s47, v193
	v_mul_f32_e32 v194, s47, v194
	v_mul_f32_e32 v195, s47, v195
	v_fma_f32 v192, s46, v132, v192
	v_fma_f32 v193, s46, v133, v193
	v_fma_f32 v194, s46, v134, v194
	v_fma_f32 v195, s46, v135, v195
	v_mul_f32_e32 v192, v192, v198
	v_mul_f32_e32 v193, v193, v199
	v_mul_f32_e32 v194, v194, v200
	v_mul_f32_e32 v195, v195, v201
	v_fma_f32 v13, v192, v192, v13
	v_fma_f32 v13, v193, v193, v13
	v_fma_f32 v13, v194, v194, v13
	v_fma_f32 v13, v195, v195, v13
	v_mul_f32_e32 v192, 0x41800000, v192
	v_mul_f32_e32 v193, 0x41800000, v193
	v_mul_f32_e32 v194, 0x41800000, v194
	v_mul_f32_e32 v195, 0x41800000, v195
	v_cvt_pk_f16_f32 v196, v192, v193
	v_cvt_pk_f16_f32 v197, v194, v195
	ds_write_b64 v29, v[196:197] offset:32768
	v_cvt_f32_f16_e32 v198, v180
	v_cvt_f32_f16_sdwa v199, v180 dst_sel:DWORD dst_unused:UNUSED_PAD src0_sel:WORD_1
	v_cvt_f32_f16_e32 v200, v181
	v_cvt_f32_f16_sdwa v201, v181 dst_sel:DWORD dst_unused:UNUSED_PAD src0_sel:WORD_1
	v_fma_f32 v192, v190, v104, v120
	v_fma_f32 v193, v190, v105, v121
	v_fma_f32 v194, v190, v106, v122
	v_fma_f32 v195, v190, v107, v123
	v_mul_f32_e32 v192, s47, v192
	v_mul_f32_e32 v193, s47, v193
	v_mul_f32_e32 v194, s47, v194
	v_mul_f32_e32 v195, s47, v195
	v_fma_f32 v192, s46, v136, v192
	v_fma_f32 v193, s46, v137, v193
	v_fma_f32 v194, s46, v138, v194
	v_fma_f32 v195, s46, v139, v195
	v_mul_f32_e32 v192, v192, v198
	v_mul_f32_e32 v193, v193, v199
	v_mul_f32_e32 v194, v194, v200
	v_mul_f32_e32 v195, v195, v201
	v_fma_f32 v13, v192, v192, v13
	v_fma_f32 v13, v193, v193, v13
	v_fma_f32 v13, v194, v194, v13
	v_fma_f32 v13, v195, v195, v13
	v_mul_f32_e32 v192, 0x41800000, v192
	v_mul_f32_e32 v193, 0x41800000, v193
	v_mul_f32_e32 v194, 0x41800000, v194
	v_mul_f32_e32 v195, 0x41800000, v195
	v_cvt_pk_f16_f32 v196, v192, v193
	v_cvt_pk_f16_f32 v197, v194, v195
	ds_write_b64 v30, v[196:197] offset:32768
	v_cvt_f32_f16_e32 v198, v182
	v_cvt_f32_f16_sdwa v199, v182 dst_sel:DWORD dst_unused:UNUSED_PAD src0_sel:WORD_1
	v_cvt_f32_f16_e32 v200, v183
	v_cvt_f32_f16_sdwa v201, v183 dst_sel:DWORD dst_unused:UNUSED_PAD src0_sel:WORD_1
	v_fma_f32 v192, v190, v108, v124
	v_fma_f32 v193, v190, v109, v125
	v_fma_f32 v194, v190, v110, v126
	v_fma_f32 v195, v190, v111, v127
	v_mul_f32_e32 v192, s47, v192
	v_mul_f32_e32 v193, s47, v193
	v_mul_f32_e32 v194, s47, v194
	v_mul_f32_e32 v195, s47, v195
	v_fma_f32 v192, s46, v140, v192
	v_fma_f32 v193, s46, v141, v193
	v_fma_f32 v194, s46, v142, v194
	v_fma_f32 v195, s46, v143, v195
	v_mul_f32_e32 v192, v192, v198
	v_mul_f32_e32 v193, v193, v199
	v_mul_f32_e32 v194, v194, v200
	v_mul_f32_e32 v195, v195, v201
	v_fma_f32 v13, v192, v192, v13
	v_fma_f32 v13, v193, v193, v13
	v_fma_f32 v13, v194, v194, v13
	v_fma_f32 v13, v195, v195, v13
	v_mul_f32_e32 v192, 0x41800000, v192
	v_mul_f32_e32 v193, 0x41800000, v193
	v_mul_f32_e32 v194, 0x41800000, v194
	v_mul_f32_e32 v195, 0x41800000, v195
	v_cvt_pk_f16_f32 v196, v192, v193
	v_cvt_pk_f16_f32 v197, v194, v195
	ds_write_b64 v31, v[196:197] offset:32768
	s_waitcnt lgkmcnt(0)
	s_barrier
	ds_read_b128 v[204:207], v32 offset:32768
	ds_read_b128 v[208:211], v33 offset:32768
	s_waitcnt lgkmcnt(0)
	global_store_dwordx4 v8, v[204:207], s[38:39]
	global_store_dwordx4 v9, v[208:211], s[38:39]
	s_add_u32 s38, s38, 0x80
	s_addc_u32 s39, s39, 0
	v_mbcnt_lo_u32_b32 v188, -1, 0
	v_mbcnt_hi_u32_b32 v188, -1, v188
	v_xor_b32_e32 v189, 16, v188
	v_lshlrev_b32_e32 v189, 2, v189
	ds_bpermute_b32 v190, v189, v13
	s_waitcnt lgkmcnt(0)
	v_add_f32_e32 v13, v13, v190
	v_xor_b32_e32 v189, 32, v188
	v_lshlrev_b32_e32 v189, 2, v189
	ds_bpermute_b32 v190, v189, v13
	s_waitcnt lgkmcnt(0)
	v_add_f32_e32 v13, v13, v190
	v_cmp_gt_u32_e32 vcc, 16, v188
	s_and_saveexec_b64 s[48:49], vcc
	s_cbranch_execz .Lmy_s2_noat73
	global_atomic_add_f32 v15, v13, s[24:25]

	.amdhsa_kernel _Z12scan2_kernelPKDF16_S0_S0_S0_S0_PKfS2_S2_S2_PDF16_PfS4_
		.amdhsa_group_segment_fixed_size 34816
		.amdhsa_private_segment_fixed_size 0
		.amdhsa_kernarg_size 96
		.amdhsa_user_sgpr_count 2
		.amdhsa_user_sgpr_dispatch_ptr 0
		.amdhsa_user_sgpr_queue_ptr 0
		.amdhsa_user_sgpr_kernarg_segment_ptr 1
		.amdhsa_user_sgpr_dispatch_id 0
		.amdhsa_user_sgpr_kernarg_preload_length 0
		.amdhsa_user_sgpr_kernarg_preload_offset 0
		.amdhsa_user_sgpr_private_segment_size 0
		.amdhsa_uses_dynamic_stack 0
		.amdhsa_enable_private_segment 0
		.amdhsa_system_sgpr_workgroup_id_x 1
		.amdhsa_system_sgpr_workgroup_id_y 0
		.amdhsa_system_sgpr_workgroup_id_z 0
		.amdhsa_system_sgpr_workgroup_info 0
		.amdhsa_system_vgpr_workitem_id 0
		.amdhsa_next_free_vgpr 222
		.amdhsa_next_free_sgpr 68
		.amdhsa_accum_offset 224
		.amdhsa_reserve_vcc 1
		.amdhsa_float_round_mode_32 0
		.amdhsa_float_round_mode_16_64 0
		.amdhsa_float_denorm_mode_32 3
		.amdhsa_float_denorm_mode_16_64 3
		.amdhsa_dx10_clamp 1
		.amdhsa_ieee_mode 1
		.amdhsa_fp16_overflow 0
		.amdhsa_tg_split 0
		.amdhsa_exception_fp_ieee_invalid_op 0
		.amdhsa_exception_fp_denorm_src 0
		.amdhsa_exception_fp_ieee_div_zero 0
		.amdhsa_exception_fp_ieee_overflow 0
		.amdhsa_exception_fp_ieee_underflow 0
		.amdhsa_exception_fp_ieee_inexact 0
		.amdhsa_exception_int_div_zero 0
	.end_amdhsa_kernel

amdhsa.kernels:
  - .agpr_count:     0
    .args:
      - .actual_access:  read_only
        .address_space:  global
        .offset:         0
        .size:           8
        .value_kind:     global_buffer
      - .actual_access:  read_only
        .address_space:  global
        .offset:         8
        .size:           8
        .value_kind:     global_buffer
      - .actual_access:  read_only
        .address_space:  global
        .offset:         16
        .size:           8
        .value_kind:     global_buffer
      - .actual_access:  read_only
        .address_space:  global
        .offset:         24
        .size:           8
        .value_kind:     global_buffer
      - .actual_access:  write_only
        .address_space:  global
        .offset:         32
        .size:           8
        .value_kind:     global_buffer
      - .actual_access:  write_only
        .address_space:  global
        .offset:         40
        .size:           8
        .value_kind:     global_buffer
      - .actual_access:  write_only
        .address_space:  global
        .offset:         48
        .size:           8
        .value_kind:     global_buffer
      - .actual_access:  write_only
        .address_space:  global
        .offset:         56
        .size:           8
        .value_kind:     global_buffer
    .group_segment_fixed_size: 16640
    .kernarg_segment_align: 8
    .kernarg_segment_size: 64
    .language:       OpenCL C
    .language_version:
      - 2
      - 0
    .max_flat_workgroup_size: 256
    .name:           _Z11prep_kernelPKfS0_S0_S0_PDF16_S1_S1_Pf
    .private_segment_fixed_size: 0
    .sgpr_count:     18
    .sgpr_spill_count: 0
    .symbol:         _Z11prep_kernelPKfS0_S0_S0_PDF16_S1_S1_Pf.kd
    .uniform_work_group_size: 1
    .uses_dynamic_stack: false
    .vgpr_count:     42
    .vgpr_spill_count: 0
    .wavefront_size: 64
  - .agpr_count:     0
    .args:
      - .address_space:  global
        .offset:         0
        .size:           8
        .value_kind:     global_buffer
      - .address_space:  global
        .offset:         8
        .size:           8
        .value_kind:     global_buffer
      - .actual_access:  write_only
        .address_space:  global
        .offset:         16
        .size:           8
        .value_kind:     global_buffer
      - .actual_access:  read_only
        .address_space:  global
        .offset:         24
        .size:           8
        .value_kind:     global_buffer
    .group_segment_fixed_size: 49152
    .kernarg_segment_align: 8
    .kernarg_segment_size: 32
    .language:       OpenCL C
    .language_version:
      - 2
      - 0
    .max_flat_workgroup_size: 512
    .name:           _Z13gemm2b_kernelPKDF16_S0_PfPKf
    .private_segment_fixed_size: 0
    .sgpr_count:     24
    .sgpr_spill_count: 0
    .symbol:         _Z13gemm2b_kernelPKDF16_S0_PfPKf.kd
    .uniform_work_group_size: 1
    .uses_dynamic_stack: false
    .vgpr_count:     176
    .vgpr_spill_count: 0
    .wavefront_size: 64
  - .agpr_count:     0
    .args:
      - .address_space:  global
        .offset:         0
        .size:           8
        .value_kind:     global_buffer
      - .address_space:  global
        .offset:         8
        .size:           8
        .value_kind:     global_buffer
      - .actual_access:  write_only
        .address_space:  global
        .offset:         16
        .size:           8
        .value_kind:     global_buffer
      - .actual_access:  write_only
        .address_space:  global
        .offset:         24
        .size:           8
        .value_kind:     global_buffer
    .group_segment_fixed_size: 16384
    .kernarg_segment_align: 8
    .kernarg_segment_size: 32
    .language:       OpenCL C
    .language_version:
      - 2
      - 0
    .max_flat_workgroup_size: 512
    .name:           _Z12gemm8_kernelPKDF16_S0_PDF16_S1_
    .private_segment_fixed_size: 0
    .sgpr_count:     58
    .sgpr_spill_count: 0
    .symbol:         _Z12gemm8_kernelPKDF16_S0_PDF16_S1_.kd
    .uniform_work_group_size: 1
    .uses_dynamic_stack: false
    .vgpr_count:     184
    .vgpr_spill_count: 0
    .wavefront_size: 64
  - .agpr_count:     0
    .args:
      - .actual_access:  read_only
        .address_space:  global
        .offset:         0
        .size:           8
        .value_kind:     global_buffer
      - .actual_access:  read_only
        .address_space:  global
        .offset:         8
        .size:           8
        .value_kind:     global_buffer
      - .actual_access:  read_only
        .address_space:  global
        .offset:         16
        .size:           8
        .value_kind:     global_buffer
      - .actual_access:  read_only
        .address_space:  global
        .offset:         24
        .size:           8
        .value_kind:     global_buffer
      - .actual_access:  write_only
        .address_space:  global
        .offset:         32
        .size:           8
        .value_kind:     global_buffer
      - .actual_access:  write_only
        .address_space:  global
        .offset:         40
        .size:           8
        .value_kind:     global_buffer
      - .actual_access:  read_only
        .address_space:  global
        .offset:         48
        .size:           8
        .value_kind:     global_buffer
      - .actual_access:  read_only
        .address_space:  global
        .offset:         56
        .size:           8
        .value_kind:     global_buffer
      - .actual_access:  read_only
        .address_space:  global
        .offset:         64
        .size:           8
        .value_kind:     global_buffer
      - .actual_access:  write_only
        .address_space:  global
        .offset:         72
        .size:           8
        .value_kind:     global_buffer
      - .actual_access:  write_only
        .address_space:  global
        .offset:         80
        .size:           8
        .value_kind:     global_buffer
      - .actual_access:  write_only
        .address_space:  global
        .offset:         88
        .size:           8
        .value_kind:     global_buffer
      - .actual_access:  write_only
        .address_space:  global
        .offset:         96
        .size:           8
        .value_kind:     global_buffer
    .group_segment_fixed_size: 17952
    .kernarg_segment_align: 8
    .kernarg_segment_size: 104
    .language:       OpenCL C
    .language_version:
      - 2
      - 0
    .max_flat_workgroup_size: 256
    .name:           _Z13convdt_kernelPKDF16_S0_PKfS2_PDF16_S3_S2_S2_S2_PfS4_S4_S4_
    .private_segment_fixed_size: 0
    .sgpr_count:     26
    .sgpr_spill_count: 0
    .symbol:         _Z13convdt_kernelPKDF16_S0_PKfS2_PDF16_S3_S2_S2_S2_PfS4_S4_S4_.kd
    .uniform_work_group_size: 1
    .uses_dynamic_stack: false
    .vgpr_count:     88
    .vgpr_spill_count: 0
    .wavefront_size: 64
  - .agpr_count:     0
    .args:
      - .actual_access:  read_only
        .address_space:  global
        .offset:         0
        .size:           8
        .value_kind:     global_buffer
      - .actual_access:  read_only
        .address_space:  global
        .offset:         8
        .size:           8
        .value_kind:     global_buffer
      - .actual_access:  read_only
        .address_space:  global
        .offset:         16
        .size:           8
        .value_kind:     global_buffer
      - .actual_access:  write_only
        .address_space:  global
        .offset:         24
        .size:           8
        .value_kind:     global_buffer
    .group_segment_fixed_size: 34816
    .kernarg_segment_align: 8
    .kernarg_segment_size: 32
    .language:       OpenCL C
    .language_version:
      - 2
      - 0
    .max_flat_workgroup_size: 256
    .name:           _Z11sloc_kernelPKDF16_PKfS2_PDF16_
    .private_segment_fixed_size: 0
    .sgpr_count:     28
    .sgpr_spill_count: 0
    .symbol:         _Z11sloc_kernelPKDF16_PKfS2_PDF16_.kd
    .uniform_work_group_size: 1
    .uses_dynamic_stack: false
    .vgpr_count:     120
    .vgpr_spill_count: 0
    .wavefront_size: 64
  - .agpr_count:     64
    .args:
      - .actual_access:  read_only
        .address_space:  global
        .offset:         0
        .size:           8
        .value_kind:     global_buffer
      - .address_space:  global
        .offset:         8
        .size:           8
        .value_kind:     global_buffer
      - .actual_access:  read_only
        .address_space:  global
        .offset:         16
        .size:           8
        .value_kind:     global_buffer
      - .actual_access:  write_only
        .address_space:  global
        .offset:         24
        .size:           8
        .value_kind:     global_buffer
    .group_segment_fixed_size: 0
    .kernarg_segment_align: 8
    .kernarg_segment_size: 32
    .language:       OpenCL C
    .language_version:
      - 2
      - 0
    .max_flat_workgroup_size: 256
    .name:           _Z12spass_kernelPKfPDF16_PKDF16_S1_
    .private_segment_fixed_size: 0
    .sgpr_count:     21
    .sgpr_spill_count: 0
    .symbol:         _Z12spass_kernelPKfPDF16_PKDF16_S1_.kd
    .uniform_work_group_size: 1
    .uses_dynamic_stack: false
    .vgpr_count:     180
    .vgpr_spill_count: 0
    .wavefront_size: 64
  - .agpr_count:     0
    .args:
      - .actual_access:  read_only
        .address_space:  global
        .offset:         0
        .size:           8
        .value_kind:     global_buffer
      - .actual_access:  read_only
        .address_space:  global
        .offset:         8
        .size:           8
        .value_kind:     global_buffer
      - .actual_access:  read_only
        .address_space:  global
        .offset:         16
        .size:           8
        .value_kind:     global_buffer
      - .actual_access:  read_only
        .address_space:  global
        .offset:         24
        .size:           8
        .value_kind:     global_buffer
      - .actual_access:  read_only
        .address_space:  global
        .offset:         32
        .size:           8
        .value_kind:     global_buffer
      - .actual_access:  read_only
        .address_space:  global
        .offset:         40
        .size:           8
        .value_kind:     global_buffer
      - .actual_access:  read_only
        .address_space:  global
        .offset:         48
        .size:           8
        .value_kind:     global_buffer
      - .actual_access:  read_only
        .address_space:  global
        .offset:         56
        .size:           8
        .value_kind:     global_buffer
      - .actual_access:  read_only
        .address_space:  global
        .offset:         64
        .size:           8
        .value_kind:     global_buffer
      - .actual_access:  write_only
        .address_space:  global
        .offset:         72
        .size:           8
        .value_kind:     global_buffer
      - .address_space:  global
        .offset:         80
        .size:           8
        .value_kind:     global_buffer
      - .actual_access:  read_only
        .address_space:  global
        .offset:         88
        .size:           8
        .value_kind:     global_buffer
    .group_segment_fixed_size: 54272
    .kernarg_segment_align: 8
    .kernarg_segment_size: 96
    .language:       OpenCL C
    .language_version:
      - 2
      - 0
    .max_flat_workgroup_size: 256
    .name:           _Z11scan_kernelPKDF16_S0_S0_S0_S0_PKfS2_S2_S2_PDF16_PfS4_
    .private_segment_fixed_size: 0
    .sgpr_count:     106
    .sgpr_spill_count: 56
    .symbol:         _Z11scan_kernelPKDF16_S0_S0_S0_S0_PKfS2_S2_S2_PDF16_PfS4_.kd
    .uniform_work_group_size: 1
    .uses_dynamic_stack: false
    .vgpr_count:     243
    .vgpr_spill_count: 0
    .wavefront_size: 64
  - .agpr_count:     0
    .args:
      - .actual_access:  read_only
        .address_space:  global
        .offset:         0
        .size:           8
        .value_kind:     global_buffer
      - .address_space:  global
        .offset:         8
        .size:           8
        .value_kind:     global_buffer
      - .address_space:  global
        .offset:         16
        .size:           8
        .value_kind:     global_buffer
      - .actual_access:  read_only
        .address_space:  global
        .offset:         24
        .size:           8
        .value_kind:     global_buffer
      - .address_space:  global
        .offset:         32
        .size:           8
        .value_kind:     global_buffer
      - .address_space:  global
        .offset:         40
        .size:           8
        .value_kind:     global_buffer
      - .address_space:  global
        .offset:         48
        .size:           8
        .value_kind:     global_buffer
      - .actual_access:  read_only
        .address_space:  global
        .offset:         56
        .size:           8
        .value_kind:     global_buffer
      - .actual_access:  read_only
        .address_space:  global
        .offset:         64
        .size:           8
        .value_kind:     global_buffer
      - .actual_access:  write_only
        .address_space:  global
        .offset:         72
        .size:           8
        .value_kind:     global_buffer
      - .address_space:  global
        .offset:         80
        .size:           8
        .value_kind:     global_buffer
      - .actual_access:  read_only
        .address_space:  global
        .offset:         88
        .size:           8
        .value_kind:     global_buffer
    .group_segment_fixed_size: 34816
    .kernarg_segment_align: 8
    .kernarg_segment_size: 96
    .language:       OpenCL C
    .language_version:
      - 2
      - 0
    .max_flat_workgroup_size: 512
    .name:           _Z12scan2_kernelPKDF16_S0_S0_S0_S0_PKfS2_S2_S2_PDF16_PfS4_
    .private_segment_fixed_size: 0
    .sgpr_count:     74
    .sgpr_spill_count: 0
    .symbol:         _Z12scan2_kernelPKDF16_S0_S0_S0_S0_PKfS2_S2_S2_PDF16_PfS4_.kd
    .uniform_work_group_size: 1
    .uses_dynamic_stack: false
    .vgpr_count:     222
    .vgpr_spill_count: 0
    .wavefront_size: 64
  - .agpr_count:     64
    .args:
      - .address_space:  global
        .offset:         0
        .size:           8
        .value_kind:     global_buffer
      - .address_space:  global
        .offset:         8
        .size:           8
        .value_kind:     global_buffer
      - .offset:         16
        .size:           4
        .value_kind:     by_value
      - .offset:         20
        .size:           4
        .value_kind:     by_value
      - .offset:         24
        .size:           4
        .value_kind:     by_value
      - .actual_access:  write_only
        .address_space:  global
        .offset:         32
        .size:           8
        .value_kind:     global_buffer
      - .actual_access:  write_only
        .address_space:  global
        .offset:         40
        .size:           8
        .value_kind:     global_buffer
      - .actual_access:  read_only
        .address_space:  global
        .offset:         48
        .size:           8
        .value_kind:     global_buffer
      - .offset:         56
        .size:           4
        .value_kind:     by_value
    .group_segment_fixed_size: 131072
    .kernarg_segment_align: 8
    .kernarg_segment_size: 60
    .language:       OpenCL C
    .language_version:
      - 2
      - 0
    .max_flat_workgroup_size: 256
    .name:           _Z11gemm_kernelILi1EEvPKDF16_S1_iiiPDF16_PfPKfi
    .private_segment_fixed_size: 0
    .sgpr_count:     27
    .sgpr_spill_count: 0
    .symbol:         _Z11gemm_kernelILi1EEvPKDF16_S1_iiiPDF16_PfPKfi.kd
    .uniform_work_group_size: 1
    .uses_dynamic_stack: false
    .vgpr_count:     208
    .vgpr_spill_count: 0
    .wavefront_size: 64
